# v22 + workspace pointer (kernarg 0xf8) loaded once into s[100:101]; its 50 per-phase / per-barrier SMEM re-loads become s_mov_b64
# speedup vs baseline: 1.0070x; 1.0070x over previous
; #define LAS __attribute__((address_space(3)))
; __device__ __forceinline__ unsigned xb_add(unsigned* p, unsigned v) { return __hip_atomic_fetch_add(p, v, __ATOMIC_RELAXED, __HIP_MEMORY_SCOPE_AGENT); }
; __device__ __forceinline__ unsigned xb_xcc_id() { return (unsigned)__builtin_amdgcn_s_getreg((3 << 11) | 20) & 0xFu; }
; __device__ __forceinline__ KP kargs() { KP pp = (KP)__builtin_amdgcn_kernarg_segment_ptr(); asm volatile("" : "+s"(pp)); return pp; }
; #define KWS (kargs()->ws)
; #define REP(id) for (int rep_ = 0; rep_ < ((DUP_ID == (id)) ? DUP_N : 1); ++rep_)
; #define WAVE_IDS() const int tid = opaque_tid(wbase), lane = tid & 63, wid = __builtin_amdgcn_readfirstlane(tid >> 6), gw = c * 8 + wid, ngw = G * 8; (void)tid; (void)lane; (void)gw; (void)ngw
; __device__ __forceinline__ XcdBarrier xcd_barrier_post(unsigned* bar, volatile LAS unsigned* st) {
;     XcdBarrier b; b.bar = bar; b.x = xb_xcc_id(); b.st = st;
;     if (threadIdx.x == 0) (void)xb_add(&bar[XB_XCNT(b.x)], 1u);
;     return b;
; __global__ void __launch_bounds__(512, 2) mega(Ptrs Pdummy) {
;     extern __shared__ __attribute__((aligned(16))) unsigned char lds_raw[];
;     LAS unsigned char* lds = (LAS unsigned char*)lds_raw;
;     const int G = (int)gridDim.x, c = (int)blockIdx.x, wbase = __builtin_amdgcn_readfirstlane((int)threadIdx.x) & ~63;
;     { volatile LAS unsigned* MISC0 = (volatile LAS unsigned*)(lds + LDSCTL_OFF); if (threadIdx.x < 64) MISC0[threadIdx.x] = 0u; }
;     __syncthreads();
;     (void)xcd_barrier_post((unsigned*)(KWS + WS_CTL) + CW_BAR, (volatile LAS unsigned*)(lds + LDSCTL_OFF) + 8);
;     ...
;     REP(1) { WAVE_IDS(); const KP P = kargs(); unsigned char* ws = P->ws; LAS float* scr = (LAS float*)(lds + wid * 16384);
;       { constexpr int NJ = 30 + 128 + (INPROJ_GATES_FP8 ? DEPTH : 0); LAS int* pref = (LAS int*)(lds + 9216);
;         if (tid < NJ) { const CJob jb = static_job(P, tid); pref[512 + tid] = (jb.K / 64) * (jb.N / 32); }
_Z4mega4Ptrs:
	s_mov_b64 s[88:89], s[0:1]
	s_load_dword s60, s[0:1], 0x100
	s_load_dwordx2 s[100:101], s[0:1], 0xf8
	s_waitcnt lgkmcnt(0)
	s_add_u32 s0, s88, 0x100
	s_addc_u32 s1, s89, 0
	s_mov_b32 s92, s2
	v_writelane_b32 v255, s0, 0
	v_cmp_gt_u32_e32 vcc, 64, v0
	s_nop 0
	v_writelane_b32 v255, s1, 1
	v_readfirstlane_b32 s0, v0
	s_and_saveexec_b64 s[2:3], vcc
	v_lshl_add_u32 v1, v0, 2, 0
	v_add_u32_e32 v1, 0x20000, v1
	v_mov_b32_e32 v2, 0
	ds_write_b32 v1, v2
	s_or_b64 exec, exec, s[2:3]
	s_mov_b64 s[4:5], s[88:89]
	s_waitcnt lgkmcnt(0)
	s_barrier
	s_getreg_b32 s1, hwreg(HW_REG_XCC_ID, 0, 4)
	v_cmp_eq_u32_e32 vcc, 0, v0
	s_and_saveexec_b64 s[2:3], vcc
	s_cbranch_execz .LBB0_5
	s_mov_b64 s[6:7], exec
	v_mbcnt_lo_u32_b32 v0, s6, 0
	v_mbcnt_hi_u32_b32 v0, s7, v0
	v_cmp_eq_u32_e32 vcc, 0, v0
	s_and_b64 s[8:9], exec, vcc
	s_mov_b64 exec, s[8:9]
	s_cbranch_execz .LBB0_5
	s_mov_b64 s[4:5], s[100:101]
	s_lshl_b32 s1, s1, 8
	s_and_b32 s1, s1, 0xf00
	v_mov_b32_e32 v0, 0x4000
	s_waitcnt lgkmcnt(0)
	s_add_u32 s4, s4, s1
	s_addc_u32 s5, s5, 0
	s_bcnt1_i32_b64 s1, s[6:7]
	v_mov_b32_e32 v1, s1
	global_atomic_add v0, v1, s[4:5] offset:1024
.LBB0_5:
	s_or_b64 exec, exec, s[2:3]
	s_and_b32 s93, s0, 0xffffffc0
	s_mov_b32 s0, -1
	s_mov_b64 s[10:11], s[88:89]
	v_mbcnt_lo_u32_b32 v0, s0, 0
	v_mbcnt_hi_u32_b32 v0, s0, v0
	v_add_u32_e32 v73, s93, v0
	s_mov_b64 s[8:9], s[100:101]
	s_movk_i32 s1, 0x9e
	v_readfirstlane_b32 s0, v73
	v_cmp_gt_i32_e32 vcc, s1, v73
	s_and_saveexec_b64 s[2:3], vcc
	s_cbranch_execz .LBB0_19
	v_cmp_lt_i32_e32 vcc, 23, v73
	s_and_saveexec_b64 s[4:5], vcc
	s_xor_b64 s[4:5], exec, s[4:5]
	s_cbranch_execz .LBB0_10
	v_cmp_gt_u32_e32 vcc, 30, v73
	v_mov_b32_e32 v1, 1
	v_mov_b32_e32 v0, 2
	s_and_saveexec_b64 s[6:7], vcc
	v_subrev_u32_e32 v0, 24, v73
	v_subrev_u32_e32 v1, 27, v73
	v_cmp_gt_u32_e32 vcc, 3, v0
	s_nop 1
	v_cndmask_b32_e32 v0, v1, v0, vcc
	v_cmp_gt_u32_e32 vcc, 2, v0
	v_mov_b32_e32 v0, 0x70
	s_nop 0
	v_cndmask_b32_e64 v1, 56, 16, vcc
	v_cndmask_b32_e32 v0, 32, v0, vcc
	s_or_b64 exec, exec, s[6:7]

; __device__ __forceinline__ unsigned xb_ld(unsigned* p)              { return __hip_atomic_load(p, __ATOMIC_RELAXED, __HIP_MEMORY_SCOPE_AGENT); }
; __device__ __forceinline__ void xcd_barrier_complete(unsigned* bar, unsigned x, unsigned& nloc, unsigned& nx) {
;     const unsigned G = gridDim.x * gridDim.y * gridDim.z;
;     unsigned sum, cnt, mine, sp = 0u;
;     for (;;) {
;         sum = 0u; cnt = 0u; mine = 0u;
; #pragma unroll
;         for (unsigned j = 0; j < 16; ++j) { const unsigned c = xb_ld(&bar[XB_XCNT(j)]); sum += c; cnt += (c > 0u) ? 1u : 0u; mine = (j == x) ? c : mine; }
; __device__ __forceinline__ void xcd_barrier(const XcdBarrier& b, bool leader) {
;     asm volatile("s_waitcnt vmcnt(0)" ::: "memory");
;     __syncthreads();
;     if (leader) {
;         unsigned zo_; asm volatile("v_mov_b32 %0, 0" : "=v"(zo_)); unsigned* bar = b.bar + zo_;
;         __builtin_amdgcn_s_waitcnt(0);
;         unsigned nloc = b.st[0], nx = b.st[1];
;         if (nloc == 0u) { xcd_barrier_complete(bar, b.x, nloc, nx); b.st[0] = nloc; b.st[1] = nx; }
.Lbinv_skip_0:
	s_and_saveexec_b64 s[4:5], vcc
	v_writelane_b32 v255, s94, 29
	s_xor_b64 s[10:11], exec, s[4:5]
	s_nop 0
	v_writelane_b32 v255, s95, 30
	s_cbranch_execz .LBB0_241
	s_add_i32 s1, 0, 0x20020
	v_mov_b32_e32 v2, s1
	s_mov_b64 s[2:3], s[100:101]
	v_mov_b32 v0, 0
	s_waitcnt vmcnt(0) expcnt(0) lgkmcnt(0)
	ds_read_b32 v6, v2
	s_add_i32 s1, 0, 0x20024
	v_mov_b32_e32 v2, s1
	ds_read_b32 v4, v2
	v_mov_b32_e32 v1, 0
	v_lshl_add_u64 v[0:1], v[0:1], 2, s[2:3]
	s_mov_b64 s[2:3], 0x4000
	s_waitcnt lgkmcnt(1)
	v_cmp_ne_u32_e32 vcc, 0, v6
	s_and_b32 s0, s0, 15
	v_lshl_add_u64 v[0:1], v[0:1], 0, s[2:3]
	s_cbranch_vccnz .LBB0_211
	v_readlane_b32 s4, v255, 0
	v_readlane_b32 s5, v255, 1
	s_load_dwordx2 s[2:3], s[4:5], 0x4
	s_mov_b64 s[4:5], 0x1000
	v_lshl_add_u64 v[2:3], v[0:1], 0, s[4:5]
	s_mov_b32 s22, 1
	s_waitcnt lgkmcnt(0)
	s_mul_i32 s1, s2, s60
	s_mul_i32 s1, s1, s3
	s_mov_b64 s[2:3], 0x1100
	v_lshl_add_u64 v[4:5], v[0:1], 0, s[2:3]
	s_mov_b64 s[2:3], 0x1200
	v_lshl_add_u64 v[6:7], v[0:1], 0, s[2:3]
	s_mov_b64 s[2:3], 0x1300
	v_lshl_add_u64 v[8:9], v[0:1], 0, s[2:3]
	s_mov_b64 s[2:3], 0
	s_branch .LBB0_201

; __device__ __forceinline__ int opaque_s(int x) { asm volatile("" : "+s"(x)); return x; }
; template <class Epi, class Sched, bool ALIGN_EPI = false, bool SP2 = false, bool FP8 = false>
; __device__ __forceinline__ void gemm_phase(LAS unsigned char* lds, const Gemm g, const Sched& S, const Epi& E, int wbase) {
;     const int tid = opaque_tid(wbase), wid = __builtin_amdgcn_readfirstlane(tid >> 6), lane = tid & 63, wr = wid >> 2, wc = wid & 3, fr = lane & 15, fq = lane >> 4;
;     const int K = opaque_s(g.K), nt = K / BK;
;     unsigned voffA[2], voffB[2];
; #pragma unroll
;     for (int i = 0; i < 2; ++i) { int R, C; stage_rc(tid * 16 + i * 8192, R, C); const int Rb = Epi::PERM ? ((R & ~31) + perm32(R & 31)) : R;
;         voffA[i] = (unsigned)(R * K + C) * 2u; voffB[i] = (unsigned)(Rb * K + C) * 2u; }
;     const unsigned kstep = (unsigned)(BK * 2);
;     const unsigned hstep = (unsigned)HALF * (unsigned)K * 2u;
;     typedef __amdgpu_buffer_rsrc_t rsrc_t;
;     const rsrc_t rA0 = __builtin_amdgcn_make_buffer_rsrc((void*)g.A, 0, 0xffffffff, 0x00020000), rB0 = __builtin_amdgcn_make_buffer_rsrc((void*)g.Bt, 0, 0xffffffff, 0x00020000);
;     rsrc_t rA1 = rA0, rB1 = rB0;
;     if constexpr (Sched::TWO) { rA1 = __builtin_amdgcn_make_buffer_rsrc((void*)S.A1, 0, 0xffffffff, 0x00020000); rB1 = __builtin_amdgcn_make_buffer_rsrc((void*)S.Bt1, 0, 0xffffffff, 0x00020000); }
;     const unsigned ldsw = (unsigned)wid * 1024u;
;     const int aoff = lds_byte(wr * 64 + fr, fq * 8), boff = lds_byte(wc * 32 + fr, fq * 8);
;     ...
;     Unit cur, nxt; int ui = 0;
;     if (!S.next(0, cur)) return;
;     f32x4 acc[2][2][4][2];
;     ...
;     PG8_ZERO_ACC();
;     v8i_t At[4], B0[2], B1[2];
;     unsigned cA = S.a_off(cur, g), cB = S.b_off(cur, g); rsrc_t rAc = (Sched::TWO && cur.part) ? rA1 : rA0, rBc = (Sched::TWO && cur.part) ? rB1 : rB0;
;     S.a_ready(cur);
;     if constexpr (SP2) {
;         PG8_STAGE(PG8_SB(0, 0), rBc, cB, voffB); PG8_STAGE(PG8_SB(0, 1), rBc, cB + hstep, voffB); PG8_STAGE(PG8_SA(0, 0), rAc, cA, voffA); PG8_STAGE(PG8_SA(0, 1), rAc, cA + hstep, voffA);
;         if (wr == 1) PG8_BAR;
; __global__ void __launch_bounds__(512, 2) mega(Ptrs Pdummy) {
;     ...
;           REP(2) { unsigned char* ws = KWS; pg8::Gemm g{(const bf16*)(ws + WS_HB8), (const bf16*)(ws + WS_WIN + (size_t)l * NIN * DM * 2), DM / 2, 0}; pg8::StaticOrder S; S.init(M, NIN, opaque_s(G), opaque_s(c));
.LBB0_248:
	s_andn2_b64 vcc, exec, s[8:9]
	s_cbranch_vccnz .LBB0_338
	v_bfe_i32 v2, v4, 27, 1
	v_lshlrev_b32_e32 v0, 4, v4
	v_lshrrev_b32_e32 v2, 22, v2
	v_add_u32_e32 v2, v0, v2
	v_and_b32_e32 v2, 0xfffffc00, v2
	v_sub_u32_e32 v2, v0, v2
	v_lshrrev_b32_e32 v3, 4, v2
	v_ashrrev_i32_e32 v1, 31, v4
	v_bitop3_b32 v3, v3, v2, 32 bitop3:0x6c
	v_ashrrev_i32_e32 v2, 31, v2
	v_lshrrev_b32_e32 v1, 26, v1
	v_lshrrev_b32_e32 v2, 26, v2
	v_add_u32_e32 v1, v4, v1
	v_add_u32_e32 v2, v3, v2
	v_ashrrev_i32_e32 v1, 6, v1
	v_ashrrev_i32_e32 v2, 6, v2
	v_lshlrev_b32_e32 v5, 3, v1
	v_mul_i32_i24_e32 v6, 64, v2
	v_and_b32_e32 v5, -16, v5
	v_lshlrev_b32_e32 v1, 5, v1
	v_sub_u32_e32 v3, v3, v6
	v_add_u32_e32 v5, v2, v5
	v_and_b32_e32 v1, 32, v1
	v_ashrrev_i16_sdwa v3, v231, sext(v3) dst_sel:DWORD dst_unused:UNUSED_PAD src0_sel:DWORD src1_sel:BYTE_0
	s_mov_b64 s[2:3], s[100:101]
	s_nop 0
	s_load_dwordx2 s[8:9], s[4:5], 0x20
	s_load_dwordx2 s[10:11], s[6:7], 0x28
	v_add_u32_sdwa v1, v1, sext(v3) dst_sel:DWORD dst_unused:UNUSED_PAD src0_sel:DWORD src1_sel:WORD_0
	v_lshlrev_b32_e32 v3, 1, v5
	v_lshrrev_b32_e32 v6, 2, v5
	v_and_b32_e32 v2, 3, v2
	s_mov_b32 s7, 0x7fffffe0
	v_and_b32_e32 v3, 24, v3
	v_and_b32_e32 v6, 4, v6
	v_and_or_b32 v2, v5, s7, v2
	v_or3_b32 v2, v2, v6, v3
	v_mul_lo_u32 v3, v5, s16
	v_mul_lo_u32 v2, v2, s16
	v_add_u32_e32 v0, 0x2000, v0
	v_add_lshl_u32 v192, v1, v3, 1
	v_add_lshl_u32 v222, v2, v1, 1
	v_ashrrev_i32_e32 v1, 31, v0
	v_lshrrev_b32_e32 v1, 22, v1
	v_add_u32_e32 v1, v0, v1
	v_ashrrev_i32_e32 v1, 10, v1
	v_mul_i32_i24_e32 v2, 0x400, v1
	v_sub_u32_e32 v0, v0, v2
	v_lshrrev_b32_e32 v2, 4, v0
	v_bitop3_b32 v0, v2, v0, 32 bitop3:0x6c
	s_waitcnt lgkmcnt(0)
	s_add_u32 s36, s2, 0xb200000
	v_ashrrev_i32_e32 v3, 31, v0
	s_mul_i32 s4, s95, 0xb00000
	s_addc_u32 s5, s3, 0
	v_lshrrev_b32_e32 v3, 26, v3
	s_add_u32 s4, s2, s4
	v_add_u32_e32 v3, v0, v3
	s_addc_u32 s6, s3, 0
	v_lshlrev_b32_e32 v2, 3, v1
	v_ashrrev_i32_e32 v5, 6, v3
	v_and_b32_e32 v3, 0xc0, v3
	s_add_u32 s4, s4, 0x100000
	v_and_b32_e32 v2, -16, v2
	v_lshlrev_b32_e32 v1, 5, v1
	v_sub_u32_e32 v0, v0, v3
	s_addc_u32 s6, s6, 0
	s_ashr_i32 s18, s1, 6
	v_add_u32_e32 v2, v5, v2
	v_and_b32_e32 v1, 32, v1
	v_ashrrev_i16_sdwa v0, v231, sext(v0) dst_sel:DWORD dst_unused:UNUSED_PAD src0_sel:DWORD src1_sel:BYTE_0
	v_add_u32_sdwa v0, v1, sext(v0) dst_sel:DWORD dst_unused:UNUSED_PAD src0_sel:DWORD src1_sel:WORD_0
	v_lshlrev_b32_e32 v1, 1, v2
	v_lshrrev_b32_e32 v3, 2, v2
	v_and_b32_e32 v5, 3, v5
	s_lshl_b32 s12, s18, 10
	v_and_b32_e32 v1, 24, v1
	v_and_b32_e32 v3, 4, v3
	v_and_or_b32 v5, v2, s7, v5
	s_add_i32 s42, s12, 0
	v_or3_b32 v1, v5, v3, v1
	s_add_i32 s43, s42, 0x10000
	v_mul_lo_u32 v2, v2, s16
	v_mul_lo_u32 v1, v1, s16
	s_and_b32 s37, s5, 0xffff
	s_and_b32 s5, s6, 0xffff
	s_mov_b32 s6, s38
	s_mov_b32 s7, s39
	s_lshl_b32 s28, s17, 18
	s_mov_b32 m0, s43
	s_add_i32 s44, s42, 0x12000
	v_add_lshl_u32 v223, v0, v2, 1
	v_add_lshl_u32 v193, v1, v0, 1
	s_lshl_b32 s41, s16, 8
	v_mov_b32 v0, 0
	buffer_load_dwordx4 v222, s[4:7], s28 offen lds
	s_mov_b32 m0, s44
	s_add_i32 s45, s42, 0x14000
	buffer_load_dwordx4 v193, s[4:7], s28 offen lds
	s_add_i32 s20, s28, s41
	s_mov_b32 m0, s45
	s_add_i32 s52, s42, 0x16000
	buffer_load_dwordx4 v222, s[4:7], s20 offen lds
	s_mov_b32 m0, s52
	s_lshl_b32 s29, s25, 18
	buffer_load_dwordx4 v193, s[4:7], s20 offen lds
	s_mov_b32 m0, s42
	s_add_i32 s53, s42, 0x2000
	buffer_load_dwordx4 v192, s[36:39], s29 offen lds
	s_mov_b32 m0, s53
	s_add_i32 s56, s42, 0x4000
	buffer_load_dwordx4 v223, s[36:39], s29 offen lds
	s_add_i32 s6, s29, s41
	s_mov_b32 m0, s56
	s_add_i32 s57, s42, 0x6000
	buffer_load_dwordx4 v192, s[36:39], s6 offen lds
	s_mov_b32 m0, s57
	s_ashr_i32 s19, s1, 8
	buffer_load_dwordx4 v223, s[36:39], s6 offen lds
	s_cmp_eq_u32 s19, 1
	s_cselect_b64 s[60:61], -1, 0
	s_cmp_lg_u32 s19, 1
	s_cbranch_scc1 .LBB0_251
	s_barrier

; __device__ __forceinline__ int opaque_s(int x) { asm volatile("" : "+s"(x)); return x; }
; template <class Epi, class Sched, bool ALIGN_EPI = false, bool SP2 = false, bool FP8 = false>
; __device__ __forceinline__ void gemm_phase(LAS unsigned char* lds, const Gemm g, const Sched& S, const Epi& E, int wbase) {
;     const int tid = opaque_tid(wbase), wid = __builtin_amdgcn_readfirstlane(tid >> 6), lane = tid & 63, wr = wid >> 2, wc = wid & 3, fr = lane & 15, fq = lane >> 4;
;     const int K = opaque_s(g.K), nt = K / BK;
;     unsigned voffA[2], voffB[2];
; #pragma unroll
;     for (int i = 0; i < 2; ++i) { int R, C; stage_rc(tid * 16 + i * 8192, R, C); const int Rb = Epi::PERM ? ((R & ~31) + perm32(R & 31)) : R;
;         voffA[i] = (unsigned)(R * K + C) * 2u; voffB[i] = (unsigned)(Rb * K + C) * 2u; }
;     const unsigned kstep = (unsigned)(BK * 2);
;     const unsigned hstep = (unsigned)HALF * (unsigned)K * 2u;
;     typedef __amdgpu_buffer_rsrc_t rsrc_t;
;     const rsrc_t rA0 = __builtin_amdgcn_make_buffer_rsrc((void*)g.A, 0, 0xffffffff, 0x00020000), rB0 = __builtin_amdgcn_make_buffer_rsrc((void*)g.Bt, 0, 0xffffffff, 0x00020000);
;     rsrc_t rA1 = rA0, rB1 = rB0;
;     if constexpr (Sched::TWO) { rA1 = __builtin_amdgcn_make_buffer_rsrc((void*)S.A1, 0, 0xffffffff, 0x00020000); rB1 = __builtin_amdgcn_make_buffer_rsrc((void*)S.Bt1, 0, 0xffffffff, 0x00020000); }
;     const unsigned ldsw = (unsigned)wid * 1024u;
;     const int aoff = lds_byte(wr * 64 + fr, fq * 8), boff = lds_byte(wc * 32 + fr, fq * 8);
;     ...
;     Unit cur, nxt; int ui = 0;
;     if (!S.next(0, cur)) return;
;     f32x4 acc[2][2][4][2];
;     ...
;     PG8_ZERO_ACC();
;     v8i_t At[4], B0[2], B1[2];
;     unsigned cA = S.a_off(cur, g), cB = S.b_off(cur, g); rsrc_t rAc = (Sched::TWO && cur.part) ? rA1 : rA0, rBc = (Sched::TWO && cur.part) ? rB1 : rB0;
;     S.a_ready(cur);
;     if constexpr (SP2) {
;         PG8_STAGE(PG8_SB(0, 0), rBc, cB, voffB); PG8_STAGE(PG8_SB(0, 1), rBc, cB + hstep, voffB); PG8_STAGE(PG8_SA(0, 0), rAc, cA, voffA); PG8_STAGE(PG8_SA(0, 1), rAc, cA + hstep, voffA);
;         if (wr == 1) PG8_BAR;
; __global__ void __launch_bounds__(512, 2) mega(Ptrs Pdummy) {
;     ...
;         REP(2) { unsigned char* ws = KWS; pg8::Gemm g{HBUF(hc), (const bf16*)(ws + WS_WIN + (size_t)l * NIN * DM * 2), DM, 0}; pg8::StaticOrder S; S.init(M, INPROJ_GATES_FP8 ? NIN_A : NIN, opaque_s(G), opaque_s(c));
.LBB0_342:
	s_andn2_b64 vcc, exec, s[8:9]
	s_cbranch_vccnz .LBB0_432
	v_bfe_i32 v2, v4, 27, 1
	v_lshlrev_b32_e32 v0, 4, v4
	v_lshrrev_b32_e32 v2, 22, v2
	v_add_u32_e32 v2, v0, v2
	v_and_b32_e32 v2, 0xfffffc00, v2
	v_sub_u32_e32 v2, v0, v2
	v_lshrrev_b32_e32 v3, 4, v2
	v_ashrrev_i32_e32 v1, 31, v4
	v_bitop3_b32 v3, v3, v2, 32 bitop3:0x6c
	v_ashrrev_i32_e32 v2, 31, v2
	v_lshrrev_b32_e32 v1, 26, v1
	v_lshrrev_b32_e32 v2, 26, v2
	v_add_u32_e32 v1, v4, v1
	v_add_u32_e32 v2, v3, v2
	v_ashrrev_i32_e32 v1, 6, v1
	v_ashrrev_i32_e32 v2, 6, v2
	v_lshlrev_b32_e32 v5, 3, v1
	v_mul_i32_i24_e32 v6, 64, v2
	v_and_b32_e32 v5, -16, v5
	v_lshlrev_b32_e32 v1, 5, v1
	v_sub_u32_e32 v3, v3, v6
	v_add_u32_e32 v5, v2, v5
	v_and_b32_e32 v1, 32, v1
	v_ashrrev_i16_sdwa v3, v231, sext(v3) dst_sel:DWORD dst_unused:UNUSED_PAD src0_sel:DWORD src1_sel:BYTE_0
	s_mov_b64 s[2:3], s[100:101]
	s_nop 0
	s_load_dwordx2 s[8:9], s[4:5], 0x20
	s_load_dwordx2 s[10:11], s[6:7], 0x28
	v_add_u32_sdwa v1, v1, sext(v3) dst_sel:DWORD dst_unused:UNUSED_PAD src0_sel:DWORD src1_sel:WORD_0
	v_lshlrev_b32_e32 v3, 1, v5
	v_lshrrev_b32_e32 v6, 2, v5
	v_and_b32_e32 v2, 3, v2
	s_mov_b32 s6, 0x7fffffe0
	v_and_b32_e32 v3, 24, v3
	v_and_b32_e32 v6, 4, v6
	v_and_or_b32 v2, v5, s6, v2
	v_or3_b32 v2, v2, v6, v3
	v_mul_lo_u32 v3, v5, s12
	v_mul_lo_u32 v2, v2, s12
	v_add_u32_e32 v0, 0x2000, v0
	v_add_lshl_u32 v164, v1, v3, 1
	v_add_lshl_u32 v165, v2, v1, 1
	v_ashrrev_i32_e32 v1, 31, v0
	v_lshrrev_b32_e32 v1, 22, v1
	v_add_u32_e32 v1, v0, v1
	v_ashrrev_i32_e32 v1, 10, v1
	v_mul_i32_i24_e32 v2, 0x400, v1
	v_readlane_b32 s1, v255, 10
	v_sub_u32_e32 v0, v0, v2
	s_cmp_eq_u32 s1, 0
	s_mov_b32 s1, 0x13200000
	v_lshrrev_b32_e32 v2, 4, v0
	s_cselect_b32 s1, s1, 0x1b800000
	v_bitop3_b32 v0, v2, v0, 32 bitop3:0x6c
	s_waitcnt lgkmcnt(0)
	s_add_u32 s36, s2, s1
	v_ashrrev_i32_e32 v3, 31, v0
	s_mul_i32 s4, s95, 0xb00000
	s_addc_u32 s1, s3, 0
	v_lshrrev_b32_e32 v3, 26, v3
	s_add_u32 s4, s2, s4
	v_add_u32_e32 v3, v0, v3
	s_addc_u32 s5, s3, 0
	v_lshlrev_b32_e32 v2, 3, v1
	v_ashrrev_i32_e32 v5, 6, v3
	v_and_b32_e32 v3, 0xc0, v3
	s_add_u32 s4, s4, 0x100000
	v_and_b32_e32 v2, -16, v2
	v_lshlrev_b32_e32 v1, 5, v1
	v_sub_u32_e32 v0, v0, v3
	s_addc_u32 s5, s5, 0
	s_ashr_i32 s13, s16, 6
	v_add_u32_e32 v2, v5, v2
	v_and_b32_e32 v1, 32, v1
	v_ashrrev_i16_sdwa v0, v231, sext(v0) dst_sel:DWORD dst_unused:UNUSED_PAD src0_sel:DWORD src1_sel:BYTE_0
	v_add_u32_sdwa v0, v1, sext(v0) dst_sel:DWORD dst_unused:UNUSED_PAD src0_sel:DWORD src1_sel:WORD_0
	v_lshlrev_b32_e32 v1, 1, v2
	v_lshrrev_b32_e32 v3, 2, v2
	v_and_b32_e32 v5, 3, v5
	s_and_b32 s37, s1, 0xffff
	s_lshl_b32 s1, s13, 10
	v_and_b32_e32 v1, 24, v1
	v_and_b32_e32 v3, 4, v3
	v_and_or_b32 v5, v2, s6, v5
	s_add_i32 s41, s1, 0
	v_or3_b32 v1, v5, v3, v1
	s_add_i32 s42, s41, 0x10000
	v_mul_lo_u32 v2, v2, s12
	v_mul_lo_u32 v1, v1, s12
	s_and_b32 s5, s5, 0xffff
	s_mov_b32 s6, s38
	s_mov_b32 s7, s39
	s_lshl_b32 s28, s17, 19
	s_mov_b32 m0, s42
	s_add_i32 s43, s41, 0x12000
	v_add_lshl_u32 v166, v0, v2, 1
	v_add_lshl_u32 v167, v1, v0, 1
	s_lshl_b32 s33, s12, 8
	v_mov_b32 v0, 0
	buffer_load_dwordx4 v165, s[4:7], s28 offen lds
	s_mov_b32 m0, s43
	s_add_i32 s44, s41, 0x14000
	buffer_load_dwordx4 v167, s[4:7], s28 offen lds
	s_add_i32 s19, s28, s33
	s_mov_b32 m0, s44
	s_add_i32 s45, s41, 0x16000
	buffer_load_dwordx4 v165, s[4:7], s19 offen lds
	s_mov_b32 m0, s45
	s_lshl_b32 s29, s25, 19
	buffer_load_dwordx4 v167, s[4:7], s19 offen lds
	s_mov_b32 m0, s41
	s_add_i32 s52, s41, 0x2000
	buffer_load_dwordx4 v164, s[36:39], s29 offen lds
	s_mov_b32 m0, s52
	s_add_i32 s53, s41, 0x4000
	buffer_load_dwordx4 v166, s[36:39], s29 offen lds
	s_add_i32 s6, s29, s33
	s_mov_b32 m0, s53
	s_add_i32 s1, s41, 0x6000
	buffer_load_dwordx4 v164, s[36:39], s6 offen lds
	s_mov_b32 m0, s1
	s_ashr_i32 s18, s16, 8
	buffer_load_dwordx4 v166, s[36:39], s6 offen lds
	s_cmp_eq_u32 s18, 1
	s_cselect_b64 s[60:61], -1, 0
	s_cmp_lg_u32 s18, 1
	s_cbranch_scc1 .LBB0_345
	s_barrier

; __device__ __forceinline__ int opaque_s(int x) { asm volatile("" : "+s"(x)); return x; }
;     __device__ __forceinline__ bool next(int i, Unit& u) const { return so.next(i, u); }
;     __device__ __forceinline__ bool next(int i, Unit& u) const { const bool ok = so.next(i >> 1, u); u.part = i & 1; return ok; }
; #define KWS (kargs()->ws)
; #define REP(id) for (int rep_ = 0; rep_ < ((DUP_ID == (id)) ? DUP_N : 1); ++rep_)
;     __host__ __device__ bool next(int i, Unit& u) const {
;         const int L = i * G + c; if (L >= nwg) return false;
;         int wgid = L; { const int q = nwg / NXCD, r = nwg % NXCD, xcd = wgid % NXCD, off = wgid / NXCD; wgid = (xcd < r ? xcd * (q + 1) : r * (q + 1) + (xcd - r) * q) + off; }
;         const int nig = WGM * nN, gid = wgid / nig, fm = gid * WGM, gsz = (nM - fm) < WGM ? (nM - fm) : WGM;
;         u.pm = fm + ((wgid % nig) % gsz); u.pn = (wgid % nig) / gsz; u.part = 0; return true;
; __global__ void __launch_bounds__(512, 2) mega(Ptrs Pdummy) {
;     ...
;         REP(3) { unsigned char* ws = KWS; pg8::Gemm g{(const bf16*)(ws + WS_PB), (const bf16*)(ws + WS_WPP) + (size_t)l * DM * PLE, PLE, 0}; pg8::StaticOrder S; S.init(M, DM, opaque_s(G), opaque_s(c));
;           pg8::EpiStore16 E{(bf16*)(ws + WS_PP), DM, 1.f}; pg8::gemm_phase<pg8::EpiStore16, pg8::StaticOrder, true, true>(lds, g, S, E, wbase); }
.LBB0_435:
	s_mov_b64 s[8:9], s[100:101]
	s_andn2_b64 vcc, exec, s[4:5]
	s_ashr_i32 s2, s7, 3
	s_cbranch_vccnz .LBB0_437
	s_mul_i32 s13, s6, 0x41

; __device__ __forceinline__ unsigned xb_ld(unsigned* p)              { return __hip_atomic_load(p, __ATOMIC_RELAXED, __HIP_MEMORY_SCOPE_AGENT); }
; __device__ __forceinline__ void xcd_barrier_complete(unsigned* bar, unsigned x, unsigned& nloc, unsigned& nx) {
;     const unsigned G = gridDim.x * gridDim.y * gridDim.z;
;     unsigned sum, cnt, mine, sp = 0u;
;     for (;;) {
;         sum = 0u; cnt = 0u; mine = 0u;
; #pragma unroll
;         for (unsigned j = 0; j < 16; ++j) { const unsigned c = xb_ld(&bar[XB_XCNT(j)]); sum += c; cnt += (c > 0u) ? 1u : 0u; mine = (j == x) ? c : mine; }
; __device__ __forceinline__ void xcd_barrier(const XcdBarrier& b, bool leader) {
;     asm volatile("s_waitcnt vmcnt(0)" ::: "memory");
;     __syncthreads();
;     if (leader) {
;         unsigned zo_; asm volatile("v_mov_b32 %0, 0" : "=v"(zo_)); unsigned* bar = b.bar + zo_;
;         __builtin_amdgcn_s_waitcnt(0);
;         unsigned nloc = b.st[0], nx = b.st[1];
;         if (nloc == 0u) { xcd_barrier_complete(bar, b.x, nloc, nx); b.st[0] = nloc; b.st[1] = nx; }
.Lbinv_skip_1:
	s_and_saveexec_b64 s[4:5], vcc
	s_xor_b64 s[10:11], exec, s[4:5]
	s_cbranch_execz .LBB0_503
	s_mov_b64 s[2:3], s[100:101]
	v_mov_b32 v232, 0
	s_waitcnt vmcnt(0) expcnt(0) lgkmcnt(0)
	s_and_b32 s1, s1, 15
	v_lshl_add_u64 v[0:1], v[232:233], 2, s[2:3]
	s_mov_b64 s[2:3], 0x4000
	v_lshl_add_u64 v[0:1], v[0:1], 0, s[2:3]
	v_readlane_b32 s2, v255, 7
	s_nop 1
	v_mov_b32_e32 v2, s2
	ds_read_b32 v6, v2
	v_readlane_b32 s2, v255, 8
	s_waitcnt lgkmcnt(0)
	v_cmp_ne_u32_e32 vcc, 0, v6
	v_mov_b32_e32 v2, s2
	ds_read_b32 v4, v2
	s_cbranch_vccnz .LBB0_473
	v_readlane_b32 s4, v255, 0
	v_readlane_b32 s5, v255, 1
	s_load_dwordx2 s[2:3], s[4:5], 0x4
	s_mov_b64 s[4:5], 0x1100
	s_waitcnt lgkmcnt(0)
	v_lshl_add_u64 v[4:5], v[0:1], 0, s[4:5]
	s_mov_b64 s[4:5], 0x1200
	v_lshl_add_u64 v[6:7], v[0:1], 0, s[4:5]
	s_mov_b64 s[4:5], 0x1300
	v_lshl_add_u64 v[8:9], v[0:1], 0, s[4:5]
	v_readlane_b32 s4, v255, 4
	s_mul_i32 s22, s2, s4
	v_lshl_add_u64 v[2:3], v[0:1], 0, s[72:73]
	v_readlane_b32 s5, v255, 5
	s_mul_i32 s22, s22, s3
	s_mov_b32 s23, 1
	s_mov_b64 s[2:3], 0
	s_branch .LBB0_463

; #define LAS __attribute__((address_space(3)))
; __device__ __forceinline__ CJob moe_job(KP P, int j2, int j) {
;     CJob jb; jb.pad = 0; jb.gain = nullptr; jb.mode = 0; jb.fp8 = MOE_FP8 ? 1 : 0; jb.wscale = 1.f; jb.col0 = 0; const int e = j / 3, k = j % 3;
;     if (k < 2) { jb.W = P->in[24 + k] + ((size_t)j2 * NEXP + e) * DM * DFF; jb.gain = P->in[18] + (2 * j2 + 1) * DM; jb.dst = (bf16*)(P->ws + WS_W13E + (size_t)e * 2 * DFF * DM * (MOE_FP8 ? 1 : 2)); jb.K = DM; jb.N = DFF; jb.mode = 4 + k; jb.wscale = MOE_FP8 ? W13_SCALE : 1.f; }
;     else { jb.W = P->in[26] + ((size_t)j2 * NEXP + e) * DFF * DM; jb.dst = (bf16*)(P->ws + WS_W2E + (size_t)e * DM * DFF * (MOE_FP8 ? 1 : 2)); jb.K = DFF; jb.N = DM; jb.wscale = MOE_FP8 ? W2_SCALE : 1.f; }
;     jb.ldw = jb.N;
;     return jb;
; }
; __device__ __forceinline__ void conv_moe_layer(KP P, int j2, LAS float* scr, int gw, int ngw, int lane) {
;     constexpr int IT = (DM / 64) * (DFF / 32), NT = 24 * IT;
;     int fl = gw; if (fl >= NT) return;
;     CJob jb = moe_job(P, j2, fl / IT); f32x4 v[8]; conv_load(jb, fl % IT, lane, v);
;     for (;;) { const int nx = fl + ngw; const bool has = nx < NT; CJob jn = jb; f32x4 w[8];
;         if (has) { jn = moe_job(P, j2, nx / IT); conv_load(jn, nx % IT, lane, w); }
.LBB0_505:
	s_andn2_b64 vcc, exec, s[62:63]
	s_cbranch_vccnz .LBB0_543
	s_mov_b32 s1, s38
	s_barrier
	s_mov_b64 s[4:5], s[88:89]
	v_mbcnt_lo_u32_b32 v0, s1, 0
	v_mbcnt_hi_u32_b32 v0, s1, v0
	v_add_u32_e32 v0, s93, v0
	s_nop 0
	v_readfirstlane_b32 s1, v0
	s_ashr_i32 s20, s1, 6
	v_readlane_b32 s1, v255, 27
	s_add_i32 s31, s20, s1
	s_cmp_gt_i32 s31, 0xa7ff
	s_cbranch_scc1 .LBB0_542
	s_mul_hi_i32 s1, s31, 0x92492493
	s_add_i32 s1, s1, s31
	s_lshr_b32 s2, s1, 31
	s_ashr_i32 s21, s1, 10
	s_add_i32 s21, s21, s2
	s_mul_hi_i32 s1, s31, 0x30c30c31
	s_lshr_b32 s2, s1, 31
	s_ashr_i32 s13, s1, 10
	s_mul_hi_i32 s1, s21, 0x55555556
	s_add_i32 s13, s13, s2
	s_lshr_b32 s2, s1, 31
	s_add_i32 s1, s1, s2
	s_mul_i32 s1, s1, 3
	s_lshr_b32 s16, s95, 1
	s_sub_i32 s18, s21, s1
	s_cmp_gt_i32 s18, 1
	s_mov_b64 s[2:3], -1
	s_mul_hi_u32 s1, s16, 0x7000000
	s_mul_i32 s12, s16, 0x7000000
	s_cbranch_scc0 .LBB0_509
	s_mov_b32 s17, s40
	s_lshl_b64 s[8:9], s[16:17], 3
	s_ashr_i32 s2, s13, 31
	s_add_u32 s6, s8, s13
	s_addc_u32 s2, s9, s2
	s_mul_i32 s7, s2, 0xe00000
	s_load_dwordx2 s[2:3], s[4:5], 0xd0
	s_mul_hi_u32 s10, s6, 0xe00000
	s_add_i32 s10, s10, s7
	s_mul_i32 s11, s6, 0xe00000
	s_mov_b64 s[6:7], s[100:101]
	s_waitcnt lgkmcnt(0)
	s_add_u32 s14, s2, s11
	s_addc_u32 s15, s3, s10
	s_mul_i32 s3, s13, 0x380000
	s_mul_hi_i32 s2, s13, 0x380000
	s_add_u32 s3, s6, s3
	s_addc_u32 s2, s7, s2
	s_add_u32 s10, s3, 0xea00000
	s_addc_u32 s11, s2, 0
	s_mov_b64 s[2:3], 0
.LBB0_509:
	s_lshl_b32 s6, s16, 11
	s_andn2_b64 vcc, exec, s[2:3]
	s_mov_b32 s7, s40
	s_cbranch_vccnz .LBB0_511
	s_ashr_i32 s19, s18, 31
	s_lshl_b64 s[2:3], s[18:19], 3
	s_add_u32 s2, s4, s2
	s_addc_u32 s3, s5, s3
	s_load_dwordx2 s[2:3], s[2:3], 0xc0
	s_mul_i32 s9, s13, 0xe00000
	s_mul_hi_i32 s8, s13, 0xe00000
	s_mul_hi_i32 s10, s13, 0x700000
	s_mul_i32 s13, s13, 0x700000
	s_waitcnt lgkmcnt(0)
	s_add_u32 s2, s2, s9
	s_addc_u32 s3, s3, s8
	s_add_u32 s14, s2, s12
	s_addc_u32 s15, s3, s1
	s_load_dwordx2 s[2:3], s[4:5], 0x90
	s_lshl_b64 s[8:9], s[6:7], 2
	s_mov_b32 s17, s40
	s_mov_b32 s24, 0x42800000
	s_movk_i32 s33, 0xe00
	s_waitcnt lgkmcnt(0)
	s_add_u32 s2, s2, s8
	s_addc_u32 s3, s3, s9
	s_mov_b64 s[8:9], s[100:101]
	s_add_u32 s2, s2, 0x1000
	s_addc_u32 s3, s3, 0
	s_waitcnt lgkmcnt(0)
	s_add_u32 s8, s8, s13
	s_addc_u32 s9, s9, s10
	s_add_u32 s10, s8, 0x7a00000
	s_addc_u32 s11, s9, 0
	s_add_i32 s30, s18, 4
	s_lshl_b64 s[8:9], s[16:17], 3
	s_movk_i32 s13, 0x400
	s_branch .LBB0_512

; #define LAS __attribute__((address_space(3)))
; __device__ __forceinline__ CJob moe_job(KP P, int j2, int j) {
;     CJob jb; jb.pad = 0; jb.gain = nullptr; jb.mode = 0; jb.fp8 = MOE_FP8 ? 1 : 0; jb.wscale = 1.f; jb.col0 = 0; const int e = j / 3, k = j % 3;
;     if (k < 2) { jb.W = P->in[24 + k] + ((size_t)j2 * NEXP + e) * DM * DFF; jb.gain = P->in[18] + (2 * j2 + 1) * DM; jb.dst = (bf16*)(P->ws + WS_W13E + (size_t)e * 2 * DFF * DM * (MOE_FP8 ? 1 : 2)); jb.K = DM; jb.N = DFF; jb.mode = 4 + k; jb.wscale = MOE_FP8 ? W13_SCALE : 1.f; }
;     else { jb.W = P->in[26] + ((size_t)j2 * NEXP + e) * DFF * DM; jb.dst = (bf16*)(P->ws + WS_W2E + (size_t)e * DM * DFF * (MOE_FP8 ? 1 : 2)); jb.K = DFF; jb.N = DM; jb.wscale = MOE_FP8 ? W2_SCALE : 1.f; }
;     jb.ldw = jb.N;
;     return jb;
; }
; __device__ __forceinline__ void conv_moe_layer(KP P, int j2, LAS float* scr, int gw, int ngw, int lane) {
;     constexpr int IT = (DM / 64) * (DFF / 32), NT = 24 * IT;
;     int fl = gw; if (fl >= NT) return;
;     CJob jb = moe_job(P, j2, fl / IT); f32x4 v[8]; conv_load(jb, fl % IT, lane, v);
;     for (;;) { const int nx = fl + ngw; const bool has = nx < NT; CJob jn = jb; f32x4 w[8];
;         if (has) { jn = moe_job(P, j2, nx / IT); conv_load(jn, nx % IT, lane, w); }
.LBB0_514:
	s_add_i32 s25, s31, s94
	s_cmp_lt_i32 s25, 0xa800
	s_cselect_b64 s[18:19], -1, 0
	s_cmp_gt_i32 s25, 0xa7ff
	s_cbranch_scc1 .LBB0_521
	s_mul_hi_i32 s14, s25, 0x92492493
	s_add_i32 s14, s14, s25
	s_lshr_b32 s15, s14, 31
	s_ashr_i32 s34, s14, 10
	s_add_i32 s34, s34, s15
	s_mul_hi_i32 s14, s25, 0x30c30c31
	s_lshr_b32 s15, s14, 31
	s_ashr_i32 s26, s14, 10
	s_mul_hi_i32 s14, s34, 0x55555556
	s_add_i32 s26, s26, s15
	s_lshr_b32 s15, s14, 31
	s_add_i32 s14, s14, s15
	s_mul_i32 s14, s14, 3
	s_sub_i32 s22, s34, s14
	s_cmp_gt_i32 s22, 1
	s_mov_b64 s[14:15], -1
	s_cbranch_scc0 .LBB0_517
	s_ashr_i32 s14, s26, 31
	s_add_u32 s16, s8, s26
	s_addc_u32 s14, s9, s14
	s_mul_i32 s17, s14, 0xe00000
	s_load_dwordx2 s[14:15], s[4:5], 0xd0
	s_mul_hi_u32 s20, s16, 0xe00000
	s_add_i32 s21, s20, s17
	s_mul_i32 s20, s16, 0xe00000
	s_mov_b64 s[16:17], s[100:101]
	s_waitcnt lgkmcnt(0)
	s_add_u32 s20, s14, s20
	s_addc_u32 s21, s15, s21
	s_mul_i32 s15, s26, 0x380000
	s_mul_hi_i32 s14, s26, 0x380000
	s_add_u32 s15, s16, s15
	s_addc_u32 s14, s17, s14
	s_add_u32 s16, s15, 0xea00000
	s_addc_u32 s17, s14, 0
	s_mov_b64 s[14:15], 0
.LBB0_517:
	s_andn2_b64 vcc, exec, s[14:15]
	s_cbranch_vccnz .LBB0_519
	s_ashr_i32 s23, s22, 31
	s_lshl_b64 s[14:15], s[22:23], 3
	s_add_u32 s14, s4, s14
	s_addc_u32 s15, s5, s15
	s_load_dwordx2 s[14:15], s[14:15], 0xc0
	s_mul_i32 s17, s26, 0xe00000
	s_mul_hi_i32 s16, s26, 0xe00000
	s_mul_hi_i32 s23, s26, 0x700000
	s_mul_i32 s26, s26, 0x700000
	s_waitcnt lgkmcnt(0)
	s_add_u32 s14, s14, s17
	s_addc_u32 s15, s15, s16
	s_add_u32 s20, s14, s12
	s_addc_u32 s21, s15, s1
	s_load_dwordx2 s[14:15], s[4:5], 0x90
	s_lshl_b64 s[16:17], s[6:7], 2
	s_mov_b32 s27, 0x42800000
	s_movk_i32 s28, 0xe00
	s_movk_i32 s29, 0x400
	s_waitcnt lgkmcnt(0)
	s_add_u32 s14, s14, s16
	s_addc_u32 s15, s15, s17
	s_mov_b64 s[16:17], s[100:101]
	s_add_u32 s14, s14, 0x1000
	s_addc_u32 s15, s15, 0
	s_waitcnt lgkmcnt(0)
	s_add_u32 s16, s16, s26
	s_addc_u32 s17, s17, s23
	s_add_u32 s16, s16, 0x7a00000
	s_addc_u32 s17, s17, 0
	s_add_i32 s26, s22, 4
	s_branch .LBB0_520

; #define LAS __attribute__((address_space(3)))
; __device__ __forceinline__ int opaque_s(int x) { asm volatile("" : "+s"(x)); return x; }
; __device__ __forceinline__ void attn_phase(LAS unsigned char* lds, const bf16* U, bf16* YA, const float* sinks, const float* rel_bias, int G, int c, int wbase, int y8) {
;     const int tid = opaque_tid(wbase), lane = tid & 63, wid = __builtin_amdgcn_readfirstlane(tid >> 6), r32 = lane & 31, hi = lane >> 5;
;     const int g = wid >> 1, qh = wid & 1; G = opaque_s(G); c = opaque_s(c);
;     LAS float* rbt = (LAS float*)(lds + RBT); LAS float* lscr = (LAS float*)(lds + LSCR) + wid * 32; LAS bf16* stg = (LAS bf16*)(lds + OST + wid * 4096);
;     int kvh_tab = -1;
;     for (int L = c; L < BATCH * 32 * 4; L += G) {
;         const int kvh = L & 3, n = (L >> 2) & 31, b = L >> 7;
;         const int tok0 = b * SEQ + (n - 1) * 128;
;         if (kvh != kvh_tab) { kvh_tab = kvh;
;             for (int e = tid; e < 4 * 192; e += 512) { const int gg = e / 192, jj = e % 192, dist = 159 - jj;
;                 rbt[e] = (dist >= 0 && dist < 128) ? rel_bias[t5_bucket(dist) * 16 + kvh * 4 + gg] * LOG2E : -1.0e30f; } }
; #pragma unroll
;         for (int kg = 0; kg < 4; ++kg) { const int key = 64 * kg + lane; int t = tok0 + key; if (t < b * SEQ) t = b * SEQ;
;             __builtin_amdgcn_global_load_lds((const unsigned*)(U + (size_t)t * NIN + C_K + kvh * 64 + 8 * wid), (LAS unsigned*)(lds + KIMG + wid * 4096 + kg * 1024), 16, 0, 0); }
; #pragma unroll
;         for (int j = 0; j < 4; ++j) { const int kg16 = 4 * (wid & 3) + j, key = 16 * kg16 + (lane >> 2); int t = tok0 + key; if (t < b * SEQ) t = b * SEQ;
;             __builtin_amdgcn_global_load_lds((const unsigned*)(U + (size_t)t * NIN + C_V + kvh * 64 + 32 * (wid >> 2) + 8 * (lane & 3)), (LAS unsigned*)(lds + VIMG + (wid >> 2) * 16384 + kg16 * 1024), 16, 0, 0); }
;         const size_t mq0 = (size_t)b * SEQ + n * 128 + 64 * qh;
;         bf16x8 qf[2][4];
; #pragma unroll
;         for (int qt = 0; qt < 2; ++qt)
; #pragma unroll
;             for (int d0 = 0; d0 < 4; ++d0) qf[qt][d0] = *(const bf16x8*)(U + (mq0 + 32 * qt + r32) * NIN + (kvh * 4 + g) * 64 + 16 * d0 + 8 * hi);
;         asm volatile("s_waitcnt vmcnt(0)" ::: "memory"); __syncthreads();
;         const float sink2 = sinks[kvh * 4 + g] * LOG2E; const LAS float* bt = rbt + g * 192 + 31 - r32 + 4 * hi;
.LBB0_543:
	s_mov_b64 s[6:7], s[88:89]
	s_mov_b64 s[4:5], s[88:89]
	s_mov_b64 s[2:3], s[88:89]
	s_mov_b32 s8, s95
	s_mov_b32 s1, s38
	v_readlane_b32 s10, v255, 4
	v_mbcnt_lo_u32_b32 v0, s1, 0
	v_mbcnt_hi_u32_b32 v0, s1, v0
	s_waitcnt vmcnt(11)
	v_add_u32_e32 v109, s93, v0
	s_mov_b32 s1, s10
	s_mov_b32 s33, s92
	s_cmpk_gt_i32 s33, 0x3ff
	v_readfirstlane_b32 s9, v109
	v_readlane_b32 s11, v255, 5
	s_cbranch_scc1 .LBB0_590
	s_mov_b64 s[12:13], s[100:101]
	s_lshl_b32 s6, s95, 4
	s_load_dwordx2 s[4:5], s[4:5], 0x30
	s_mov_b32 s7, s40
	s_load_dwordx2 s[14:15], s[2:3], 0x38
	s_waitcnt lgkmcnt(0)
	s_add_u32 s10, s12, 0x1f800000
	s_addc_u32 s11, s13, 0
	s_lshl_b64 s[6:7], s[6:7], 2
	s_add_u32 s36, s4, s6
	s_addc_u32 s37, s5, s7
	s_ashr_i32 s2, s9, 6
	s_lshl_b32 s3, s2, 7
	s_add_i32 s3, s3, 0
	s_add_i32 s22, s3, 0x10c00
	s_lshl_b32 s3, s2, 12
	s_lshl_b32 s4, s2, 3
	s_lshl_b32 s2, s2, 2
	s_and_b32 s20, s2, 12
	s_ashr_i32 s2, s9, 8
	s_ashr_i32 s41, s9, 7
	s_lshl_b32 s6, s2, 5
	s_lshl_b32 s2, s2, 14
	v_and_b32_e32 v108, 31, v109
	s_add_i32 s28, s2, 0
	s_mul_i32 s2, s41, 0x300
	s_add_i32 s23, 0, 0x10000
	v_bfe_u32 v1, v109, 5, 1
	s_add_i32 s2, s23, s2
	v_lshlrev_b32_e32 v3, 2, v108
	v_lshlrev_b32_e32 v232, 4, v1
	v_sub_u32_e32 v4, s2, v3
	s_waitcnt vmcnt(8)
	v_add_u32_e32 v121, v4, v232
	v_lshlrev_b32_e32 v4, 12, v1
	v_lshlrev_b32_e32 v5, 4, v108
	s_add_i32 s42, s3, 0
	s_and_b32 s16, s9, 64
	v_add3_u32 v123, 0, v4, v5
	v_lshlrev_b32_e32 v4, 1, v109
	v_lshlrev_b32_e32 v5, 4, v109
	s_lshl_b32 s8, 1, s8
	s_add_i32 s18, s42, 0x11000
	s_ashr_i32 s5, s4, 31
	s_ashr_i32 s7, s6, 31
	v_lshlrev_b32_e32 v2, 3, v109
	s_lshl_b32 s43, s41, 6
	s_lshr_b32 s24, s16, 5
	v_and_b32_e32 v4, 32, v4
	v_and_b32_e32 v5, 0xc0, v5
	s_and_b32 s8, s8, 14
	v_and_b32_e32 v0, 24, v2
	v_add_u32_e32 v4, 0, v4
	v_lshl_or_b32 v5, v1, 8, v5
	v_add_u32_e32 v126, s22, v3
	v_and_b32_e32 v2, 56, v2
	s_cmp_lg_u32 s8, 0
	v_mov_b32_e32 v3, v233
	v_add3_u32 v125, v4, v0, v5
	v_lshl_add_u32 v127, v108, 1, s18
	v_lshl_add_u32 v6, v2, 1, s18
	s_cselect_b64 s[18:19], -1, 0
	v_lshl_add_u64 v[4:5], s[12:13], 0, v[2:3]
	s_or_b32 s12, s20, 2
	s_mov_b64 s[8:9], 0x35800000
	s_lshl_b32 s52, s12, 4
	s_lshl_b32 s29, s12, 10
	s_or_b32 s12, s20, 3
	v_lshl_add_u64 v[114:115], v[4:5], 0, s[8:9]
	s_or_b32 s9, s20, 1
	s_lshl_b32 s53, s12, 4
	s_lshl_b32 s30, s12, 10
	s_or_b32 s12, s24, 1
	s_add_i32 s13, s24, 2
	s_add_i32 s25, s24, 3
	s_or_b32 s26, s24, 4
	v_bfe_u32 v112, v109, 3, 3
	s_lshl_b32 s44, s20, 4
	s_lshl_b32 s8, s20, 10
	s_lshl_b32 s45, s9, 4
	s_lshl_b32 s9, s9, 10
	s_lshl_b32 s58, s16, 4
	s_lshl_b32 s59, s12, 9
	s_lshl_b32 s65, s13, 9
	s_lshl_b32 s76, s25, 9
	s_lshl_b32 s77, s26, 9
	s_movk_i32 s3, 0x2ff
	s_cmp_eq_u32 s16, 0
	v_lshlrev_b32_e32 v129, 9, v1
	v_or_b32_e32 v120, 8, v112
	v_or_b32_e32 v122, 16, v112
	v_or_b32_e32 v124, 24, v112
	s_mov_b64 s[60:61], s[84:85]
	v_and_b32_e32 v113, 63, v109
	v_cmp_lt_i32_e32 vcc, s3, v109
	v_lshl_add_u64 v[116:117], v[114:115], 0, v[2:3]
	s_cselect_b64 s[20:21], -1, 0
	v_add_u32_e32 v128, s22, v232
	v_or_b32_e32 v1, 0x80, v129
	v_or_b32_e32 v2, 0x100, v129
	v_or_b32_e32 v3, 0x180, v129
	v_or_b32_e32 v4, 0x400, v129
	v_or_b32_e32 v5, 0x480, v129
	v_or_b32_e32 v7, 0x500, v129
	v_or_b32_e32 v8, 0x580, v129
	v_or_b32_e32 v9, 0x800, v129
	v_or_b32_e32 v10, 0x880, v129
	v_or_b32_e32 v11, 0x900, v129
	v_or_b32_e32 v12, 0x980, v129
	v_or_b32_e32 v13, 0xc00, v129
	v_or_b32_e32 v14, 0xc80, v129
	v_or_b32_e32 v15, 0xd00, v129
	v_or_b32_e32 v16, 0xd80, v129
	v_lshlrev_b32_e32 v17, 7, v112
	v_lshlrev_b32_e32 v18, 7, v120
	v_lshlrev_b32_e32 v19, 7, v122
	v_lshlrev_b32_e32 v20, 7, v124
	s_or_b32 s22, s24, 5
	s_add_i32 s85, s28, s8
	s_add_i32 s48, s28, s9
	s_add_i32 s46, s28, s29
	s_add_i32 s47, s28, s30
	v_bfe_u32 v119, v109, 2, 4
	s_mov_b32 s17, s40
	v_lshl_add_u64 v[110:111], s[10:11], 0, v[232:233]
	v_cmp_gt_u32_e64 s[2:3], 32, v113
	v_or_b32_e32 v118, 32, v108
	s_lshl_b32 s82, s16, 6
	s_lshl_b32 s83, s12, 11
	s_lshl_b32 s12, s13, 11
	s_lshl_b32 s13, s25, 11
	s_lshl_b32 s56, s26, 11
	s_lshl_b32 s57, s22, 9
	s_lshl_b32 s79, s22, 11
	v_sub_u32_e32 v130, 0x9f, v109
	v_lshl_add_u32 v131, v109, 2, s23
	s_mov_b32 s84, -1
	s_xor_b64 s[22:23], vcc, -1
	s_lshl_b64 s[24:25], s[4:5], 1
	s_lshl_b64 s[26:27], s[6:7], 1
	v_lshlrev_b32_e32 v232, 1, v0
	s_add_i32 s85, s85, 0x8000
	s_add_i32 s48, s48, 0x8000
	s_add_i32 s46, s46, 0x8000
	s_add_i32 s47, s47, 0x8000
	v_add_u32_e32 v132, v127, v1
	v_add_u32_e32 v133, v127, v2
	v_add_u32_e32 v134, v127, v3
	v_add_u32_e32 v135, v127, v4
	v_add_u32_e32 v136, v127, v5
	v_add_u32_e32 v137, v127, v7
	v_add_u32_e32 v138, v127, v8
	v_add_u32_e32 v139, v127, v9
	v_add_u32_e32 v140, v127, v10
	v_add_u32_e32 v141, v127, v11
	v_add_u32_e32 v142, v127, v12
	v_add_u32_e32 v143, v127, v13
	v_add_u32_e32 v144, v127, v14
	v_add_u32_e32 v145, v127, v15
	v_add_u32_e32 v146, v127, v16
	v_add_u32_e32 v147, v6, v17
	v_add_u32_e32 v148, v6, v18
	v_add_u32_e32 v149, v6, v19
	v_add_u32_e32 v150, v6, v20
	s_branch .LBB0_547

; #define LAS __attribute__((address_space(3)))
; __device__ __forceinline__ void lru_scan(LAS unsigned char* lds, const bf16* U, bf16* HR, bf16* PQ, float* AGG, const bf16* Wt, const float* conv_w, const float* conv_b,
;                                          const float* b_rg, const float* b_ig, const float* lam, int G, int c, int wbase) {
;     const int tid = opaque_tid(wbase), lane = tid & 63, wid = __builtin_amdgcn_readfirstlane(tid >> 6), r32 = lane & 31, hi = lane >> 5; G = opaque_s(G); c = opaque_s(c);
;     LAS unsigned char* wl = lds + wid * WAVE_LDS; LAS bf16* stH = (LAS bf16*)wl; LAS bf16* stP = (LAS bf16*)(wl + 32 * 128);
;     LAS float* cw = (LAS float*)(wl + ST_BYTES);
;     int nb_l = -1;
;     for (int un = c * 8 + wid; un < NUNIT; un += G * 8) {
;         const int ck = un & (NCK - 1), nb = (un >> 5) & 15, b = un >> 9, ch0 = nb * 64;
;         if (nb != nb_l) {
;             __syncthreads();
; #pragma unroll
;             for (int j = 0; j < 2; ++j) { const int p = tid + 512 * j, row = p >> 3, seg = p & 7;
;                 *(LAS u32x4*)(lds + WL_OFF + row * WL_ROW + seg * 16) = *(const u32x4*)(Wt + (size_t)(row >> 6) * 16 * 64 * 64 + (size_t)(nb * 64 + (row & 63)) * 64 + seg * 8); }
;             __syncthreads(); nb_l = nb; }
; #pragma unroll
;         for (int j = 0; j < 4; ++j) cw[j * 64 + lane] = conv_w[j * DM + ch0 + lane];
;         cw[4 * 64 + lane] = conv_b[ch0 + lane];
;         float brg[2], big[2], sp8[2], carry[2], prodA[2];
; #pragma unroll
;         for (int ct = 0; ct < 2; ++ct) { const int ch = ch0 + 32 * ct + r32; brg[ct] = b_rg[ch] * -LOG2E; big[ct] = b_ig[ch] * -LOG2E; { const float x = fast_exp(-lam[ch]); sp8[ct] = (-8.f * LOG2E) * (x < 0.25f ? x * (1.f - x * (0.5f - x * ((1.f / 3.f) - x * (0.25f - x * (0.2f - x * (1.f / 6.f)))))) : (__builtin_amdgcn_logf(1.f + x) * 0.6931471805599453f)); } carry[ct] = 0.f; prodA[ct] = 1.f; }
;         asm volatile("s_waitcnt lgkmcnt(0)" ::: "memory");
;         u32x4 raw[4][4];
;     ...
;         LRU_LOAD_RAW(0);
;         for (int st = 0; st < 4; ++st) {
;             const int t0 = ck * TC + st * 32, t = t0 + r32;
;             bf16x8 af[4];
; #pragma unroll
;             for (int ks = 0; ks < 4; ++ks) { const int cl = 16 * ks + 8 * hi; f32x4 x0 = *(const LAS f32x4*)(cw + 256 + cl), x1 = *(const LAS f32x4*)(cw + 256 + cl + 4);
; #pragma unroll
.LBB0_590:
	s_mov_b64 s[8:9], s[88:89]
	s_mov_b64 s[14:15], s[88:89]
	s_mov_b64 s[10:11], s[88:89]
	s_mov_b64 s[6:7], s[88:89]
	s_mov_b64 s[4:5], s[88:89]
	s_mov_b64 s[2:3], s[88:89]
	s_mov_b32 s1, s38
	s_barrier
	v_readlane_b32 s12, v255, 4
	v_mbcnt_lo_u32_b32 v0, s1, 0
	v_mbcnt_hi_u32_b32 v0, s1, v0
	v_add_u32_e32 v0, s93, v0
	v_readlane_b32 s13, v255, 5
	v_readfirstlane_b32 s28, v0
	s_mov_b32 s1, s92
	s_lshl_b32 s16, s95, 10
	s_ashr_i32 s29, s28, 6
	s_lshl_b32 s13, s1, 3
	s_mov_b32 s17, s40
	s_add_i32 s1, s13, s29
	v_writelane_b32 v255, s16, 33
	s_cmpk_lt_i32 s1, 0x1000
	s_nop 0
	v_writelane_b32 v255, s17, 34
	s_cbranch_scc0 .LBB0_633
	s_mov_b64 s[8:9], s[100:101]
	s_lshl_b32 s18, s95, 12
	s_load_dwordx2 s[20:21], s[14:15], 0x40
	s_mov_b32 s19, s40
	s_load_dwordx2 s[10:11], s[10:11], 0x48
	s_waitcnt lgkmcnt(0)
	s_add_u32 s14, s8, 0x1f800000
	s_addc_u32 s15, s9, 0
	s_add_u32 s16, s8, 0x17600000
	s_addc_u32 s17, s9, 0
	s_lshl_b64 s[18:19], s[18:19], 2
	s_add_u32 s18, s20, s18
	s_addc_u32 s19, s21, s19
	v_readlane_b32 s20, v255, 33
	s_load_dwordx2 s[6:7], s[6:7], 0x58
	v_readlane_b32 s21, v255, 34
	s_lshl_b64 s[26:27], s[20:21], 2
	s_load_dwordx2 s[4:5], s[4:5], 0x68
	s_add_u32 s20, s10, s26
	s_addc_u32 s21, s11, s27
	s_load_dwordx2 s[2:3], s[2:3], 0x70
	s_waitcnt lgkmcnt(0)
	s_add_u32 s22, s6, s26
	s_addc_u32 s23, s7, s27
	s_add_u32 s24, s4, s26
	s_addc_u32 s25, s5, s27
	s_add_u32 s26, s2, s26
	s_mulk_i32 s29, 0x2600
	s_addc_u32 s27, s3, s27
	s_add_i32 s6, s29, 0
	s_lshr_b32 s7, s28, 6
	s_lshl_b32 s2, s95, 18
	s_add_u32 s2, s8, s2
	v_lshlrev_b32_e32 v4, 3, v0
	s_addc_u32 s3, s9, 0
	v_and_b32_e32 v183, 56, v4
	v_ashrrev_i32_e32 v4, 9, v0
	s_add_u32 s4, s2, 0x7900000
	v_bfe_u32 v1, v0, 5, 1
	v_lshlrev_b32_e32 v2, 4, v0
	v_ashrrev_i32_e32 v5, 31, v4
	v_and_b32_e32 v144, 31, v0
	s_addc_u32 s5, s3, 0
	v_and_b32_e32 v232, 0x70, v2
	v_lshlrev_b32_e32 v2, 3, v1
	v_lshlrev_b64 v[4:5], 17, v[4:5]
	v_lshl_add_u64 v[4:5], s[4:5], 0, v[4:5]
	v_cmp_eq_u32_e32 vcc, v2, v144
	v_mov_b32_e32 v18, 0x3f80
	v_or_b32_e32 v12, 1, v2
	v_lshl_add_u64 v[146:147], v[4:5], 0, v[232:233]
	v_add_u32_e32 v4, 0x200, v0
	v_cndmask_b32_e32 v10, 0, v18, vcc
	v_or_b32_e32 v11, 2, v2
	v_cmp_eq_u32_e32 vcc, v12, v144
	v_ashrrev_i32_e32 v9, 3, v4
	v_ashrrev_i32_e32 v4, 9, v4
	v_cndmask_b32_e32 v12, 0, v18, vcc
	v_cmp_eq_u32_e32 vcc, v11, v144
	v_or_b32_e32 v14, 3, v2
	v_ashrrev_i32_e32 v5, 31, v4
	v_cndmask_b32_e32 v11, 0, v18, vcc
	v_or_b32_e32 v13, 4, v2
	v_cmp_eq_u32_e32 vcc, v14, v144
	v_lshlrev_b64 v[4:5], 17, v[4:5]
	v_or_b32_e32 v15, 6, v2
	v_cndmask_b32_e32 v14, 0, v18, vcc
	v_cmp_eq_u32_e32 vcc, v13, v144
	v_lshl_add_u64 v[4:5], s[4:5], 0, v[4:5]
	v_or_b32_e32 v16, 5, v2
	v_cndmask_b32_e32 v13, 0, v18, vcc
	v_cmp_eq_u32_e32 vcc, v15, v144
	v_lshl_add_u64 v[148:149], v[4:5], 0, v[232:233]
	v_and_b32_e32 v5, 32, v0
	v_cndmask_b32_e32 v15, 0, v18, vcc
	v_cmp_eq_u32_e32 vcc, v16, v144
	v_or_b32_e32 v17, 7, v2
	v_add_u32_e32 v186, s6, v5
	v_or_b32_e32 v5, 16, v2
	v_cndmask_b32_e32 v16, 0, v18, vcc
	v_cmp_eq_u32_e32 vcc, v17, v144
	s_mov_b32 s4, 0x5040100
	v_perm_b32 v49, v14, v11, s4
	v_cndmask_b32_e32 v17, 0, v18, vcc
	v_cmp_eq_u32_e32 vcc, v5, v144
	v_or_b32_e32 v11, 18, v2
	v_perm_b32 v48, v12, v10, s4
	v_cndmask_b32_e32 v5, 0, v18, vcc
	v_or_b32_e32 v10, 19, v2
	v_cmp_eq_u32_e32 vcc, v11, v144
	v_lshlrev_b32_e32 v6, 4, v1
	v_or_b32_e32 v12, 48, v2
	v_cndmask_b32_e32 v11, 0, v18, vcc
	v_cmp_eq_u32_e32 vcc, v10, v144
	v_readlane_b32 s11, v255, 9
	v_bfe_u32 v182, v0, 3, 3
	v_cndmask_b32_e32 v10, 0, v18, vcc
	v_perm_b32 v53, v10, v11, s4
	v_or_b32_e32 v11, 20, v2
	v_or_b32_e32 v10, 21, v2
	v_cmp_eq_u32_e32 vcc, v11, v144
	v_ashrrev_i32_e32 v8, 3, v0
	s_movk_i32 s10, 0x90
	v_cndmask_b32_e32 v11, 0, v18, vcc
	v_cmp_eq_u32_e32 vcc, v10, v144
	v_and_b32_e32 v145, 63, v0
	v_add_u32_e32 v3, s11, v232
	v_cndmask_b32_e32 v10, 0, v18, vcc
	v_perm_b32 v54, v10, v11, s4
	v_or_b32_e32 v11, 22, v2
	v_or_b32_e32 v10, 23, v2
	v_cmp_eq_u32_e32 vcc, v11, v144
	v_lshl_add_u32 v7, v183, 1, s6
	v_and_b32_e32 v184, 63, v8
	v_cndmask_b32_e32 v11, 0, v18, vcc
	v_cmp_eq_u32_e32 vcc, v10, v144
	v_mul_lo_u32 v8, v8, s10
	v_and_b32_e32 v185, 63, v9
	v_cndmask_b32_e32 v10, 0, v18, vcc
	v_perm_b32 v55, v10, v11, s4
	v_lshlrev_b32_e32 v10, 1, v144
	v_lshl_or_b32 v1, v1, 9, v10
	v_add_u32_e32 v187, s6, v1
	v_or_b32_e32 v1, 32, v144
	v_or_b32_e32 v11, 17, v2
	v_cmp_eq_u32_e32 vcc, v12, v1
	v_mul_u32_u24_e32 v10, 0x90, v1
	v_mul_lo_u32 v4, v9, s10
	v_cndmask_b32_e32 v1, 0, v18, vcc
	v_cmp_eq_u32_e32 vcc, v11, v144
	v_mul_u32_u24_e32 v9, 0x90, v144
	v_or_b32_e32 v190, 8, v182
	v_cndmask_b32_e32 v11, 0, v18, vcc
	v_or_b32_e32 v194, 16, v182
	v_or_b32_e32 v196, 24, v182
	v_lshrrev_b32_e32 v0, 1, v0
	v_lshl_add_u32 v151, v145, 2, s6
	v_cmp_gt_u32_e64 s[2:3], 32, v145
	s_lshl_b32 s12, s12, 3
	v_perm_b32 v50, v16, v13, s4
	v_perm_b32 v51, v17, v15, s4
	v_lshl_add_u32 v188, v12, 2, s6
	v_perm_b32 v52, v11, v5, s4
	v_perm_b32 v56, v11, v1, s4
	v_mov_b32_e32 v57, v53
	v_mov_b32_e32 v58, v54
	v_mov_b32_e32 v59, v55
	v_lshl_add_u32 v189, v182, 7, v7
	v_lshl_add_u32 v191, v190, 7, v7
	v_lshl_add_u32 v195, v194, 7, v7
	v_lshl_add_u32 v197, v196, 7, v7
	v_add3_u32 v198, v6, v9, s11
	v_add3_u32 v199, v10, v6, s11
	v_and_b32_e32 v150, 16, v0
	s_add_i32 s13, s13, s7
	s_mov_b32 s31, -1
	v_add_u32_e32 v200, v3, v8
	v_add_u32_e32 v201, v3, v4
	v_lshlrev_b32_e32 v152, 1, v2
	s_branch .LBB0_593

; __device__ __forceinline__ int opaque_tid(int wbase) { int t = wbase + lane_id(); asm volatile("" : "+v"(t)); return t; }
; __device__ __forceinline__ int opaque_s(int x) { asm volatile("" : "+s"(x)); return x; }
; __device__ __forceinline__ unsigned cvt_pk_bf16(float lo, float hi) { unsigned r; asm volatile("v_cvt_pk_bf16_f32 %0, %1, %2" : "=v"(r) : "v"(lo), "v"(hi)); return r; }
; #define KIN(i) (kargs()->in[i])
; #define KWS (kargs()->ws)
; #define REP(id) for (int rep_ = 0; rep_ < ((DUP_ID == (id)) ? DUP_N : 1); ++rep_)
; __device__ __forceinline__ void cvt_p_bf16(const f32x4* src, u32x2* dst, int i0, int stride) {
;     constexpr int N4 = M * PLE / 4; int i = i0;
;     for (; i + 3 * stride < N4; i += 4 * stride) { f32x4 v[4];
; #pragma unroll
;         for (int k = 0; k < 4; ++k) v[k] = __builtin_nontemporal_load(src + i + k * stride);
; #pragma unroll
;         for (int k = 0; k < 4; ++k) { u32x2 o; o.x = cvt_pk_bf16(v[k].x, v[k].y); o.y = cvt_pk_bf16(v[k].z, v[k].w); dst[i + k * stride] = o; } }
;     for (; i < N4; i += stride) { const f32x4 v = __builtin_nontemporal_load(src + i); u32x2 o; o.x = cvt_pk_bf16(v.x, v.y); o.y = cvt_pk_bf16(v.z, v.w); dst[i] = o; }
; __global__ void __launch_bounds__(512, 2) mega(Ptrs Pdummy) {
;     ...
;         if (l + 1 < DEPTH) REP(6) { unsigned char* ws = KWS; const f32x4* src = (const f32x4*)(KIN(1) + (size_t)(l + 1) * M * PLE); bf16* PB = (bf16*)(ws + WS_PB);
;             cvt_p_bf16(src, (u32x2*)PB, opaque_s(c) * 512 + opaque_tid(wbase), G * 512); }
.LBB0_633:
	s_add_i32 s1, s95, 1
	s_cmp_eq_u32 s95, 3
	v_writelane_b32 v255, s1, 35
	s_cselect_b64 s[2:3], -1, 0
	v_writelane_b32 v255, s2, 36
	s_cmp_lg_u32 s95, 3
	s_nop 0
	v_writelane_b32 v255, s3, 37
	s_cselect_b64 s[2:3], -1, 0
	v_writelane_b32 v255, s2, 38
	s_and_b64 vcc, exec, s[2:3]
	s_nop 0
	v_writelane_b32 v255, s3, 39
	s_cbranch_vccz .LBB0_642
	s_mov_b64 s[2:3], s[88:89]
	s_mov_b64 s[4:5], s[88:89]
	s_mov_b64 s[2:3], s[100:101]
	s_mov_b32 s1, s92
	s_mov_b32 s6, s38
	s_load_dwordx2 s[4:5], s[4:5], 0x8
	s_waitcnt lgkmcnt(0)
	s_add_u32 s2, s2, 0x12200000
	v_mbcnt_lo_u32_b32 v0, s6, 0
	v_mbcnt_hi_u32_b32 v0, s6, v0
	v_add_u32_e32 v0, s93, v0
	s_mov_b32 s6, 0x200000
	v_lshl_add_u32 v0, s1, 9, v0
	v_readlane_b32 s1, v255, 28
	s_addc_u32 s3, s3, 0
	s_nop 0
	v_add_u32_e32 v1, s1, v0
	v_cmp_gt_i32_e32 vcc, s6, v1
	s_and_saveexec_b64 s[6:7], vcc
	s_cbranch_execz .LBB0_638
	v_readlane_b32 s8, v255, 35
	s_lshl_b32 s8, s8, 23
	s_mov_b32 s9, s40
	s_lshl_b64 s[8:9], s[8:9], 2
	s_add_u32 s8, s4, s8
	v_readlane_b32 s12, v255, 12
	s_addc_u32 s9, s5, s9
	s_mov_b64 s[10:11], 0
	v_readlane_b32 s13, v255, 13
	s_mov_b32 s14, 0x1fffff

; #define LAS __attribute__((address_space(3)))
; __device__ __forceinline__ CJob moe_job(KP P, int j2, int j) {
;     CJob jb; jb.pad = 0; jb.gain = nullptr; jb.mode = 0; jb.fp8 = MOE_FP8 ? 1 : 0; jb.wscale = 1.f; jb.col0 = 0; const int e = j / 3, k = j % 3;
;     if (k < 2) { jb.W = P->in[24 + k] + ((size_t)j2 * NEXP + e) * DM * DFF; jb.gain = P->in[18] + (2 * j2 + 1) * DM; jb.dst = (bf16*)(P->ws + WS_W13E + (size_t)e * 2 * DFF * DM * (MOE_FP8 ? 1 : 2)); jb.K = DM; jb.N = DFF; jb.mode = 4 + k; jb.wscale = MOE_FP8 ? W13_SCALE : 1.f; }
;     else { jb.W = P->in[26] + ((size_t)j2 * NEXP + e) * DFF * DM; jb.dst = (bf16*)(P->ws + WS_W2E + (size_t)e * DM * DFF * (MOE_FP8 ? 1 : 2)); jb.K = DFF; jb.N = DM; jb.wscale = MOE_FP8 ? W2_SCALE : 1.f; }
;     jb.ldw = jb.N;
;     return jb;
; }
; __device__ __forceinline__ void conv_moe_layer(KP P, int j2, LAS float* scr, int gw, int ngw, int lane) {
;     constexpr int IT = (DM / 64) * (DFF / 32), NT = 24 * IT;
;     int fl = gw; if (fl >= NT) return;
;     CJob jb = moe_job(P, j2, fl / IT); f32x4 v[8]; conv_load(jb, fl % IT, lane, v);
;     for (;;) { const int nx = fl + ngw; const bool has = nx < NT; CJob jn = jb; f32x4 w[8];
;         if (has) { jn = moe_job(P, j2, nx / IT); conv_load(jn, nx % IT, lane, w); }
.LBB0_642:
	s_or_b64 s[2:3], s[84:85], s[62:63]
	s_and_b64 vcc, exec, s[2:3]
	s_cbranch_vccnz .LBB0_679
	s_mov_b32 s1, s38
	s_barrier
	s_mov_b64 s[4:5], s[88:89]
	v_mbcnt_lo_u32_b32 v0, s1, 0
	v_mbcnt_hi_u32_b32 v0, s1, v0
	v_add_u32_e32 v0, s93, v0
	s_nop 0
	v_readfirstlane_b32 s1, v0
	s_ashr_i32 s18, s1, 6
	v_readlane_b32 s1, v255, 27
	s_add_i32 s31, s18, s1
	s_cmp_gt_i32 s31, 0xa7ff
	s_cbranch_scc1 .LBB0_679
	s_mul_hi_i32 s1, s31, 0x92492493
	s_lshr_b32 s2, s95, 1
	s_mov_b32 s3, s40
	s_add_i32 s1, s1, s31
	s_lshl_b64 s[6:7], s[2:3], 3
	s_lshr_b32 s3, s1, 31
	s_ashr_i32 s19, s1, 10
	s_add_i32 s19, s19, s3
	s_mul_hi_i32 s1, s31, 0x30c30c31
	s_lshr_b32 s3, s1, 31
	s_ashr_i32 s20, s1, 10
	s_mul_hi_i32 s1, s19, 0x55555556
	s_add_i32 s20, s20, s3
	s_lshr_b32 s3, s1, 31
	s_add_i32 s1, s1, s3
	s_mul_i32 s1, s1, 3
	s_sub_i32 s14, s19, s1
	s_cmp_gt_i32 s14, 1
	s_mov_b64 s[16:17], -1
	s_cbranch_scc0 .LBB0_646
	s_ashr_i32 s1, s20, 31
	s_load_dwordx2 s[8:9], s[4:5], 0xd0
	s_mov_b64 s[12:13], s[100:101]
	s_add_u32 s3, s6, s20
	s_addc_u32 s1, s7, s1
	s_mul_i32 s1, s1, 0xe00000
	s_mul_hi_u32 s10, s3, 0xe00000
	s_add_i32 s1, s10, s1
	s_mul_i32 s3, s3, 0xe00000
	s_waitcnt lgkmcnt(0)
	s_add_u32 s10, s8, s3
	s_addc_u32 s11, s9, s1
	s_mul_i32 s3, s20, 0x380000
	s_mul_hi_i32 s1, s20, 0x380000
	s_add_u32 s3, s12, s3
	s_addc_u32 s1, s13, s1
	s_add_u32 s12, s3, 0xea00000
	s_addc_u32 s13, s1, 0
	s_mov_b64 s[16:17], 0
.LBB0_646:
	s_lshl_b32 s8, s2, 11
	s_mov_b32 s9, s40
	s_mul_hi_u32 s1, s2, 0x7000000
	s_andn2_b64 vcc, exec, s[16:17]
	s_mul_i32 s22, s2, 0x7000000
	s_cbranch_vccnz .LBB0_648
	s_ashr_i32 s15, s14, 31
	s_lshl_b64 s[2:3], s[14:15], 3
	s_add_u32 s2, s4, s2
	s_addc_u32 s3, s5, s3
	s_load_dwordx2 s[2:3], s[2:3], 0xc0
	s_mul_i32 s11, s20, 0xe00000
	s_mul_hi_i32 s10, s20, 0xe00000
	s_mul_hi_i32 s15, s20, 0x700000
	s_mul_i32 s20, s20, 0x700000
	s_waitcnt lgkmcnt(0)
	s_add_u32 s2, s2, s11
	s_addc_u32 s3, s3, s10
	s_add_u32 s10, s2, s22
	s_addc_u32 s11, s3, s1
	s_load_dwordx2 s[2:3], s[4:5], 0x90
	s_lshl_b64 s[12:13], s[8:9], 2
	s_mov_b32 s24, 0x42800000
	s_movk_i32 s33, 0xe00
	s_movk_i32 s23, 0x400
	s_waitcnt lgkmcnt(0)
	s_add_u32 s2, s2, s12
	s_addc_u32 s3, s3, s13
	s_mov_b64 s[12:13], s[100:101]
	s_add_u32 s2, s2, 0x1000
	s_addc_u32 s3, s3, 0
	s_waitcnt lgkmcnt(0)
	s_add_u32 s12, s12, s20
	s_addc_u32 s13, s13, s15
	s_add_u32 s12, s12, 0x7a00000
	s_addc_u32 s13, s13, 0
	s_add_i32 s30, s14, 4
	s_branch .LBB0_649

; #define LAS __attribute__((address_space(3)))
; __device__ __forceinline__ CJob moe_job(KP P, int j2, int j) {
;     CJob jb; jb.pad = 0; jb.gain = nullptr; jb.mode = 0; jb.fp8 = MOE_FP8 ? 1 : 0; jb.wscale = 1.f; jb.col0 = 0; const int e = j / 3, k = j % 3;
;     if (k < 2) { jb.W = P->in[24 + k] + ((size_t)j2 * NEXP + e) * DM * DFF; jb.gain = P->in[18] + (2 * j2 + 1) * DM; jb.dst = (bf16*)(P->ws + WS_W13E + (size_t)e * 2 * DFF * DM * (MOE_FP8 ? 1 : 2)); jb.K = DM; jb.N = DFF; jb.mode = 4 + k; jb.wscale = MOE_FP8 ? W13_SCALE : 1.f; }
;     else { jb.W = P->in[26] + ((size_t)j2 * NEXP + e) * DFF * DM; jb.dst = (bf16*)(P->ws + WS_W2E + (size_t)e * DM * DFF * (MOE_FP8 ? 1 : 2)); jb.K = DFF; jb.N = DM; jb.wscale = MOE_FP8 ? W2_SCALE : 1.f; }
;     jb.ldw = jb.N;
;     return jb;
; }
; __device__ __forceinline__ void conv_moe_layer(KP P, int j2, LAS float* scr, int gw, int ngw, int lane) {
;     constexpr int IT = (DM / 64) * (DFF / 32), NT = 24 * IT;
;     int fl = gw; if (fl >= NT) return;
;     CJob jb = moe_job(P, j2, fl / IT); f32x4 v[8]; conv_load(jb, fl % IT, lane, v);
;     for (;;) { const int nx = fl + ngw; const bool has = nx < NT; CJob jn = jb; f32x4 w[8];
;         if (has) { jn = moe_job(P, j2, nx / IT); conv_load(jn, nx % IT, lane, w); }
.LBB0_651:
	s_add_i32 s25, s31, s94
	s_cmp_lt_i32 s25, 0xa800
	s_cselect_b64 s[18:19], -1, 0
	s_cmp_gt_i32 s25, 0xa7ff
	s_cbranch_scc1 .LBB0_658
	s_mul_hi_i32 s10, s25, 0x92492493
	s_add_i32 s10, s10, s25
	s_lshr_b32 s11, s10, 31
	s_ashr_i32 s34, s10, 10
	s_add_i32 s34, s34, s11
	s_mul_hi_i32 s10, s25, 0x30c30c31
	s_lshr_b32 s11, s10, 31
	s_ashr_i32 s26, s10, 10
	s_mul_hi_i32 s10, s34, 0x55555556
	s_add_i32 s26, s26, s11
	s_lshr_b32 s11, s10, 31
	s_add_i32 s10, s10, s11
	s_mul_i32 s10, s10, 3
	s_sub_i32 s20, s34, s10
	s_cmp_gt_i32 s20, 1
	s_mov_b64 s[14:15], -1
	s_cbranch_scc0 .LBB0_654
	s_ashr_i32 s10, s26, 31
	s_add_u32 s14, s6, s26
	s_addc_u32 s10, s7, s10
	s_mul_i32 s15, s10, 0xe00000
	s_load_dwordx2 s[10:11], s[4:5], 0xd0
	s_mul_hi_u32 s16, s14, 0xe00000
	s_add_i32 s16, s16, s15
	s_mul_i32 s17, s14, 0xe00000
	s_mov_b64 s[14:15], s[100:101]
	s_waitcnt lgkmcnt(0)
	s_add_u32 s10, s10, s17
	s_addc_u32 s11, s11, s16
	s_mul_i32 s17, s26, 0x380000
	s_mul_hi_i32 s16, s26, 0x380000
	s_add_u32 s14, s14, s17
	s_addc_u32 s15, s15, s16
	s_add_u32 s16, s14, 0xea00000
	s_addc_u32 s17, s15, 0
	s_mov_b64 s[14:15], 0
.LBB0_654:
	s_andn2_b64 vcc, exec, s[14:15]
	s_cbranch_vccnz .LBB0_656
	s_ashr_i32 s21, s20, 31
	s_lshl_b64 s[10:11], s[20:21], 3
	s_add_u32 s10, s4, s10
	s_addc_u32 s11, s5, s11
	s_load_dwordx2 s[10:11], s[10:11], 0xc0
	s_mul_i32 s15, s26, 0xe00000
	s_mul_hi_i32 s14, s26, 0xe00000
	s_mul_hi_i32 s21, s26, 0x700000
	s_mul_i32 s26, s26, 0x700000
	s_waitcnt lgkmcnt(0)
	s_add_u32 s10, s10, s15
	s_addc_u32 s11, s11, s14
	s_load_dwordx2 s[14:15], s[4:5], 0x90
	s_add_u32 s10, s10, s22
	s_addc_u32 s11, s11, s1
	s_lshl_b64 s[16:17], s[8:9], 2
	s_mov_b32 s27, 0x42800000
	s_waitcnt lgkmcnt(0)
	s_add_u32 s14, s14, s16
	s_addc_u32 s15, s15, s17
	s_mov_b64 s[16:17], s[100:101]
	s_add_u32 s14, s14, 0x1000
	s_addc_u32 s15, s15, 0
	s_movk_i32 s28, 0xe00
	s_movk_i32 s29, 0x400
	s_waitcnt lgkmcnt(0)
	s_add_u32 s16, s16, s26
	s_addc_u32 s17, s17, s21
	s_add_u32 s16, s16, 0x7a00000
	s_addc_u32 s17, s17, 0
	s_add_i32 s26, s20, 4
	s_branch .LBB0_657

; __device__ __forceinline__ unsigned xb_ld(unsigned* p)              { return __hip_atomic_load(p, __ATOMIC_RELAXED, __HIP_MEMORY_SCOPE_AGENT); }
; __device__ __forceinline__ void xcd_barrier_complete(unsigned* bar, unsigned x, unsigned& nloc, unsigned& nx) {
;     const unsigned G = gridDim.x * gridDim.y * gridDim.z;
;     unsigned sum, cnt, mine, sp = 0u;
;     for (;;) {
;         sum = 0u; cnt = 0u; mine = 0u;
; #pragma unroll
;         for (unsigned j = 0; j < 16; ++j) { const unsigned c = xb_ld(&bar[XB_XCNT(j)]); sum += c; cnt += (c > 0u) ? 1u : 0u; mine = (j == x) ? c : mine; }
; __device__ __forceinline__ void xcd_barrier(const XcdBarrier& b, bool leader) {
;     asm volatile("s_waitcnt vmcnt(0)" ::: "memory");
;     __syncthreads();
;     if (leader) {
;         unsigned zo_; asm volatile("v_mov_b32 %0, 0" : "=v"(zo_)); unsigned* bar = b.bar + zo_;
;         __builtin_amdgcn_s_waitcnt(0);
;         unsigned nloc = b.st[0], nx = b.st[1];
;         if (nloc == 0u) { xcd_barrier_complete(bar, b.x, nloc, nx); b.st[0] = nloc; b.st[1] = nx; }
.Lbinv_skip_2:
	s_and_saveexec_b64 s[36:37], vcc
	s_cbranch_execz .LBB0_723
	s_mov_b64 s[2:3], s[100:101]
	v_mov_b32 v232, 0
	s_waitcnt vmcnt(0) expcnt(0) lgkmcnt(0)
	s_and_b32 s1, s1, 15
	v_lshl_add_u64 v[0:1], v[232:233], 2, s[2:3]
	s_mov_b64 s[2:3], 0x4000
	v_lshl_add_u64 v[0:1], v[0:1], 0, s[2:3]
	v_readlane_b32 s2, v255, 7
	s_nop 1
	v_mov_b32_e32 v2, s2
	ds_read_b32 v6, v2
	v_readlane_b32 s2, v255, 8
	s_waitcnt lgkmcnt(0)
	v_cmp_ne_u32_e32 vcc, 0, v6
	v_mov_b32_e32 v2, s2
	ds_read_b32 v4, v2
	s_cbranch_vccnz .LBB0_694
	v_readlane_b32 s4, v255, 0
	v_readlane_b32 s5, v255, 1
	s_load_dwordx2 s[2:3], s[4:5], 0x4
	s_mov_b64 s[4:5], 0x1100
	s_waitcnt lgkmcnt(0)
	v_lshl_add_u64 v[4:5], v[0:1], 0, s[4:5]
	s_mov_b64 s[4:5], 0x1200
	v_lshl_add_u64 v[6:7], v[0:1], 0, s[4:5]
	s_mov_b64 s[4:5], 0x1300
	v_lshl_add_u64 v[8:9], v[0:1], 0, s[4:5]
	v_readlane_b32 s4, v255, 4
	s_mul_i32 s20, s2, s4
	v_lshl_add_u64 v[2:3], v[0:1], 0, s[72:73]
	v_readlane_b32 s5, v255, 5
	s_mul_i32 s20, s20, s3
	s_mov_b32 s21, 1
	s_mov_b64 s[2:3], 0
	s_branch .LBB0_684

; __device__ __forceinline__ int opaque_tid(int wbase) { int t = wbase + lane_id(); asm volatile("" : "+v"(t)); return t; }
; __device__ __forceinline__ int opaque_s(int x) { asm volatile("" : "+s"(x)); return x; }
; #define KWS (kargs()->ws)
; template <bool F8> __device__ __forceinline__ void lru_apply(const bf16* U, const bf16* HR, const bf16* PQ, const float* AGG, bf16* YB, int G, int c, int wbase) {
;     const int tid = opaque_tid(wbase); G = opaque_s(G); c = opaque_s(c); const int ch = 8 * (tid & 127), tq = tid >> 7;
;     for (int cu = c; cu < BATCH * NCK; cu += G) { const int b = cu / NCK, ck = cu % NCK;
;         f32x4 c0 = {}, c1 = {};
;         int j = 0;
;         for (; j + 8 <= ck; j += 8) { f32x4 p[8][4];
; #pragma unroll
;             for (int k = 0; k < 8; ++k) { const f32x4* ap = (const f32x4*)(AGG + ((size_t)(b * NCK + j + k) * DM + ch) * 2); p[k][0] = ap[0]; p[k][1] = ap[1]; p[k][2] = ap[2]; p[k][3] = ap[3]; }
; #pragma unroll
;             for (int k = 0; k < 8; ++k) { c0 = (f32x4){p[k][0].x * c0.x + p[k][0].y, p[k][0].z * c0.y + p[k][0].w, p[k][1].x * c0.z + p[k][1].y, p[k][1].z * c0.w + p[k][1].w};
;                                           c1 = (f32x4){p[k][2].x * c1.x + p[k][2].y, p[k][2].z * c1.y + p[k][2].w, p[k][3].x * c1.z + p[k][3].y, p[k][3].z * c1.w + p[k][3].w}; } }
;         for (; j < ck; ++j) { const f32x4* ap = (const f32x4*)(AGG + ((size_t)(b * NCK + j) * DM + ch) * 2); const f32x4 p0 = ap[0], p1 = ap[1], p2 = ap[2], p3 = ap[3];
;             c0 = (f32x4){p0.x * c0.x + p0.y, p0.z * c0.y + p0.w, p1.x * c0.z + p1.y, p1.z * c0.w + p1.w}; c1 = (f32x4){p2.x * c1.x + p2.y, p2.z * c1.y + p2.w, p3.x * c1.z + p3.y, p3.z * c1.w + p3.w}; }
; __global__ void __launch_bounds__(512, 2) mega(Ptrs Pdummy) {
;     ...
;         if ((MERGE_FP8_MASK >> opaque_s(l)) & 1) { unsigned char* ws = KWS; lru::lru_apply<true>((const bf16*)(ws + WS_R + R_U), (const bf16*)(ws + WS_R + R_HR), (const bf16*)(ws + WS_R + R_PQ), (const float*)(ws + WS_AGG), (bf16*)(ws + WS_R + R_YB), G, c, wbase); }
.LBB0_723:
	s_or_b64 exec, exec, s[36:37]
	s_mov_b32 s1, s95
	s_waitcnt lgkmcnt(0)
	s_barrier
	s_lshl_b32 s1, 1, s1
	s_and_b32 s1, s1, 14
	s_cmp_eq_u32 s1, 0
	s_cbranch_scc1 .LBB0_737
	s_mov_b64 s[2:3], s[88:89]
	s_mov_b32 s1, s38
	v_readlane_b32 s4, v255, 4
	v_mbcnt_lo_u32_b32 v0, s1, 0
	v_mbcnt_hi_u32_b32 v0, s1, v0
	v_add_u32_e32 v0, s93, v0
	s_mov_b32 s1, s4
	s_mov_b32 s8, s92
	s_cmpk_gt_i32 s8, 0xff
	v_readlane_b32 s5, v255, 5
	s_cbranch_scc1 .LBB0_736
	s_mov_b64 s[2:3], s[100:101]
	v_and_b32_e32 v2, 0x7f, v0
	v_lshlrev_b32_e32 v1, 3, v0
	v_lshlrev_b32_e32 v232, 6, v2
	v_ashrrev_i32_e32 v53, 7, v0
	v_and_b32_e32 v52, 0x3f8, v1
	s_waitcnt lgkmcnt(0)
	v_lshl_add_u64 v[0:1], s[2:3], 0, v[232:233]
	s_mov_b64 s[4:5], 0x1760e030
	v_lshl_add_u64 v[54:55], v[0:1], 0, s[4:5]
	s_mov_b64 s[4:5], 0x17600000
	v_lshl_add_u64 v[56:57], v[0:1], 0, s[4:5]
	v_lshlrev_b32_e32 v58, 4, v2

; __device__ __forceinline__ int opaque_tid(int wbase) { int t = wbase + lane_id(); asm volatile("" : "+v"(t)); return t; }
; __device__ __forceinline__ int opaque_s(int x) { asm volatile("" : "+s"(x)); return x; }
; #define KWS (kargs()->ws)
; #define REP(id) for (int rep_ = 0; rep_ < ((DUP_ID == (id)) ? DUP_N : 1); ++rep_)
; template <bool F8> __device__ __forceinline__ void lru_apply(const bf16* U, const bf16* HR, const bf16* PQ, const float* AGG, bf16* YB, int G, int c, int wbase) {
;     const int tid = opaque_tid(wbase); G = opaque_s(G); c = opaque_s(c); const int ch = 8 * (tid & 127), tq = tid >> 7;
;     for (int cu = c; cu < BATCH * NCK; cu += G) { const int b = cu / NCK, ck = cu % NCK;
;         f32x4 c0 = {}, c1 = {};
;         int j = 0;
;         for (; j + 8 <= ck; j += 8) { f32x4 p[8][4];
; #pragma unroll
;             for (int k = 0; k < 8; ++k) { const f32x4* ap = (const f32x4*)(AGG + ((size_t)(b * NCK + j + k) * DM + ch) * 2); p[k][0] = ap[0]; p[k][1] = ap[1]; p[k][2] = ap[2]; p[k][3] = ap[3]; }
; #pragma unroll
;             for (int k = 0; k < 8; ++k) { c0 = (f32x4){p[k][0].x * c0.x + p[k][0].y, p[k][0].z * c0.y + p[k][0].w, p[k][1].x * c0.z + p[k][1].y, p[k][1].z * c0.w + p[k][1].w};
;                                           c1 = (f32x4){p[k][2].x * c1.x + p[k][2].y, p[k][2].z * c1.y + p[k][2].w, p[k][3].x * c1.z + p[k][3].y, p[k][3].z * c1.w + p[k][3].w}; } }
;         for (; j < ck; ++j) { const f32x4* ap = (const f32x4*)(AGG + ((size_t)(b * NCK + j) * DM + ch) * 2); const f32x4 p0 = ap[0], p1 = ap[1], p2 = ap[2], p3 = ap[3];
;             c0 = (f32x4){p0.x * c0.x + p0.y, p0.z * c0.y + p0.w, p1.x * c0.z + p1.y, p1.z * c0.w + p1.w}; c1 = (f32x4){p2.x * c1.x + p2.y, p2.z * c1.y + p2.w, p3.x * c1.z + p3.y, p3.z * c1.w + p3.w}; }
; __global__ void __launch_bounds__(512, 2) mega(Ptrs Pdummy) {
;     ...
;         else REP(8) { unsigned char* ws = KWS; lru::lru_apply<false>((const bf16*)(ws + WS_R + R_U), (const bf16*)(ws + WS_R + R_HR), (const bf16*)(ws + WS_R + R_PQ), (const float*)(ws + WS_AGG), (bf16*)(ws + WS_R + R_YB), G, c, wbase); }
.LBB0_737:
.LBB0_738:
	s_mov_b64 s[2:3], s[88:89]
	s_mov_b32 s1, s38
	v_readlane_b32 s4, v255, 4
	v_mbcnt_lo_u32_b32 v0, s1, 0
	v_mbcnt_hi_u32_b32 v0, s1, v0
	v_add_u32_e32 v0, s93, v0
	s_mov_b32 s1, s4
	s_mov_b32 s8, s92
	s_cmpk_gt_i32 s8, 0xff
	v_readlane_b32 s5, v255, 5
	s_cbranch_scc1 .LBB0_750
	s_mov_b64 s[2:3], s[100:101]
	v_and_b32_e32 v2, 0x7f, v0
	v_lshlrev_b32_e32 v232, 6, v2
	s_waitcnt vmcnt(22)
	v_ashrrev_i32_e32 v66, 7, v0
	s_mov_b64 s[4:5], 0x1760e030
	s_waitcnt lgkmcnt(0)
	v_lshl_add_u64 v[0:1], s[2:3], 0, v[232:233]
	v_lshl_add_u64 v[52:53], v[0:1], 0, s[4:5]
	s_mov_b64 s[4:5], 0x17600000
	v_lshl_add_u64 v[54:55], v[0:1], 0, s[4:5]
	v_lshlrev_b32_e32 v232, 4, v2

; __device__ __forceinline__ int opaque_s(int x) { asm volatile("" : "+s"(x)); return x; }
; #define KWS (kargs()->ws)
; #define REP(id) for (int rep_ = 0; rep_ < ((DUP_ID == (id)) ? DUP_N : 1); ++rep_)
; __global__ void __launch_bounds__(512, 2) mega(Ptrs Pdummy) {
;     ...
;         {
;         if ((MERGE_FP8_MASK >> opaque_s(l)) & 1) {
;           REP(9) { unsigned char* ws = KWS; pg8::Gemm g{(const bf16*)(ws + WS_R + R_YA), (const bf16*)(ws + WS_WPA) + (size_t)l * DM * DM, DM / 2, 0};
;             pg8::MergeOrder S; S.A1 = (const bf16*)(ws + WS_R + R_YB); S.Bt1 = (const bf16*)(ws + WS_WPB) + (size_t)l * DM * DM; S.so.init(M, DM, opaque_s(G), opaque_s(c));
;             pg8::EpiMerge<true> E{(bf16*)(ws + WS_R + R_MB), (const bf16*)(ws + WS_R + R_U), MB8_SCALE / (WIN_SCALE * Y8_SCALE), 0}; pg8::gemm_phase<pg8::EpiMerge<true>, pg8::MergeOrder, true, true, true>(lds, g, S, E, wbase); }
;         } else if ((OUT_FP8_MASK & ~MERGE_FP8_MASK) != 0 && ((OUT_FP8_MASK >> opaque_s(l)) & 1)) { unsigned char* ws = KWS; pg8::Gemm g{(const bf16*)(ws + WS_R + R_YA), (const bf16*)(ws + WS_WPA) + (size_t)l * DM * DM, DM, 0};
;           pg8::MergeOrder S; S.A1 = (const bf16*)(ws + WS_R + R_YB); S.Bt1 = (const bf16*)(ws + WS_WPB) + (size_t)l * DM * DM; S.so.init(M, DM, opaque_s(G), opaque_s(c));
;           pg8::EpiMerge<true> E{(bf16*)(ws + WS_R + R_MB), (const bf16*)(ws + WS_R + R_U), MB8_SCALE, 0}; pg8::gemm_phase<pg8::EpiMerge<true>, pg8::MergeOrder, true, true>(lds, g, S, E, wbase); }
;         else
;         REP(9) { unsigned char* ws = KWS; pg8::Gemm g{(const bf16*)(ws + WS_R + R_YA), (const bf16*)(ws + WS_WPA) + (size_t)l * DM * DM, DM, 0};
;           pg8::MergeOrder S; S.A1 = (const bf16*)(ws + WS_R + R_YB); S.Bt1 = (const bf16*)(ws + WS_WPB) + (size_t)l * DM * DM; S.so.init(M, DM, opaque_s(G), opaque_s(c));
;           pg8::EpiMerge<false> E{(bf16*)(ws + WS_R + R_MB), (const bf16*)(ws + WS_R + R_U), 1.f, 0}; pg8::gemm_phase<pg8::EpiMerge<false>, pg8::MergeOrder, true, true>(lds, g, S, E, wbase); }
.LBB0_798:
	s_mov_b64 s[10:11], s[100:101]
	s_andn2_b64 vcc, exec, s[4:5]
	s_ashr_i32 s3, s7, 3
	s_cbranch_vccnz .LBB0_800
	s_mul_i32 s8, s6, 0x41

; #define PG8_BAR __builtin_amdgcn_s_barrier()
; template <class Epi, class Sched, bool ALIGN_EPI = false, bool SP2 = false, bool FP8 = false>
; __device__ __forceinline__ void gemm_phase(LAS unsigned char* lds, const Gemm g, const Sched& S, const Epi& E, int wbase) {
;     const int tid = opaque_tid(wbase), wid = __builtin_amdgcn_readfirstlane(tid >> 6), lane = tid & 63, wr = wid >> 2, wc = wid & 3, fr = lane & 15, fq = lane >> 4;
;     const int K = opaque_s(g.K), nt = K / BK;
;     unsigned voffA[2], voffB[2];
; #pragma unroll
;     for (int i = 0; i < 2; ++i) { int R, C; stage_rc(tid * 16 + i * 8192, R, C); const int Rb = Epi::PERM ? ((R & ~31) + perm32(R & 31)) : R;
;         voffA[i] = (unsigned)(R * K + C) * 2u; voffB[i] = (unsigned)(Rb * K + C) * 2u; }
;     const unsigned kstep = (unsigned)(BK * 2);
;     const unsigned hstep = (unsigned)HALF * (unsigned)K * 2u;
;     typedef __amdgpu_buffer_rsrc_t rsrc_t;
;     const rsrc_t rA0 = __builtin_amdgcn_make_buffer_rsrc((void*)g.A, 0, 0xffffffff, 0x00020000), rB0 = __builtin_amdgcn_make_buffer_rsrc((void*)g.Bt, 0, 0xffffffff, 0x00020000);
;     rsrc_t rA1 = rA0, rB1 = rB0;
;     if constexpr (Sched::TWO) { rA1 = __builtin_amdgcn_make_buffer_rsrc((void*)S.A1, 0, 0xffffffff, 0x00020000); rB1 = __builtin_amdgcn_make_buffer_rsrc((void*)S.Bt1, 0, 0xffffffff, 0x00020000); }
;     const unsigned ldsw = (unsigned)wid * 1024u;
;     const int aoff = lds_byte(wr * 64 + fr, fq * 8), boff = lds_byte(wc * 32 + fr, fq * 8);
;     ...
;     Unit cur, nxt; int ui = 0;
;     if (!S.next(0, cur)) return;
;     f32x4 acc[2][2][4][2];
;     ...
;     PG8_ZERO_ACC();
;     v8i_t At[4], B0[2], B1[2];
;     unsigned cA = S.a_off(cur, g), cB = S.b_off(cur, g); rsrc_t rAc = (Sched::TWO && cur.part) ? rA1 : rA0, rBc = (Sched::TWO && cur.part) ? rB1 : rB0;
;     S.a_ready(cur);
;     if constexpr (SP2) {
;         PG8_STAGE(PG8_SB(0, 0), rBc, cB, voffB); PG8_STAGE(PG8_SB(0, 1), rBc, cB + hstep, voffB); PG8_STAGE(PG8_SA(0, 0), rAc, cA, voffA); PG8_STAGE(PG8_SA(0, 1), rAc, cA + hstep, voffA);
;         if (wr == 1) PG8_BAR;
; __global__ void __launch_bounds__(512, 2) mega(Ptrs Pdummy) {
;     ...
;         if ((OUT_FP8_MASK >> opaque_s(l)) & 1) { unsigned char* ws = KWS; pg8::Gemm g{(const bf16*)(ws + WS_R + R_MB), (const bf16*)(ws + WS_WOUT) + (size_t)l * DM * DM, DM / 2, 0}; pg8::StaticOrder S; S.init(M, DM, opaque_s(G), opaque_s(c));
.LBB0_912:
	s_mov_b64 s[2:3], s[100:101]
	s_andn2_b64 vcc, exec, s[4:5]
	s_cbranch_vccnz .LBB0_983
	v_bfe_i32 v2, v4, 27, 1
	v_lshlrev_b32_e32 v0, 4, v4
	v_lshrrev_b32_e32 v2, 22, v2
	v_add_u32_e32 v2, v0, v2
	v_and_b32_e32 v2, 0xfffffc00, v2
	v_sub_u32_e32 v2, v0, v2
	v_lshrrev_b32_e32 v3, 4, v2
	v_ashrrev_i32_e32 v1, 31, v4
	v_bitop3_b32 v3, v3, v2, 32 bitop3:0x6c
	v_ashrrev_i32_e32 v2, 31, v2
	v_lshrrev_b32_e32 v1, 26, v1
	v_lshrrev_b32_e32 v2, 26, v2
	s_waitcnt lgkmcnt(0)
	s_add_u32 s36, s2, 0x3d800000
	v_readlane_b32 s5, v255, 40
	v_add_u32_e32 v1, v4, v1
	v_add_u32_e32 v2, v3, v2
	s_addc_u32 s4, s3, 0
	s_lshl_b32 s5, s5, 1
	v_ashrrev_i32_e32 v1, 6, v1
	v_ashrrev_i32_e32 v2, 6, v2
	s_add_u32 s5, s2, s5
	v_lshlrev_b32_e32 v5, 3, v1
	v_mul_i32_i24_e32 v6, 64, v2
	s_addc_u32 s6, s3, 0
	v_and_b32_e32 v5, -16, v5
	v_lshlrev_b32_e32 v1, 5, v1
	v_sub_u32_e32 v3, v3, v6
	s_add_u32 s12, s5, 0x3d00000
	v_add_u32_e32 v5, v2, v5
	v_and_b32_e32 v1, 32, v1
	v_ashrrev_i16_sdwa v3, v231, sext(v3) dst_sel:DWORD dst_unused:UNUSED_PAD src0_sel:DWORD src1_sel:BYTE_0
	s_addc_u32 s5, s6, 0
	v_add_u32_sdwa v1, v1, sext(v3) dst_sel:DWORD dst_unused:UNUSED_PAD src0_sel:DWORD src1_sel:WORD_0
	v_lshlrev_b32_e32 v3, 1, v5
	v_lshrrev_b32_e32 v6, 2, v5
	v_and_b32_e32 v2, 3, v2
	s_mov_b32 s6, 0x7fffffe0
	v_and_b32_e32 v3, 24, v3
	v_and_b32_e32 v6, 4, v6
	v_and_or_b32 v2, v5, s6, v2
	v_or3_b32 v2, v2, v6, v3
	v_mul_lo_u32 v3, v5, s21
	v_mul_lo_u32 v2, v2, s21
	v_add_u32_e32 v0, 0x2000, v0
	v_add_lshl_u32 v222, v1, v3, 1
	v_add_lshl_u32 v223, v2, v1, 1
	v_ashrrev_i32_e32 v1, 31, v0
	v_lshrrev_b32_e32 v1, 22, v1
	v_add_u32_e32 v1, v0, v1
	v_ashrrev_i32_e32 v1, 10, v1
	v_mul_i32_i24_e32 v2, 0x400, v1
	v_sub_u32_e32 v0, v0, v2
	v_lshrrev_b32_e32 v2, 4, v0
	v_bitop3_b32 v0, v2, v0, 32 bitop3:0x6c
	v_ashrrev_i32_e32 v3, 31, v0
	v_lshrrev_b32_e32 v3, 26, v3
	v_add_u32_e32 v3, v0, v3
	v_lshlrev_b32_e32 v2, 3, v1
	v_ashrrev_i32_e32 v5, 6, v3
	v_and_b32_e32 v3, 0xc0, v3
	v_and_b32_e32 v2, -16, v2
	v_lshlrev_b32_e32 v1, 5, v1
	v_sub_u32_e32 v0, v0, v3
	s_ashr_i32 s20, s11, 6
	v_add_u32_e32 v2, v5, v2
	v_and_b32_e32 v1, 32, v1
	v_ashrrev_i16_sdwa v0, v231, sext(v0) dst_sel:DWORD dst_unused:UNUSED_PAD src0_sel:DWORD src1_sel:BYTE_0
	v_add_u32_sdwa v0, v1, sext(v0) dst_sel:DWORD dst_unused:UNUSED_PAD src0_sel:DWORD src1_sel:WORD_0
	v_lshlrev_b32_e32 v1, 1, v2
	v_lshrrev_b32_e32 v3, 2, v2
	v_and_b32_e32 v5, 3, v5
	s_and_b32 s37, s4, 0xffff
	s_lshl_b32 s4, s20, 10
	v_and_b32_e32 v1, 24, v1
	v_and_b32_e32 v3, 4, v3
	v_and_or_b32 v5, v2, s6, v5
	s_add_i32 s31, s4, 0
	v_or3_b32 v1, v5, v3, v1
	s_add_i32 s33, s31, 0x10000
	v_mul_lo_u32 v2, v2, s21
	v_mul_lo_u32 v1, v1, s21
	s_and_b32 s13, s5, 0xffff
	s_mov_b32 s14, s38
	s_mov_b32 s15, s39
	s_lshl_b32 s5, s29, 18
	s_mov_b32 m0, s33
	s_add_i32 s34, s31, 0x12000
	v_add_lshl_u32 v156, v0, v2, 1
	v_add_lshl_u32 v157, v1, v0, 1
	s_lshl_b32 s30, s21, 8
	v_mov_b32 v0, 0
	buffer_load_dwordx4 v223, s[12:15], s5 offen lds
	s_mov_b32 m0, s34
	s_add_i32 s35, s31, 0x14000
	buffer_load_dwordx4 v157, s[12:15], s5 offen lds
	s_add_i32 s23, s5, s30
	s_mov_b32 m0, s35
	s_add_i32 s41, s31, 0x16000
	buffer_load_dwordx4 v223, s[12:15], s23 offen lds
	s_mov_b32 m0, s41
	s_lshl_b32 s4, s10, 18
	buffer_load_dwordx4 v157, s[12:15], s23 offen lds
	s_mov_b32 m0, s31
	s_add_i32 s42, s31, 0x2000
	buffer_load_dwordx4 v222, s[36:39], s4 offen lds
	s_mov_b32 m0, s42
	s_add_i32 s43, s31, 0x4000
	buffer_load_dwordx4 v156, s[36:39], s4 offen lds
	s_add_i32 s6, s4, s30
	s_mov_b32 m0, s43
	s_add_i32 s44, s31, 0x6000
	buffer_load_dwordx4 v222, s[36:39], s6 offen lds
	s_mov_b32 m0, s44
	s_ashr_i32 s22, s11, 8
	buffer_load_dwordx4 v156, s[36:39], s6 offen lds
	s_cmp_eq_u32 s22, 1
	s_cselect_b64 s[6:7], -1, 0
	s_cmp_lg_u32 s22, 1
	s_cbranch_scc1 .LBB0_915
	s_barrier

; #define KWS (kargs()->ws)
; template <class Epi, class Sched, bool ALIGN_EPI = false, bool SP2 = false, bool FP8 = false>
; __device__ __forceinline__ void gemm_phase(LAS unsigned char* lds, const Gemm g, const Sched& S, const Epi& E, int wbase) {
;     const int tid = opaque_tid(wbase), wid = __builtin_amdgcn_readfirstlane(tid >> 6), lane = tid & 63, wr = wid >> 2, wc = wid & 3, fr = lane & 15, fq = lane >> 4;
;     const int K = opaque_s(g.K), nt = K / BK;
;     unsigned voffA[2], voffB[2];
; #pragma unroll
;     for (int i = 0; i < 2; ++i) { int R, C; stage_rc(tid * 16 + i * 8192, R, C); const int Rb = Epi::PERM ? ((R & ~31) + perm32(R & 31)) : R;
;         voffA[i] = (unsigned)(R * K + C) * 2u; voffB[i] = (unsigned)(Rb * K + C) * 2u; }
;     const unsigned kstep = (unsigned)(BK * 2);
;     const unsigned hstep = (unsigned)HALF * (unsigned)K * 2u;
;     typedef __amdgpu_buffer_rsrc_t rsrc_t;
;     const rsrc_t rA0 = __builtin_amdgcn_make_buffer_rsrc((void*)g.A, 0, 0xffffffff, 0x00020000), rB0 = __builtin_amdgcn_make_buffer_rsrc((void*)g.Bt, 0, 0xffffffff, 0x00020000);
;     rsrc_t rA1 = rA0, rB1 = rB0;
;     if constexpr (Sched::TWO) { rA1 = __builtin_amdgcn_make_buffer_rsrc((void*)S.A1, 0, 0xffffffff, 0x00020000); rB1 = __builtin_amdgcn_make_buffer_rsrc((void*)S.Bt1, 0, 0xffffffff, 0x00020000); }
;     const unsigned ldsw = (unsigned)wid * 1024u;
;     const int aoff = lds_byte(wr * 64 + fr, fq * 8), boff = lds_byte(wc * 32 + fr, fq * 8);
;     ...
;     Unit cur, nxt; int ui = 0;
;     if (!S.next(0, cur)) return;
;     f32x4 acc[2][2][4][2];
;     ...
;     PG8_ZERO_ACC();
;     v8i_t At[4], B0[2], B1[2];
;     unsigned cA = S.a_off(cur, g), cB = S.b_off(cur, g); rsrc_t rAc = (Sched::TWO && cur.part) ? rA1 : rA0, rBc = (Sched::TWO && cur.part) ? rB1 : rB0;
;     S.a_ready(cur);
;     if constexpr (SP2) {
;         PG8_STAGE(PG8_SB(0, 0), rBc, cB, voffB); PG8_STAGE(PG8_SB(0, 1), rBc, cB + hstep, voffB); PG8_STAGE(PG8_SA(0, 0), rAc, cA, voffA); PG8_STAGE(PG8_SA(0, 1), rAc, cA + hstep, voffA);
;         if (wr == 1) PG8_BAR;
; __global__ void __launch_bounds__(512, 2) mega(Ptrs Pdummy) {
;     ...
;         for (int rep_ = 0; rep_ < ((DUP_ID == 10 && l == 0) ? DUP_N : 1); ++rep_) { unsigned char* ws = KWS; pg8::Gemm g{(const bf16*)(ws + WS_R + R_MB), (const bf16*)(ws + WS_WOUT) + (size_t)l * DM * DM, DM, 0}; pg8::StaticOrder S; S.init(M, DM, opaque_s(G), opaque_s(c));
.LBB0_990:
	s_mov_b64 s[2:3], s[100:101]
	s_andn2_b64 vcc, exec, s[4:5]
	s_cbranch_vccnz .LBB0_1060
	v_bfe_i32 v2, v4, 27, 1
	v_lshlrev_b32_e32 v0, 4, v4
	v_lshrrev_b32_e32 v2, 22, v2
	v_add_u32_e32 v2, v0, v2
	v_and_b32_e32 v2, 0xfffffc00, v2
	v_sub_u32_e32 v2, v0, v2
	v_lshrrev_b32_e32 v3, 4, v2
	v_ashrrev_i32_e32 v1, 31, v4
	v_bitop3_b32 v3, v3, v2, 32 bitop3:0x6c
	v_ashrrev_i32_e32 v2, 31, v2
	v_lshrrev_b32_e32 v1, 26, v1
	v_lshrrev_b32_e32 v2, 26, v2
	s_waitcnt lgkmcnt(0)
	s_add_u32 s36, s2, 0x3d800000
	v_readlane_b32 s5, v255, 40
	v_add_u32_e32 v1, v4, v1
	v_add_u32_e32 v2, v3, v2
	s_addc_u32 s4, s3, 0
	s_lshl_b32 s5, s5, 1
	v_ashrrev_i32_e32 v1, 6, v1
	v_ashrrev_i32_e32 v2, 6, v2
	s_add_u32 s5, s2, s5
	v_lshlrev_b32_e32 v5, 3, v1
	v_mul_i32_i24_e32 v6, 64, v2
	s_addc_u32 s6, s3, 0
	v_and_b32_e32 v5, -16, v5
	v_lshlrev_b32_e32 v1, 5, v1
	v_sub_u32_e32 v3, v3, v6
	s_add_u32 s12, s5, 0x3d00000
	v_add_u32_e32 v5, v2, v5
	v_and_b32_e32 v1, 32, v1
	v_ashrrev_i16_sdwa v3, v231, sext(v3) dst_sel:DWORD dst_unused:UNUSED_PAD src0_sel:DWORD src1_sel:BYTE_0
	s_addc_u32 s5, s6, 0
	v_add_u32_sdwa v1, v1, sext(v3) dst_sel:DWORD dst_unused:UNUSED_PAD src0_sel:DWORD src1_sel:WORD_0
	v_lshlrev_b32_e32 v3, 1, v5
	v_lshrrev_b32_e32 v6, 2, v5
	v_and_b32_e32 v2, 3, v2
	s_mov_b32 s6, 0x7fffffe0
	v_and_b32_e32 v3, 24, v3
	v_and_b32_e32 v6, 4, v6
	v_and_or_b32 v2, v5, s6, v2
	v_or3_b32 v2, v2, v6, v3
	v_mul_lo_u32 v3, v5, s23
	v_mul_lo_u32 v2, v2, s23
	v_add_u32_e32 v0, 0x2000, v0
	v_add_lshl_u32 v174, v1, v3, 1
	v_add_lshl_u32 v175, v2, v1, 1
	v_ashrrev_i32_e32 v1, 31, v0
	v_lshrrev_b32_e32 v1, 22, v1
	v_add_u32_e32 v1, v0, v1
	v_ashrrev_i32_e32 v1, 10, v1
	v_mul_i32_i24_e32 v2, 0x400, v1
	v_sub_u32_e32 v0, v0, v2
	v_lshrrev_b32_e32 v2, 4, v0
	v_bitop3_b32 v0, v2, v0, 32 bitop3:0x6c
	v_ashrrev_i32_e32 v3, 31, v0
	v_lshrrev_b32_e32 v3, 26, v3
	v_add_u32_e32 v3, v0, v3
	v_lshlrev_b32_e32 v2, 3, v1
	v_ashrrev_i32_e32 v5, 6, v3
	v_and_b32_e32 v3, 0xc0, v3
	v_and_b32_e32 v2, -16, v2
	v_lshlrev_b32_e32 v1, 5, v1
	v_sub_u32_e32 v0, v0, v3
	s_ashr_i32 s22, s11, 6
	v_add_u32_e32 v2, v5, v2
	v_and_b32_e32 v1, 32, v1
	v_ashrrev_i16_sdwa v0, v231, sext(v0) dst_sel:DWORD dst_unused:UNUSED_PAD src0_sel:DWORD src1_sel:BYTE_0
	v_add_u32_sdwa v0, v1, sext(v0) dst_sel:DWORD dst_unused:UNUSED_PAD src0_sel:DWORD src1_sel:WORD_0
	v_lshlrev_b32_e32 v1, 1, v2
	v_lshrrev_b32_e32 v3, 2, v2
	v_and_b32_e32 v5, 3, v5
	s_and_b32 s37, s4, 0xffff
	s_lshl_b32 s4, s22, 10
	v_and_b32_e32 v1, 24, v1
	v_and_b32_e32 v3, 4, v3
	v_and_or_b32 v5, v2, s6, v5
	s_add_i32 s34, s4, 0
	v_or3_b32 v1, v5, v3, v1
	s_add_i32 s35, s34, 0x10000
	v_mul_lo_u32 v2, v2, s23
	v_mul_lo_u32 v1, v1, s23
	s_and_b32 s13, s5, 0xffff
	s_mov_b32 s14, s38
	s_mov_b32 s15, s39
	s_lshl_b32 s5, s31, 19
	s_mov_b32 m0, s35
	s_add_i32 s41, s34, 0x12000
	v_add_lshl_u32 v176, v0, v2, 1
	v_add_lshl_u32 v177, v1, v0, 1
	s_lshl_b32 s33, s23, 8
	v_mov_b32 v0, 0
	buffer_load_dwordx4 v175, s[12:15], s5 offen lds
	s_mov_b32 m0, s41
	s_add_i32 s42, s34, 0x14000
	buffer_load_dwordx4 v177, s[12:15], s5 offen lds
	s_add_i32 s25, s5, s33
	s_mov_b32 m0, s42
	s_add_i32 s43, s34, 0x16000
	buffer_load_dwordx4 v175, s[12:15], s25 offen lds
	s_mov_b32 m0, s43
	s_lshl_b32 s4, s10, 19
	buffer_load_dwordx4 v177, s[12:15], s25 offen lds
	s_mov_b32 m0, s34
	s_add_i32 s44, s34, 0x2000
	buffer_load_dwordx4 v174, s[36:39], s4 offen lds
	s_mov_b32 m0, s44
	s_add_i32 s45, s34, 0x4000
	buffer_load_dwordx4 v176, s[36:39], s4 offen lds
	s_add_i32 s6, s4, s33
	s_mov_b32 m0, s45
	s_add_i32 s46, s34, 0x6000
	buffer_load_dwordx4 v174, s[36:39], s6 offen lds
	s_mov_b32 m0, s46
	s_ashr_i32 s24, s11, 8
	buffer_load_dwordx4 v176, s[36:39], s6 offen lds
	s_cmp_eq_u32 s24, 1
	s_cselect_b64 s[6:7], -1, 0
	s_cmp_lg_u32 s24, 1
	s_cbranch_scc1 .LBB0_993
	s_barrier

; #define LAS __attribute__((address_space(3)))
; __device__ __forceinline__ int opaque_tid(int wbase) { int t = wbase + lane_id(); asm volatile("" : "+v"(t)); return t; }
; __device__ __forceinline__ int opaque_s(int x) { asm volatile("" : "+s"(x)); return x; }
; #define KIN(i) (kargs()->in[i])
; #define KWS (kargs()->ws)
; #define REP(id) for (int rep_ = 0; rep_ < ((DUP_ID == (id)) ? DUP_N : 1); ++rep_)
; __device__ __forceinline__ void route_a(LAS unsigned char* lds, const bf16* h, const float* ssq, const float* gain, const float* rw, const float* rb, int* sel, float* selw, int* CNT, int G, int c, int wbase) {
;     const int tid = opaque_tid(wbase), lane = tid & 63, wid = __builtin_amdgcn_readfirstlane(tid >> 6); LAS int* lc = (LAS int*)lds; G = opaque_s(G); c = opaque_s(c);
;     f32x4 wg[4][4][2];
; #pragma unroll
;     for (int j = 0; j < 4; ++j) { const f32x4 gk = *(const f32x4*)(gain + 4 * lane + 256 * j);
; #pragma unroll
;         for (int q = 0; q < 4; ++q) { const float* wp = rw + (size_t)(4 * lane + 256 * j + q) * 8; wg[j][q][0] = *(const f32x4*)wp * gk[q]; wg[j][q][1] = *(const f32x4*)(wp + 4) * gk[q]; } }
;     float rbv[8];
; #pragma unroll
;     for (int e = 0; e < 8; ++e) rbv[e] = rb[e];
; __global__ void __launch_bounds__(512, 2) mega(Ptrs Pdummy) {
;     ...
;             REP(12) { unsigned char* ws = KWS; moe::route_a(lds, HBUF(hc), SBUF(sc), KIN(18) + l * DM, KIN(22) + (size_t)(l >> 1) * DM * NEXP, KIN(23) + (l >> 1) * NEXP, (int*)(ws + WS_SEL), (float*)(ws + WS_SEL + 256 * 1024), (int*)(ws + WS_SLOT + 964 * 1024), G, c, wbase); }
.LBB0_1104:
	s_or_b64 exec, exec, s[36:37]
	v_readlane_b32 s2, v255, 31
	v_readlane_b32 s3, v255, 32
	s_andn2_b64 vcc, exec, s[2:3]
	s_mov_b64 s[2:3], -1
	s_waitcnt lgkmcnt(0)
	s_barrier
	s_cbranch_vccnz .LBB0_1616
	s_mov_b64 s[8:9], s[88:89]
	s_mov_b64 s[4:5], s[88:89]
	s_mov_b64 s[6:7], s[88:89]
	s_mov_b64 s[2:3], s[88:89]
	s_mov_b32 s1, s38
	v_readlane_b32 s10, v255, 4
	v_mbcnt_lo_u32_b32 v0, s1, 0
	v_mbcnt_hi_u32_b32 v0, s1, v0
	v_add_u32_e32 v170, s93, v0
	s_mov_b32 s1, s10
	s_mov_b32 s33, s92
	s_cmpk_lt_i32 s33, 0x100
	v_readfirstlane_b32 s12, v170
	v_readlane_b32 s11, v255, 5
	s_cbranch_scc0 .LBB0_1118
	s_mov_b64 s[24:25], s[100:101]
	s_nop 0
	s_load_dwordx2 s[4:5], s[4:5], 0x90
	v_readlane_b32 s8, v255, 33
	s_lshr_b32 s13, s95, 1
	v_readlane_b32 s9, v255, 34
	s_load_dwordx2 s[6:7], s[6:7], 0xb0
	s_lshl_b32 s10, s13, 13
	s_lshl_b32 s14, s13, 3
	s_lshl_b64 s[8:9], s[8:9], 2
	s_waitcnt lgkmcnt(0)
	s_add_u32 s4, s4, s8
	v_and_b32_e32 v8, 63, v170
	s_mov_b32 s11, s40
	s_addc_u32 s5, s5, s9
	v_lshlrev_b32_e32 v2, 4, v8
	s_lshl_b64 s[8:9], s[10:11], 2
	global_load_dwordx4 v[4:7], v2, s[4:5]
	s_add_u32 s6, s6, s8
	s_addc_u32 s7, s7, s9
	v_lshlrev_b32_e32 v232, 7, v8
	s_load_dwordx2 s[2:3], s[2:3], 0xb8
	global_load_dwordx4 v[10:13], v232, s[6:7] offset:48
	global_load_dwordx4 v[24:27], v232, s[6:7] offset:32
	global_load_dwordx4 v[20:23], v232, s[6:7] offset:16
	global_load_dwordx4 v[16:19], v232, s[6:7]
	v_lshl_add_u64 v[0:1], s[6:7], 0, v[232:233]
	v_lshl_add_u64 v[14:15], v[0:1], 0, s[70:71]
	s_mov_b32 s15, s40
	s_lshl_b64 s[8:9], s[14:15], 2
	s_waitcnt lgkmcnt(0)
	s_add_u32 s2, s2, s8
	s_addc_u32 s3, s3, s9
	s_add_u32 s34, s24, 0x17600000
	s_addc_u32 s35, s25, 0
	s_add_u32 s36, s24, 0x17640000
	s_addc_u32 s37, s25, 0
	s_add_u32 s10, s24, 0x177f1000
	s_addc_u32 s11, s25, 0
	v_and_b32_e32 v9, 3, v170
	s_mov_b32 s41, 0
	v_lshl_add_u32 v171, v170, 2, 0
	s_waitcnt vmcnt(3)
	v_pk_mul_f32 v[28:29], v[4:5], v[10:11] op_sel:[1,0]
	v_pk_mul_f32 v[30:31], v[4:5], v[12:13] op_sel:[1,0]
	global_load_dwordx4 v[10:13], v232, s[6:7] offset:112
	global_load_dwordx4 v[40:43], v232, s[6:7] offset:96
	global_load_dwordx4 v[36:39], v232, s[6:7] offset:80
	global_load_dwordx4 v[32:35], v232, s[6:7] offset:64
	s_movk_i32 s6, 0x2000
	v_add_co_u32_e32 v64, vcc, s6, v0
	s_waitcnt vmcnt(4)
	v_pk_mul_f32 v[16:17], v[4:5], v[16:17] op_sel_hi:[0,1]
	v_pk_mul_f32 v[18:19], v[4:5], v[18:19] op_sel_hi:[0,1]
	v_pk_mul_f32 v[20:21], v[4:5], v[20:21] op_sel_hi:[0,1]
	v_pk_mul_f32 v[22:23], v[4:5], v[22:23] op_sel_hi:[0,1]
	v_pk_mul_f32 v[24:25], v[4:5], v[24:25] op_sel:[1,0]
	v_pk_mul_f32 v[26:27], v[4:5], v[26:27] op_sel:[1,0]
	v_mov_b32_e32 v4, v7
	v_addc_co_u32_e32 v65, vcc, 0, v1, vcc
	s_mov_b64 s[6:7], 0x2040
	s_waitcnt vmcnt(3)
	v_pk_mul_f32 v[44:45], v[4:5], v[10:11] op_sel_hi:[0,1]
	s_waitcnt vmcnt(2)
	v_pk_mul_f32 v[40:41], v[4:5], v[40:41] op_sel_hi:[0,1]
	s_waitcnt vmcnt(1)
	v_pk_mul_f32 v[36:37], v[6:7], v[36:37] op_sel_hi:[0,1]
	s_waitcnt vmcnt(0)
	v_pk_mul_f32 v[32:33], v[6:7], v[32:33] op_sel_hi:[0,1]
	v_pk_mul_f32 v[34:35], v[6:7], v[34:35] op_sel_hi:[0,1]
	v_pk_mul_f32 v[38:39], v[6:7], v[38:39] op_sel_hi:[0,1]
	v_pk_mul_f32 v[42:43], v[4:5], v[42:43] op_sel_hi:[0,1]
	v_pk_mul_f32 v[46:47], v[4:5], v[12:13] op_sel_hi:[0,1]
	global_load_dwordx4 v[4:7], v2, s[4:5] offset:1024
	global_load_dwordx4 v[10:13], v[64:65], off
	global_load_dwordx4 v[60:63], v[14:15], off offset:48
	global_load_dwordx4 v[56:59], v[14:15], off offset:32
	global_load_dwordx4 v[52:55], v[14:15], off offset:16
	s_waitcnt vmcnt(3)
	v_pk_mul_f32 v[48:49], v[4:5], v[12:13] op_sel_hi:[0,1]
	v_pk_mul_f32 v[50:51], v[4:5], v[10:11] op_sel_hi:[0,1]
	s_waitcnt vmcnt(0)
	v_pk_mul_f32 v[52:53], v[4:5], v[52:53] op_sel_hi:[0,1]
	v_pk_mul_f32 v[54:55], v[4:5], v[54:55] op_sel_hi:[0,1]
	v_pk_mul_f32 v[56:57], v[4:5], v[56:57] op_sel:[1,0]
	v_pk_mul_f32 v[58:59], v[4:5], v[58:59] op_sel:[1,0]
	v_pk_mul_f32 v[60:61], v[4:5], v[60:61] op_sel:[1,0]
	v_pk_mul_f32 v[62:63], v[4:5], v[62:63] op_sel:[1,0]
	v_lshl_add_u64 v[4:5], v[0:1], 0, s[6:7]
	global_load_dwordx4 v[10:13], v[64:65], off offset:64
	global_load_dwordx4 v[76:79], v[4:5], off offset:48
	global_load_dwordx4 v[72:75], v[4:5], off offset:32
	global_load_dwordx4 v[68:71], v[4:5], off offset:16
	s_mov_b64 s[6:7], 0x4000
	v_lshl_add_u64 v[14:15], v[0:1], 0, s[6:7]
	s_movk_i32 s6, 0x4000
	v_add_co_u32_e32 v96, vcc, s6, v0
	v_mov_b32_e32 v4, v7
	s_nop 0
	v_addc_co_u32_e32 v97, vcc, 0, v1, vcc
	s_mov_b64 s[6:7], 0x4040
	s_waitcnt vmcnt(3)
; __device__ __forceinline__ void route_a(LAS unsigned char* lds, const bf16* h, const float* ssq, const float* gain, const float* rw, const float* rb, int* sel, float* selw, int* CNT, int G, int c, int wbase) {
;     ...
;     f32x4 wg[4][4][2];
; #pragma unroll
;     for (int j = 0; j < 4; ++j) { const f32x4 gk = *(const f32x4*)(gain + 4 * lane + 256 * j);
; #pragma unroll
;         for (int q = 0; q < 4; ++q) { const float* wp = rw + (size_t)(4 * lane + 256 * j + q) * 8; wg[j][q][0] = *(const f32x4*)wp * gk[q]; wg[j][q][1] = *(const f32x4*)(wp + 4) * gk[q]; } }
;     float rbv[8];
; #pragma unroll
;     for (int e = 0; e < 8; ++e) rbv[e] = rb[e];
	v_pk_mul_f32 v[64:65], v[6:7], v[12:13] op_sel_hi:[0,1]
	v_pk_mul_f32 v[66:67], v[6:7], v[10:11] op_sel_hi:[0,1]
	s_waitcnt vmcnt(1)
	v_pk_mul_f32 v[72:73], v[4:5], v[72:73] op_sel_hi:[0,1]
	s_waitcnt vmcnt(0)
	v_pk_mul_f32 v[68:69], v[6:7], v[68:69] op_sel_hi:[0,1]
	v_pk_mul_f32 v[70:71], v[6:7], v[70:71] op_sel_hi:[0,1]
	v_pk_mul_f32 v[74:75], v[4:5], v[74:75] op_sel_hi:[0,1]
	v_pk_mul_f32 v[76:77], v[4:5], v[76:77] op_sel_hi:[0,1]
	v_pk_mul_f32 v[78:79], v[4:5], v[78:79] op_sel_hi:[0,1]
	global_load_dwordx4 v[4:7], v2, s[4:5] offset:2048
	global_load_dwordx4 v[10:13], v[96:97], off
	global_load_dwordx4 v[92:95], v[14:15], off offset:48
	global_load_dwordx4 v[88:91], v[14:15], off offset:32
	global_load_dwordx4 v[84:87], v[14:15], off offset:16
	s_waitcnt vmcnt(3)
	v_pk_mul_f32 v[80:81], v[4:5], v[12:13] op_sel_hi:[0,1]
	v_pk_mul_f32 v[82:83], v[4:5], v[10:11] op_sel_hi:[0,1]
	s_waitcnt vmcnt(0)
	v_pk_mul_f32 v[84:85], v[4:5], v[84:85] op_sel_hi:[0,1]
	v_pk_mul_f32 v[86:87], v[4:5], v[86:87] op_sel_hi:[0,1]
	v_pk_mul_f32 v[88:89], v[4:5], v[88:89] op_sel:[1,0]
	v_pk_mul_f32 v[90:91], v[4:5], v[90:91] op_sel:[1,0]
	v_pk_mul_f32 v[92:93], v[4:5], v[92:93] op_sel:[1,0]
	v_pk_mul_f32 v[94:95], v[4:5], v[94:95] op_sel:[1,0]
	v_lshl_add_u64 v[4:5], v[0:1], 0, s[6:7]
	global_load_dwordx4 v[10:13], v[96:97], off offset:64
	global_load_dwordx4 v[108:111], v[4:5], off offset:48
	global_load_dwordx4 v[104:107], v[4:5], off offset:32
	global_load_dwordx4 v[100:103], v[4:5], off offset:16
	v_mov_b32_e32 v4, v7
	s_waitcnt vmcnt(3)
	v_pk_mul_f32 v[96:97], v[6:7], v[12:13] op_sel_hi:[0,1]
	s_waitcnt vmcnt(2)
	v_pk_mul_f32 v[108:109], v[4:5], v[108:109] op_sel_hi:[0,1]
	s_waitcnt vmcnt(1)
	v_pk_mul_f32 v[104:105], v[4:5], v[104:105] op_sel_hi:[0,1]
	v_pk_mul_f32 v[106:107], v[4:5], v[106:107] op_sel_hi:[0,1]
	v_pk_mul_f32 v[110:111], v[4:5], v[110:111] op_sel_hi:[0,1]
	global_load_dwordx4 v[2:5], v2, s[4:5] offset:3072
	s_mov_b64 s[4:5], 0x6000
	v_pk_mul_f32 v[98:99], v[6:7], v[10:11] op_sel_hi:[0,1]
	s_waitcnt vmcnt(1)
	v_pk_mul_f32 v[100:101], v[6:7], v[100:101] op_sel_hi:[0,1]
	v_pk_mul_f32 v[102:103], v[6:7], v[102:103] op_sel_hi:[0,1]
	v_lshl_add_u64 v[6:7], v[0:1], 0, s[4:5]
	s_movk_i32 s4, 0x6000
	v_add_co_u32_e32 v14, vcc, s4, v0
	s_mov_b64 s[4:5], 0x6040
	s_nop 0
	v_addc_co_u32_e32 v15, vcc, 0, v1, vcc
	global_load_dwordx4 v[10:13], v[14:15], off
	global_load_dwordx4 v[124:127], v[6:7], off offset:48
	global_load_dwordx4 v[120:123], v[6:7], off offset:32
	global_load_dwordx4 v[116:119], v[6:7], off offset:16
	v_lshl_add_u64 v[6:7], v[0:1], 0, s[4:5]
	v_cmp_eq_u32_e64 s[4:5], 0, v8
	s_waitcnt vmcnt(3)
	v_pk_mul_f32 v[112:113], v[2:3], v[12:13] op_sel_hi:[0,1]
	v_pk_mul_f32 v[114:115], v[2:3], v[10:11] op_sel_hi:[0,1]
	s_waitcnt vmcnt(1)
	v_pk_mul_f32 v[120:121], v[2:3], v[120:121] op_sel:[1,0]
	s_waitcnt vmcnt(0)
	v_pk_mul_f32 v[116:117], v[2:3], v[116:117] op_sel_hi:[0,1]
	v_pk_mul_f32 v[118:119], v[2:3], v[118:119] op_sel_hi:[0,1]
	v_pk_mul_f32 v[122:123], v[2:3], v[122:123] op_sel:[1,0]
	v_pk_mul_f32 v[124:125], v[2:3], v[124:125] op_sel:[1,0]
	v_pk_mul_f32 v[126:127], v[2:3], v[126:127] op_sel:[1,0]
	global_load_dwordx4 v[0:3], v[14:15], off offset:64
	global_load_dwordx4 v[10:13], v[6:7], off offset:48
	global_load_dwordx4 v[136:139], v[6:7], off offset:32
	global_load_dwordx4 v[132:135], v[6:7], off offset:16
	s_waitcnt vmcnt(3)
	v_pk_mul_f32 v[130:131], v[4:5], v[0:1] op_sel_hi:[0,1]
	v_mov_b32_e32 v0, v5
	v_pk_mul_f32 v[128:129], v[4:5], v[2:3] op_sel_hi:[0,1]
	s_waitcnt vmcnt(0)
	v_pk_mul_f32 v[132:133], v[4:5], v[132:133] op_sel_hi:[0,1]
	v_pk_mul_f32 v[134:135], v[4:5], v[134:135] op_sel_hi:[0,1]
	v_pk_mul_f32 v[136:137], v[0:1], v[136:137] op_sel_hi:[0,1]
	v_pk_mul_f32 v[138:139], v[0:1], v[138:139] op_sel_hi:[0,1]
	v_pk_mul_f32 v[140:141], v[0:1], v[10:11] op_sel_hi:[0,1]
	v_pk_mul_f32 v[142:143], v[0:1], v[12:13] op_sel_hi:[0,1]
	global_load_dwordx4 v[0:3], v233, s[2:3]
	global_load_dwordx4 v[4:7], v233, s[2:3] offset:16
	v_readlane_b32 s2, v255, 10
	s_cmp_eq_u32 s2, 0
	s_mov_b32 s2, 0x13200000
	s_cselect_b32 s6, s2, 0x1b800000
	s_ashr_i32 s2, s12, 2
	s_and_b32 s7, s2, -16
	s_lshl_b32 s2, s2, 1
	s_lshl_b32 s42, s33, 8
	s_andn2_b32 s2, s2, 31
	s_add_i32 s42, s42, s2
	s_lshl_b32 s43, s1, 8
	v_readlane_b32 s2, v255, 11
	s_cmp_eq_u32 s2, 1
	s_cselect_b32 s8, 0, 0x200000
	v_lshl_or_b32 v232, v9, 4, s8
	s_mov_b64 s[8:9], 0x17200000
	v_lshl_add_u64 v[144:145], v[232:233], 0, s[8:9]
	s_lshl_b32 s8, s33, 7
	s_add_i32 s26, s8, s7
	v_cmp_gt_i32_e64 s[2:3], 8, v170
	s_or_b32 s28, s26, 1
	s_lshl_b32 s44, s1, 7
	v_lshl_or_b32 v232, v8, 3, s6
	s_branch .LBB0_1108

; #define LAS __attribute__((address_space(3)))
; __device__ __forceinline__ int opaque_tid(int wbase) { int t = wbase + lane_id(); asm volatile("" : "+v"(t)); return t; }
; __device__ __forceinline__ int opaque_s(int x) { asm volatile("" : "+s"(x)); return x; }
; template <int MASK> __device__ __forceinline__ int swz_i(int v) { return __builtin_amdgcn_ds_swizzle(v, (MASK << 10) | 0x1f); }
; #define KWS (kargs()->ws)
; #define REP(id) for (int rep_ = 0; rep_ < ((DUP_ID == (id)) ? DUP_N : 1); ++rep_)
; __device__ __forceinline__ void route_b(LAS unsigned char* lds, const int* sel, const float* selw, const float* ssq, const int* CNT, const bf16* hb, int* tok, float* srs, float* sgw, int* tslot, int* meta, bf16* XG, int G, int c, int wbase) {
;     const int tid = opaque_tid(wbase), lane = tid & 63, wid = __builtin_amdgcn_readfirstlane(tid >> 6); G = opaque_s(G); c = opaque_s(c);
;     LAS int* tot = (LAS int*)lds; LAS int* pre = tot + 8; LAS int* start = tot + 16; LAS int* pos = tot + 32; LAS float* rsl = (LAS float*)(tot + 32 + 256);
;     for (int chunk = c; chunk < NCHUNK; chunk += G) {
;         { int t = 0, p = 0;
; #pragma unroll
;           for (int j = 0; j < NCHUNK / 64; ++j) { const int ch = lane + 64 * j; const int v = CNT[ch * 8 + wid]; t += v; p += (ch < chunk) ? v : 0; }
;           t += swz_i<1>(t); t += swz_i<2>(t); t += swz_i<4>(t); t += swz_i<8>(t); t += swz_i<16>(t); t = sum_x32i(t);
;           p += swz_i<1>(p); p += swz_i<2>(p); p += swz_i<4>(p); p += swz_i<8>(p); p += swz_i<16>(p); p = sum_x32i(p);
;           if (lane == 0) { tot[wid] = t; pre[wid] = p; } }
;         __syncthreads();
;         if (tid == 0) { int s = 0; for (int e = 0; e < 8; ++e) { start[e] = s; s += ((tot[e] + 255) >> 8) << 8; } start[8] = s; }
;         __syncthreads();
;         if (chunk == 0 && tid < 9) meta[tid] = start[tid] >> 8;
; __global__ void __launch_bounds__(512, 2) mega(Ptrs Pdummy) {
;     ...
;             REP(13) { unsigned char* ws = KWS; moe::route_b(lds, (const int*)(ws + WS_SEL), (const float*)(ws + WS_SEL + 256 * 1024), SBUF(sc), (const int*)(ws + WS_SLOT + 964 * 1024), HBUF(hc), (int*)(ws + WS_SLOT), (float*)(ws + WS_SLOT + 320 * 1024),
;                                              (float*)(ws + WS_SLOT + 640 * 1024), (int*)(ws + WS_SEL + 512 * 1024), (int*)(ws + WS_SLOT + 960 * 1024), (bf16*)(ws + WS_R + R_XG), G, c, wbase); }
.LBB0_1163:
	s_or_b64 exec, exec, s[10:11]
	s_mov_b64 s[2:3], s[88:89]
	s_mov_b32 s1, s38
	s_waitcnt lgkmcnt(0)
	s_barrier
	v_readlane_b32 s4, v255, 4
	v_mbcnt_lo_u32_b32 v0, s1, 0
	v_mbcnt_hi_u32_b32 v0, s1, v0
	v_add_u32_e32 v12, s93, v0
	s_mov_b32 s1, s4
	s_mov_b32 s30, s92
	s_cmpk_lt_i32 s30, 0x100
	v_readfirstlane_b32 s22, v12
	v_readlane_b32 s5, v255, 5
	s_cbranch_scc0 .LBB0_1267
	s_mov_b64 s[24:25], s[100:101]
	v_readlane_b32 s2, v255, 11
	s_cmp_eq_u32 s2, 1
	s_cselect_b32 s2, 0, 0x200000
	v_and_b32_e32 v17, 63, v12
	s_waitcnt lgkmcnt(0)
	s_add_u32 s8, s24, 0x17600000
	s_addc_u32 s9, s25, 0
	s_add_u32 s10, s24, 0x17640000
	s_addc_u32 s11, s25, 0
	s_add_u32 s2, s24, s2
	s_addc_u32 s3, s25, 0
	s_add_u32 s12, s2, 0x17200000
	s_addc_u32 s13, s3, 0
	s_add_u32 s14, s24, 0x17700000
	s_addc_u32 s15, s25, 0
	s_add_u32 s16, s24, 0x17750000
	s_addc_u32 s17, s25, 0
	s_add_u32 s18, s24, 0x177a0000
	s_addc_u32 s19, s25, 0
	s_add_u32 s20, s24, 0x17680000
	s_addc_u32 s21, s25, 0
	s_ashr_i32 s31, s22, 6
	v_readlane_b32 s2, v255, 10
	s_cmp_eq_u32 s2, 0
	s_mov_b32 s2, 0x13200000
	s_cselect_b32 s2, s2, 0x1b800000
	s_add_u32 s26, s24, s2
	v_ashrrev_i32_e32 v13, 31, v12
	s_addc_u32 s27, s25, 0
	v_lshl_add_u64 v[0:1], v[12:13], 2, s[24:25]
	s_mov_b64 s[34:35], 0x177f0000
	v_lshlrev_b32_e32 v232, 5, v17
	s_add_u32 s28, s24, 0x177f1000
	v_lshl_add_u64 v[14:15], v[0:1], 0, s[34:35]
	v_lshlrev_b64 v[0:1], v12, -1
	v_lshl_add_u64 v[18:19], s[26:27], 0, v[232:233]
	v_lshlrev_b32_e32 v232, 4, v17
	s_addc_u32 s29, s25, 0
	v_not_b32_e32 v13, v1
	v_not_b32_e32 v16, v0
	v_lshl_add_u64 v[0:1], s[24:25], 0, v[232:233]
	s_mov_b64 s[24:25], 0x1f800000
	v_lshl_add_u64 v[20:21], v[0:1], 0, s[24:25]
	v_lshl_add_u32 v0, v17, 3, s31
	v_ashrrev_i32_e32 v1, 31, v0
	v_or_b32_e32 v41, 64, v17
	s_lshl_b32 s4, s31, 2
	v_lshl_add_u64 v[22:23], v[0:1], 2, s[28:29]
	v_lshl_add_u32 v0, v41, 3, s31
	s_add_i32 s33, s4, 0
	v_ashrrev_i32_e32 v1, 31, v0
	v_or_b32_e32 v42, 0x80, v17
	s_cmp_gt_u32 s22, 63
	v_lshl_add_u64 v[24:25], v[0:1], 2, s[28:29]
	v_lshl_add_u32 v0, v42, 3, s31
	s_cselect_b64 s[22:23], -1, 0
	s_lshl_b32 s34, s31, 5
	v_ashrrev_i32_e32 v1, 31, v0
	v_or_b32_e32 v43, 0xc0, v17
	s_lshl_b32 s24, s31, 7
	v_lshl_add_u64 v[26:27], v[0:1], 2, s[28:29]
	v_lshl_add_u32 v0, v43, 3, s31
	s_add_i32 s36, s24, 0
	s_lshl_b32 s24, s30, 7
	s_and_b32 s25, s34, 32
	v_ashrrev_i32_e32 v1, 31, v0
	s_or_b32 s24, s24, s25
	v_cmp_eq_u32_e64 s[2:3], 0, v17
	v_cmp_eq_u32_e64 s[4:5], 0, v12
	v_cmp_gt_i32_e64 s[6:7], 9, v12
	v_lshl_add_u32 v40, v12, 2, 0
	v_lshl_add_u64 v[28:29], v[0:1], 2, s[28:29]
	v_lshl_add_u32 v44, v17, 2, 0
	s_or_b32 s35, s34, 28
	v_not_b32_e32 v45, v12
	v_add_u32_e32 v46, 0x200, v12
	s_addk_i32 s36, 0x80
	s_or_b32 s37, s24, 3
	s_lshl_b32 s44, s1, 7
	s_branch .LBB0_1166

; __device__ __forceinline__ int opaque_s(int x) { asm volatile("" : "+s"(x)); return x; }
;     __device__ __forceinline__ void setup(int G_, int c_) { so.setup(G_, c_); }
;     __device__ __forceinline__ bool next(int i, Unit& u) const { const bool ok = so.next(i >> 1, u); u.part = i & 1; return ok; }
; #define KWS (kargs()->ws)
; #define REP(id) for (int rep_ = 0; rep_ < ((DUP_ID == (id)) ? DUP_N : 1); ++rep_)
;     __device__ __forceinline__ void setup(int G_, int c_) {
; #pragma unroll
;         for (int e = 0; e < 9; ++e) ts[e] = __builtin_amdgcn_readfirstlane(__hip_atomic_load(meta + e, __ATOMIC_RELAXED, __HIP_MEMORY_SCOPE_AGENT));
;         so.init(ts[8] * BM, N, G_, c_);
;     }
;     __device__ __forceinline__ bool next(int i, Unit& u) const { return so.next(i, u); }
; __global__ void __launch_bounds__(512, 2) mega(Ptrs Pdummy) {
;     ...
;             REP(14) { unsigned char* ws = KWS; pg8::Gemm g{(const bf16*)(ws + WS_R + R_XG8), (const bf16*)(ws + WS_W13E), MOE_FP8 ? DM / 2 : DM, 0}; pg8::MoeOrder S; S.meta = (const int*)(ws + WS_SLOT + 960 * 1024); S.wstride = (size_t)2 * DFF * DM / (MOE_FP8 ? 2 : 1); S.N = 2 * DFF; S.pad0 = 0; S.setup(opaque_s(G), opaque_s(c));
;               pg8::EpiSwiglu<true> E{(bf16*)(ws + WS_R + R_GM), nullptr, (const float*)(ws + WS_SLOT + 320 * 1024), (const float*)(ws + WS_SLOT + 640 * 1024), 0, 1.f}; pg8::gemm_phase<pg8::EpiSwiglu<true>, pg8::MoeOrder, true, true, MOE_FP8>(lds, g, S, E, wbase); }
.LBB0_1312:
	s_or_b64 exec, exec, s[10:11]
	s_mov_b64 s[2:3], s[88:89]
	s_waitcnt lgkmcnt(0)
	s_barrier
	s_mov_b64 s[2:3], s[100:101]
	v_readlane_b32 s4, v255, 4
	s_mov_b32 s1, s4
	s_mov_b32 s22, s92
	v_mov_b32_e32 v1, 0x177f0000
	s_waitcnt lgkmcnt(0)
	global_load_dword v0, v1, s[2:3] sc1
	global_load_dword v33, v1, s[2:3] offset:4 sc1
	global_load_dword v34, v1, s[2:3] offset:8 sc1
	global_load_dword v35, v1, s[2:3] offset:12 sc1
	global_load_dword v36, v1, s[2:3] offset:16 sc1
	global_load_dword v37, v1, s[2:3] offset:20 sc1
	global_load_dword v38, v1, s[2:3] offset:24 sc1
	global_load_dword v39, v1, s[2:3] offset:28 sc1
	global_load_dword v40, v1, s[2:3] offset:32 sc1
	s_mov_b32 s4, s38
	s_movk_i32 s16, 0x200
	v_readlane_b32 s5, v255, 5
	s_waitcnt vmcnt(0)
	v_readfirstlane_b32 s23, v33
	v_readfirstlane_b32 s24, v34
	v_readfirstlane_b32 s25, v35
	v_readfirstlane_b32 s26, v36
	v_readfirstlane_b32 s27, v37
	v_readfirstlane_b32 s28, v38
	v_readfirstlane_b32 s29, v39
	v_readfirstlane_b32 s30, v40
	v_mbcnt_lo_u32_b32 v0, s4, 0
	v_mbcnt_hi_u32_b32 v0, s4, v0
	s_mul_i32 s31, s30, 28
	v_add_u32_e32 v1, s93, v0
	s_cmp_lt_i32 s22, s31
	v_readfirstlane_b32 s15, v1
	s_cbranch_scc0 .LBB0_1372
	s_ashr_i32 s4, s31, 31
	s_lshr_b32 s4, s4, 29
	s_add_i32 s4, s31, s4
	s_ashr_i32 s33, s4, 3
	s_and_b32 s4, s4, -8
	s_sub_i32 s34, s31, s4
	s_ashr_i32 s4, s22, 31
	s_lshr_b32 s4, s4, 29
	s_add_i32 s7, s22, s4
	s_and_b32 s4, s7, -8
	s_sub_i32 s8, s22, s4
	s_add_i32 s35, s33, 1
	s_cmp_ge_i32 s8, s34
	s_mov_b64 s[4:5], -1
	s_cbranch_scc0 .LBB0_1315
	s_sub_i32 s5, s8, s34
	s_mul_i32 s4, s35, s34
	s_mul_i32 s5, s5, s33
	s_add_i32 s6, s4, s5
	s_mov_b64 s[4:5], 0

; __device__ __forceinline__ int opaque_s(int x) { asm volatile("" : "+s"(x)); return x; }
;     __device__ __forceinline__ void setup(int G_, int c_) { so.setup(G_, c_); }
;     __device__ __forceinline__ bool next(int i, Unit& u) const { const bool ok = so.next(i >> 1, u); u.part = i & 1; return ok; }
; #define KWS (kargs()->ws)
; #define REP(id) for (int rep_ = 0; rep_ < ((DUP_ID == (id)) ? DUP_N : 1); ++rep_)
;     __device__ __forceinline__ void setup(int G_, int c_) {
; #pragma unroll
;         for (int e = 0; e < 9; ++e) ts[e] = __builtin_amdgcn_readfirstlane(__hip_atomic_load(meta + e, __ATOMIC_RELAXED, __HIP_MEMORY_SCOPE_AGENT));
;         so.init(ts[8] * BM, N, G_, c_);
;     }
;     __device__ __forceinline__ bool next(int i, Unit& u) const { return so.next(i, u); }
; __global__ void __launch_bounds__(512, 2) mega(Ptrs Pdummy) {
;     ...
;             REP(15) { unsigned char* ws = KWS; pg8::Gemm g{(const bf16*)(ws + WS_R + R_GM), (const bf16*)(ws + WS_W2E), MOE_FP8 ? DFF / 2 : DFF, 0}; pg8::MoeOrder S; S.meta = (const int*)(ws + WS_SLOT + 960 * 1024); S.wstride = (size_t)DM * DFF / (MOE_FP8 ? 2 : 1); S.N = DM; S.pad0 = 0; S.setup(opaque_s(G), opaque_s(c));
;               pg8::EpiStore16 E{(bf16*)(ws + WS_R + R_XG), DM, MOE_FP8 ? 1.f / (W2_SCALE * G8_SCALE) : 1.f}; pg8::gemm_phase<pg8::EpiStore16, pg8::MoeOrder, true, true, MOE_FP8>(lds, g, S, E, wbase); }
.LBB0_1417:
	s_or_b64 exec, exec, s[10:11]
	s_mov_b64 s[2:3], s[88:89]
	s_waitcnt lgkmcnt(0)
	s_barrier
	s_mov_b64 s[2:3], s[100:101]
	v_readlane_b32 s4, v255, 4
	s_mov_b32 s1, s4
	s_mov_b32 s20, s92
	v_mov_b32_e32 v1, 0x177f0000
	s_waitcnt lgkmcnt(0)
	global_load_dword v0, v1, s[2:3] sc1
	global_load_dword v33, v1, s[2:3] offset:4 sc1
	global_load_dword v34, v1, s[2:3] offset:8 sc1
	global_load_dword v35, v1, s[2:3] offset:12 sc1
	global_load_dword v36, v1, s[2:3] offset:16 sc1
	global_load_dword v37, v1, s[2:3] offset:20 sc1
	global_load_dword v38, v1, s[2:3] offset:24 sc1
	global_load_dword v39, v1, s[2:3] offset:28 sc1
	global_load_dword v40, v1, s[2:3] offset:32 sc1
	s_mov_b32 s4, s38
	s_movk_i32 s12, 0x700
	v_readlane_b32 s5, v255, 5
	s_waitcnt vmcnt(0)
	v_readfirstlane_b32 s21, v33
	v_readfirstlane_b32 s22, v34
	v_readfirstlane_b32 s23, v35
	v_readfirstlane_b32 s24, v36
	v_readfirstlane_b32 s25, v37
	v_readfirstlane_b32 s26, v38
	v_readfirstlane_b32 s27, v39
	v_readfirstlane_b32 s28, v40
	v_mbcnt_lo_u32_b32 v0, s4, 0
	v_mbcnt_hi_u32_b32 v0, s4, v0
	s_lshl_b32 s29, s28, 2
	v_add_u32_e32 v1, s93, v0
	s_cmp_lt_i32 s20, s29
	v_readfirstlane_b32 s14, v1
	s_cbranch_scc0 .LBB0_1477
	s_lshr_b32 s4, s28, 31
	s_add_i32 s4, s28, s4
	s_ashr_i32 s30, s4, 1
	s_ashr_i32 s4, s29, 31
	s_lshr_b32 s4, s4, 29
	s_add_i32 s4, s29, s4
	s_and_b32 s4, s4, -8
	s_sub_i32 s31, s29, s4
	s_ashr_i32 s4, s20, 31
	s_lshr_b32 s4, s4, 29
	s_add_i32 s7, s20, s4
	s_and_b32 s4, s7, -8
	s_sub_i32 s8, s20, s4
	s_add_i32 s33, s30, 1
	s_cmp_ge_i32 s8, s31
	s_mov_b64 s[4:5], -1
	s_cbranch_scc0 .LBB0_1420
	s_sub_i32 s5, s8, s31
	s_mul_i32 s4, s33, s31
	s_mul_i32 s5, s5, s30
	s_add_i32 s6, s5, s4
	s_mov_b64 s[4:5], 0

; #define KWS (kargs()->ws)
; #define WAVE_IDS() const int tid = opaque_tid(wbase), lane = tid & 63, wid = __builtin_amdgcn_readfirstlane(tid >> 6), gw = c * 8 + wid, ngw = G * 8; (void)tid; (void)lane; (void)gw; (void)ngw
; __global__ void __launch_bounds__(512, 2) mega(Ptrs Pdummy) {
;     ...
;             { WAVE_IDS(); unsigned char* ws = KWS; const int* TSLOT = (const int*)(ws + WS_SEL + 512 * 1024); const bf16* XG = (const bf16*)(ws + WS_R + R_XG);
;               for (int m = gw; m < M; m += 2 * ngw) { const int m2 = m + ngw;
;                   if (m2 >= M) { rowstats_row<true>(nullptr, HBUF(hc) + (size_t)m * DM, SBUF(sc ^ 1) + 16 * (size_t)m, XG + (size_t)TSLOT[2 * m] * DM, XG + (size_t)TSLOT[2 * m + 1] * DM, lane); break; }
;                   const int s1 = TSLOT[2 * m], s2 = TSLOT[2 * m + 1], s3 = TSLOT[2 * m2], s4 = TSLOT[2 * m2 + 1];
;                   const bool p8 = (PLE_FP8_MASK >> l) & 1;
;                   combine_rows2(HBUF(hc) + (size_t)m * DM, SBUF(sc ^ 1) + 16 * (size_t)m, XG + (size_t)s1 * DM, XG + (size_t)s2 * DM,
;                                 HBUF(hc) + (size_t)m2 * DM, SBUF(sc ^ 1) + 16 * (size_t)m2, XG + (size_t)s3 * DM, XG + (size_t)s4 * DM, lane,
;                                 p8 ? ws + WS_HB8 + (size_t)m * DM : nullptr, p8 ? ws + WS_HB8 + (size_t)m2 * DM : nullptr); } }
.LBB0_1522:
	s_or_b64 exec, exec, s[10:11]
	s_mov_b32 s1, s38
	s_waitcnt lgkmcnt(0)
	s_barrier
	s_mov_b64 s[2:3], s[88:89]
	v_mbcnt_lo_u32_b32 v0, s1, 0
	v_mbcnt_hi_u32_b32 v0, s1, v0
	v_add_u32_e32 v0, s93, v0
	s_nop 0
	v_readfirstlane_b32 s1, v0
	s_ashr_i32 s8, s1, 6
	v_readlane_b32 s1, v255, 27
	s_add_i32 s10, s8, s1
	s_cmpk_gt_i32 s10, 0x7fff
	s_cbranch_scc1 .LBB0_1571
	s_mov_b64 s[6:7], s[100:101]
	v_readlane_b32 s2, v255, 10
	v_and_b32_e32 v0, 63, v0
	v_readlane_b32 s4, v255, 11
	v_lshlrev_b32_e32 v232, 3, v0
	s_waitcnt lgkmcnt(0)
	s_add_u32 s1, s6, 0x17680000
	s_addc_u32 s22, s7, 0
	s_cmp_eq_u32 s2, 0
	s_mov_b32 s2, 0x13200000
	s_cselect_b32 s2, s2, 0x1b800000
	s_add_u32 s2, s6, s2
	s_addc_u32 s3, s7, 0
	s_cmp_eq_u32 s4, 0
	v_lshl_add_u64 v[2:3], s[2:3], 0, v[232:233]
	s_cselect_b32 s2, 0, 0x200000
	s_add_u32 s12, s6, s2
	s_addc_u32 s13, s7, 0
	v_lshl_add_u64 v[4:5], s[6:7], 0, v[232:233]
	v_lshlrev_b32_e32 v232, 2, v0
	s_add_u32 s23, s6, 0xb200000
	s_mov_b64 s[2:3], 0x1f800000
	v_lshl_add_u64 v[6:7], s[12:13], 0, v[232:233]
	s_mov_b64 s[12:13], 0x17200000
	s_addc_u32 s24, s7, 0
	s_lshl_b32 s8, s8, 1
	v_readlane_b32 s9, v255, 3
	v_lshl_add_u64 v[4:5], v[4:5], 0, s[2:3]
	v_cmp_eq_u32_e64 s[2:3], 3, v0
	v_cmp_gt_u32_e64 s[4:5], 16, v0
	v_lshl_add_u64 v[6:7], v[6:7], 0, s[12:13]
	v_cmp_ne_u32_e64 s[6:7], 0, v0
	s_add_i32 s12, s9, s8
	v_lshlrev_b32_e32 v232, 2, v0
	s_branch .LBB0_1526

; __device__ __forceinline__ unsigned xb_ld(unsigned* p)              { return __hip_atomic_load(p, __ATOMIC_RELAXED, __HIP_MEMORY_SCOPE_AGENT); }
; __device__ __forceinline__ void xcd_barrier_complete(unsigned* bar, unsigned x, unsigned& nloc, unsigned& nx) {
;     const unsigned G = gridDim.x * gridDim.y * gridDim.z;
;     unsigned sum, cnt, mine, sp = 0u;
;     for (;;) {
;         sum = 0u; cnt = 0u; mine = 0u;
; #pragma unroll
;         for (unsigned j = 0; j < 16; ++j) { const unsigned c = xb_ld(&bar[XB_XCNT(j)]); sum += c; cnt += (c > 0u) ? 1u : 0u; mine = (j == x) ? c : mine; }
; __device__ __forceinline__ void xcd_barrier(const XcdBarrier& b, bool leader) {
;     asm volatile("s_waitcnt vmcnt(0)" ::: "memory");
;     __syncthreads();
;     if (leader) {
;         unsigned zo_; asm volatile("v_mov_b32 %0, 0" : "=v"(zo_)); unsigned* bar = b.bar + zo_;
;         __builtin_amdgcn_s_waitcnt(0);
;         unsigned nloc = b.st[0], nx = b.st[1];
;         if (nloc == 0u) { xcd_barrier_complete(bar, b.x, nloc, nx); b.st[0] = nloc; b.st[1] = nx; }
.Lbinv_skip_10:
	s_and_saveexec_b64 s[10:11], vcc
	s_cbranch_execz .LBB0_1615
	s_mov_b64 s[2:3], s[100:101]
	v_mov_b32 v232, 0
	s_waitcnt vmcnt(0) expcnt(0) lgkmcnt(0)
	s_and_b32 s1, s1, 15
	v_lshl_add_u64 v[0:1], v[232:233], 2, s[2:3]
	s_mov_b64 s[2:3], 0x4000
	v_lshl_add_u64 v[0:1], v[0:1], 0, s[2:3]
	v_readlane_b32 s2, v255, 7
	s_nop 1
	v_mov_b32_e32 v2, s2
	ds_read_b32 v6, v2
	v_readlane_b32 s2, v255, 8
	s_waitcnt lgkmcnt(0)
	v_cmp_ne_u32_e32 vcc, 0, v6
	v_mov_b32_e32 v2, s2
	ds_read_b32 v4, v2
	s_cbranch_vccnz .LBB0_1586
	v_readlane_b32 s4, v255, 0
	v_readlane_b32 s5, v255, 1
	s_load_dwordx2 s[2:3], s[4:5], 0x4
	s_mov_b64 s[4:5], 0x1100
	s_waitcnt lgkmcnt(0)
	v_lshl_add_u64 v[4:5], v[0:1], 0, s[4:5]
	s_mov_b64 s[4:5], 0x1200
	v_lshl_add_u64 v[6:7], v[0:1], 0, s[4:5]
	s_mov_b64 s[4:5], 0x1300
	v_lshl_add_u64 v[8:9], v[0:1], 0, s[4:5]
	v_readlane_b32 s4, v255, 4
	s_mul_i32 s22, s2, s4
	v_lshl_add_u64 v[2:3], v[0:1], 0, s[72:73]
	v_readlane_b32 s5, v255, 5
	s_mul_i32 s22, s22, s3
	s_mov_b32 s23, 1
	s_mov_b64 s[2:3], 0
	s_branch .LBB0_1576

; __device__ __forceinline__ int opaque_tid(int wbase) { int t = wbase + lane_id(); asm volatile("" : "+v"(t)); return t; }
; template <class Epi, class Sched, bool ALIGN_EPI = false, bool SP2 = false, bool FP8 = false>
; __device__ __forceinline__ void gemm_phase(LAS unsigned char* lds, const Gemm g, const Sched& S, const Epi& E, int wbase) {
;     const int tid = opaque_tid(wbase), wid = __builtin_amdgcn_readfirstlane(tid >> 6), lane = tid & 63, wr = wid >> 2, wc = wid & 3, fr = lane & 15, fq = lane >> 4;
;     const int K = opaque_s(g.K), nt = K / BK;
;     unsigned voffA[2], voffB[2];
; #pragma unroll
;     for (int i = 0; i < 2; ++i) { int R, C; stage_rc(tid * 16 + i * 8192, R, C); const int Rb = Epi::PERM ? ((R & ~31) + perm32(R & 31)) : R;
;         voffA[i] = (unsigned)(R * K + C) * 2u; voffB[i] = (unsigned)(Rb * K + C) * 2u; }
;     const unsigned kstep = (unsigned)(BK * 2);
;     const unsigned hstep = (unsigned)HALF * (unsigned)K * 2u;
;     typedef __amdgpu_buffer_rsrc_t rsrc_t;
;     const rsrc_t rA0 = __builtin_amdgcn_make_buffer_rsrc((void*)g.A, 0, 0xffffffff, 0x00020000), rB0 = __builtin_amdgcn_make_buffer_rsrc((void*)g.Bt, 0, 0xffffffff, 0x00020000);
;     rsrc_t rA1 = rA0, rB1 = rB0;
;     if constexpr (Sched::TWO) { rA1 = __builtin_amdgcn_make_buffer_rsrc((void*)S.A1, 0, 0xffffffff, 0x00020000); rB1 = __builtin_amdgcn_make_buffer_rsrc((void*)S.Bt1, 0, 0xffffffff, 0x00020000); }
;     const unsigned ldsw = (unsigned)wid * 1024u;
;     const int aoff = lds_byte(wr * 64 + fr, fq * 8), boff = lds_byte(wc * 32 + fr, fq * 8);
;     ...
;     Unit cur, nxt; int ui = 0;
;     if (!S.next(0, cur)) return;
;     f32x4 acc[2][2][4][2];
;     ...
;     PG8_ZERO_ACC();
;     v8i_t At[4], B0[2], B1[2];
;     unsigned cA = S.a_off(cur, g), cB = S.b_off(cur, g); rsrc_t rAc = (Sched::TWO && cur.part) ? rA1 : rA0, rBc = (Sched::TWO && cur.part) ? rB1 : rB0;
;     S.a_ready(cur);
;     if constexpr (SP2) {
;         PG8_STAGE(PG8_SB(0, 0), rBc, cB, voffB); PG8_STAGE(PG8_SB(0, 1), rBc, cB + hstep, voffB); PG8_STAGE(PG8_SA(0, 0), rAc, cA, voffA); PG8_STAGE(PG8_SA(0, 1), rAc, cA + hstep, voffA);
;         if (wr == 1) PG8_BAR;
;         PG8_WAIT_V(2); PG8_BAR;
;         PG8_STAGE(PG8_SB(1, 0), rBc, cB + kstep, voffB); PG8_STAGE(PG8_SA(1, 0), rAc, cA + kstep, voffA); PG8_STAGE(PG8_SB(1, 1), rBc, cB + hstep + kstep, voffB);
;         PG8_WAIT_V(6); PG8_BAR;
;     } else {
.LBB0_1616:
	s_and_b64 vcc, exec, s[2:3]
	s_cbranch_vccz .LBB0_1923
	s_cmp_eq_u32 s95, 2
	s_mov_b64 s[2:3], -1
	s_cbranch_scc1 .LBB0_1770
	v_readlane_b32 s4, v255, 4
	s_mov_b64 s[2:3], s[88:89]
	s_mov_b32 s20, s4
	s_mov_b32 s21, s92
	s_mov_b32 s4, s38
	v_readlane_b32 s1, v255, 10
	v_mbcnt_lo_u32_b32 v0, s4, 0
	v_mbcnt_hi_u32_b32 v0, s4, v0
	s_cmp_eq_u32 s1, 0
	s_mov_b32 s1, 0x13200000
	v_add_u32_e32 v4, s93, v0
	s_cselect_b32 s1, s1, 0x1b800000
	s_movk_i32 s12, 0x400
	v_readfirstlane_b32 s14, v4
	s_cmpk_lt_i32 s21, 0xe00
	v_readlane_b32 s5, v255, 5
	s_cbranch_scc0 .LBB0_1636
	v_bfe_i32 v2, v4, 27, 1
	v_lshlrev_b32_e32 v0, 4, v4
	v_lshrrev_b32_e32 v2, 22, v2
	v_add_u32_e32 v2, v0, v2
	s_mov_b64 s[10:11], s[100:101]
	v_and_b32_e32 v2, 0xfffffc00, v2
	v_sub_u32_e32 v2, v0, v2
	v_lshrrev_b32_e32 v3, 4, v2
	v_ashrrev_i32_e32 v1, 31, v4
	v_bitop3_b32 v3, v3, v2, 32 bitop3:0x6c
	v_ashrrev_i32_e32 v2, 31, v2
	v_lshrrev_b32_e32 v1, 26, v1
	v_lshrrev_b32_e32 v2, 26, v2
	s_mul_i32 s2, s95, 0x380000
	s_mov_b32 s3, s40
	s_waitcnt lgkmcnt(0)
	s_add_u32 s36, s10, s1
	v_add_u32_e32 v1, v4, v1
	v_add_u32_e32 v2, v3, v2
	s_addc_u32 s5, s11, 0
	s_lshl_b64 s[2:3], s[2:3], 1
	v_ashrrev_i32_e32 v1, 6, v1
	v_ashrrev_i32_e32 v2, 6, v2
	s_add_u32 s2, s10, s2
	v_lshlrev_b32_e32 v5, 3, v1
	v_mul_i32_i24_e32 v6, 64, v2
	s_addc_u32 s3, s11, s3
	v_and_b32_e32 v5, -16, v5
	v_lshlrev_b32_e32 v1, 5, v1
	v_sub_u32_e32 v3, v3, v6
	s_add_u32 s4, s2, 0x4f00000
	v_add_u32_e32 v5, v2, v5
	v_and_b32_e32 v1, 32, v1
	v_ashrrev_i16_sdwa v3, v231, sext(v3) dst_sel:DWORD dst_unused:UNUSED_PAD src0_sel:DWORD src1_sel:BYTE_0
	s_addc_u32 s2, s3, 0
	v_add_u32_sdwa v1, v1, sext(v3) dst_sel:DWORD dst_unused:UNUSED_PAD src0_sel:DWORD src1_sel:WORD_0
	v_lshlrev_b32_e32 v3, 1, v5
	v_lshrrev_b32_e32 v6, 2, v5
	v_and_b32_e32 v2, 3, v2
	s_mov_b32 s3, 0x7fffffe0
	v_and_b32_e32 v3, 24, v3
	v_and_b32_e32 v6, 4, v6
	v_and_or_b32 v2, v5, s3, v2
	v_or3_b32 v2, v2, v6, v3
	v_mul_lo_u32 v3, v5, s12
	v_mul_lo_u32 v2, v2, s12
	v_add_u32_e32 v0, 0x2000, v0
	v_add_lshl_u32 v137, v1, v3, 1
	v_add_lshl_u32 v141, v2, v1, 1
	v_ashrrev_i32_e32 v1, 31, v0
	v_lshrrev_b32_e32 v1, 22, v1
	v_add_u32_e32 v1, v0, v1
	v_ashrrev_i32_e32 v1, 10, v1
	v_mul_i32_i24_e32 v2, 0x400, v1
	v_sub_u32_e32 v0, v0, v2
	v_lshrrev_b32_e32 v2, 4, v0
	v_bitop3_b32 v0, v2, v0, 32 bitop3:0x6c
	v_ashrrev_i32_e32 v3, 31, v0
	v_lshrrev_b32_e32 v3, 26, v3
	v_lshlrev_b32_e32 v2, 3, v1
	v_add_u32_e32 v3, v0, v3
	v_and_b32_e32 v2, -16, v2
	v_ashrrev_i32_e32 v5, 6, v3
	v_add_u32_e32 v2, v5, v2
	v_and_b32_e32 v5, 3, v5
	v_and_or_b32 v5, v2, s3, v5
	s_ashr_i32 s3, s21, 31
	s_lshr_b32 s3, s3, 29
	s_add_i32 s3, s21, s3
	s_ashr_i32 s15, s14, 6
	s_ashr_i32 s8, s3, 3
	s_and_b32 s3, s3, -8
	s_ashr_i32 s13, s14, 8
	s_lshl_b32 s22, s12, 8
	s_and_b32 s37, s5, 0xffff
	s_and_b32 s5, s2, 0xffff
	s_lshl_b32 s2, s15, 10
	s_sub_i32 s3, s21, s3
	s_cmp_lt_i32 s3, 0
	s_movk_i32 s9, 0x1c1
	s_cselect_b32 s9, s9, 0x1c0
	s_mul_i32 s3, s3, s9
	s_add_i32 s3, s3, s8
	s_mul_hi_i32 s8, s3, 0x92492493
	s_add_i32 s8, s8, s3
	s_lshr_b32 s9, s8, 31
	s_ashr_i32 s8, s8, 7
	s_add_i32 s8, s8, s9
	v_and_b32_e32 v3, 0xc0, v3
	s_lshl_b32 s9, s8, 3
	s_mulk_i32 s8, 0xe0
	v_lshlrev_b32_e32 v1, 5, v1
	v_sub_u32_e32 v0, v0, v3
	s_sub_i32 s3, s3, s8
	v_and_b32_e32 v1, 32, v1
	v_ashrrev_i16_sdwa v0, v231, sext(v0) dst_sel:DWORD dst_unused:UNUSED_PAD src0_sel:DWORD src1_sel:BYTE_0
	s_bfe_u32 s8, s3, 0x3001c
	v_add_u32_sdwa v0, v1, sext(v0) dst_sel:DWORD dst_unused:UNUSED_PAD src0_sel:DWORD src1_sel:WORD_0
	v_lshlrev_b32_e32 v1, 1, v2
	v_lshrrev_b32_e32 v3, 2, v2
	s_add_i32 s8, s3, s8
	v_and_b32_e32 v1, 24, v1
	v_and_b32_e32 v3, 4, v3
	s_sext_i32_i16 s16, s8
	s_add_i32 s23, s2, 0
	v_or3_b32 v1, v5, v3, v1
	s_ashr_i32 s17, s16, 3
	s_add_i32 s24, s23, 0x10000
	v_mul_lo_u32 v2, v2, s12
	v_mul_lo_u32 v1, v1, s12
	s_mov_b32 s6, s38
	s_mov_b32 s7, s39
	s_and_b32 s8, s8, 0xfff8
	s_lshl_b32 s54, s17, 19
	s_mov_b32 m0, s24
	s_add_i32 s25, s23, 0x12000
	v_add_lshl_u32 v145, v0, v2, 1
	v_add_lshl_u32 v149, v1, v0, 1
	s_sub_i32 s3, s3, s8
	v_mov_b32 v0, 0
	buffer_load_dwordx4 v141, s[4:7], s54 offen lds
	s_mov_b32 m0, s25
	s_add_i32 s26, s23, 0x14000
	s_sext_i32_i16 s3, s3
	buffer_load_dwordx4 v149, s[4:7], s54 offen lds
	s_add_i32 s16, s54, s22
	s_mov_b32 m0, s26
	s_add_i32 s27, s23, 0x16000
	s_add_i32 s58, s9, s3
	buffer_load_dwordx4 v141, s[4:7], s16 offen lds
	s_mov_b32 m0, s27
	s_lshl_b32 s55, s58, 19
	buffer_load_dwordx4 v149, s[4:7], s16 offen lds
	s_mov_b32 m0, s23
	s_add_i32 s28, s23, 0x2000
	buffer_load_dwordx4 v137, s[36:39], s55 offen lds
	s_mov_b32 m0, s28
	s_add_i32 s29, s23, 0x4000
	buffer_load_dwordx4 v145, s[36:39], s55 offen lds
	s_add_i32 s2, s55, s22
	s_mov_b32 m0, s29
	s_add_i32 s30, s23, 0x6000
	buffer_load_dwordx4 v137, s[36:39], s2 offen lds
	s_mov_b32 m0, s30
	s_cmp_eq_u32 s13, 1
	buffer_load_dwordx4 v145, s[36:39], s2 offen lds
	s_cselect_b64 s[2:3], -1, 0
	s_cmp_lg_u32 s13, 1
	s_cbranch_scc1 .LBB0_1621
	s_barrier

; __device__ __forceinline__ unsigned xb_ld(unsigned* p)              { return __hip_atomic_load(p, __ATOMIC_RELAXED, __HIP_MEMORY_SCOPE_AGENT); }
; __device__ __forceinline__ void xcd_barrier_complete(unsigned* bar, unsigned x, unsigned& nloc, unsigned& nx) {
;     const unsigned G = gridDim.x * gridDim.y * gridDim.z;
;     unsigned sum, cnt, mine, sp = 0u;
;     for (;;) {
;         sum = 0u; cnt = 0u; mine = 0u;
; #pragma unroll
;         for (unsigned j = 0; j < 16; ++j) { const unsigned c = xb_ld(&bar[XB_XCNT(j)]); sum += c; cnt += (c > 0u) ? 1u : 0u; mine = (j == x) ? c : mine; }
; __device__ __forceinline__ void xcd_barrier(const XcdBarrier& b, bool leader) {
;     asm volatile("s_waitcnt vmcnt(0)" ::: "memory");
;     __syncthreads();
;     if (leader) {
;         unsigned zo_; asm volatile("v_mov_b32 %0, 0" : "=v"(zo_)); unsigned* bar = b.bar + zo_;
;         __builtin_amdgcn_s_waitcnt(0);
;         unsigned nloc = b.st[0], nx = b.st[1];
;         if (nloc == 0u) { xcd_barrier_complete(bar, b.x, nloc, nx); b.st[0] = nloc; b.st[1] = nx; }
.Lbinv_skip_11:
	s_and_saveexec_b64 s[6:7], vcc
	s_xor_b64 s[10:11], exec, s[6:7]
	s_cbranch_execz .LBB0_1681
	s_mov_b64 s[2:3], s[100:101]
	v_mov_b32 v232, 0
	s_waitcnt vmcnt(0) expcnt(0) lgkmcnt(0)
	s_and_b32 s33, s4, 15
	v_lshl_add_u64 v[0:1], v[232:233], 2, s[2:3]
	s_mov_b64 s[2:3], 0x4000
	v_lshl_add_u64 v[0:1], v[0:1], 0, s[2:3]
	v_readlane_b32 s2, v255, 7
	s_nop 1
	v_mov_b32_e32 v2, s2
	ds_read_b32 v6, v2
	v_readlane_b32 s2, v255, 8
	s_waitcnt lgkmcnt(0)
	v_cmp_ne_u32_e32 vcc, 0, v6
	v_mov_b32_e32 v2, s2
	ds_read_b32 v4, v2
	s_cbranch_vccnz .LBB0_1651
	v_readlane_b32 s4, v255, 0
	v_readlane_b32 s5, v255, 1
	s_load_dwordx2 s[2:3], s[4:5], 0x4
	s_mov_b64 s[4:5], 0x1100
	s_waitcnt lgkmcnt(0)
	v_lshl_add_u64 v[4:5], v[0:1], 0, s[4:5]
	s_mov_b64 s[4:5], 0x1200
	v_lshl_add_u64 v[6:7], v[0:1], 0, s[4:5]
	s_mov_b64 s[4:5], 0x1300
	v_lshl_add_u64 v[8:9], v[0:1], 0, s[4:5]
	v_readlane_b32 s4, v255, 4
	s_mul_i32 s22, s2, s4
	v_lshl_add_u64 v[2:3], v[0:1], 0, s[72:73]
	v_readlane_b32 s5, v255, 5
	s_mul_i32 s22, s22, s3
	s_mov_b32 s23, 1
	s_mov_b64 s[2:3], 0
	s_branch .LBB0_1641

; __device__ __forceinline__ int opaque_s(int x) { asm volatile("" : "+s"(x)); return x; }
;     __device__ __forceinline__ bool next(int i, Unit& u) const { return so.next(i, u); }
;     __device__ __forceinline__ bool next(int i, Unit& u) const { const bool ok = so.next(i >> 1, u); u.part = i & 1; return ok; }
; #define KWS (kargs()->ws)
;     __host__ __device__ bool next(int i, Unit& u) const {
;         const int L = i * G + c; if (L >= nwg) return false;
;         int wgid = L; { const int q = nwg / NXCD, r = nwg % NXCD, xcd = wgid % NXCD, off = wgid / NXCD; wgid = (xcd < r ? xcd * (q + 1) : r * (q + 1) + (xcd - r) * q) + off; }
;         const int nig = WGM * nN, gid = wgid / nig, fm = gid * WGM, gsz = (nM - fm) < WGM ? (nM - fm) : WGM;
;         u.pm = fm + ((wgid % nig) % gsz); u.pn = (wgid % nig) / gsz; u.part = 0; return true;
; __global__ void __launch_bounds__(512, 2) mega(Ptrs Pdummy) {
;     ...
;                 { unsigned char* ws = KWS; pg8::Gemm g{(const bf16*)(ws + WS_R + R_G), (const bf16*)(ws + WS_W2D) + (size_t)(l >> 1) * DM * DFF, DFF, 0}; pg8::StaticOrder S; S.init(M, DM, opaque_s(G), opaque_s(c));
;                   pg8::EpiResid<0> E{HBUF(hc), HBUF(hc), nullptr, SBUF(sc ^ 1), nullptr, nullptr, nullptr, 1.f, 0}; pg8::gemm_phase<pg8::EpiResid<0>, pg8::StaticOrder, true, true>(lds, g, S, E, wbase); sc ^= 1; }
.LBB0_1681:
	s_or_b64 exec, exec, s[10:11]
	s_mov_b64 s[2:3], s[88:89]
	s_waitcnt lgkmcnt(0)
	s_barrier
	s_mov_b64 s[10:11], s[100:101]
	v_readlane_b32 s2, v255, 4
	s_mov_b32 s22, s2
	s_mov_b32 s23, s92
	s_mov_b32 s2, s38
	v_readlane_b32 s3, v255, 5
	v_mbcnt_lo_u32_b32 v0, s2, 0
	v_mbcnt_hi_u32_b32 v0, s2, v0
	v_add_u32_e32 v4, s93, v0
	s_cmpk_lt_i32 s23, 0x200
	s_movk_i32 s14, 0xe00
	v_readfirstlane_b32 s13, v4
	s_cselect_b64 s[2:3], -1, 0
	s_cmpk_gt_i32 s23, 0x1ff
	s_cbranch_scc1 .LBB0_1687
	s_ashr_i32 s4, s23, 31
	s_lshr_b32 s4, s4, 29
	s_add_i32 s6, s23, s4
	s_and_b32 s4, s6, -8
	s_sub_i32 s7, s23, s4
	s_cmp_gt_i32 s7, -1
	s_mov_b64 s[4:5], -1
	s_cbranch_scc0 .LBB0_1684
	s_lshl_b32 s8, s7, 6
	s_mov_b64 s[4:5], 0

; #define PG8_BAR __builtin_amdgcn_s_barrier()
; #define KWS (kargs()->ws)
; template <class Epi, class Sched, bool ALIGN_EPI = false, bool SP2 = false, bool FP8 = false>
; __device__ __forceinline__ void gemm_phase(LAS unsigned char* lds, const Gemm g, const Sched& S, const Epi& E, int wbase) {
;     const int tid = opaque_tid(wbase), wid = __builtin_amdgcn_readfirstlane(tid >> 6), lane = tid & 63, wr = wid >> 2, wc = wid & 3, fr = lane & 15, fq = lane >> 4;
;     const int K = opaque_s(g.K), nt = K / BK;
;     unsigned voffA[2], voffB[2];
; #pragma unroll
;     for (int i = 0; i < 2; ++i) { int R, C; stage_rc(tid * 16 + i * 8192, R, C); const int Rb = Epi::PERM ? ((R & ~31) + perm32(R & 31)) : R;
;         voffA[i] = (unsigned)(R * K + C) * 2u; voffB[i] = (unsigned)(Rb * K + C) * 2u; }
;     const unsigned kstep = (unsigned)(BK * 2);
;     const unsigned hstep = (unsigned)HALF * (unsigned)K * 2u;
;     typedef __amdgpu_buffer_rsrc_t rsrc_t;
;     const rsrc_t rA0 = __builtin_amdgcn_make_buffer_rsrc((void*)g.A, 0, 0xffffffff, 0x00020000), rB0 = __builtin_amdgcn_make_buffer_rsrc((void*)g.Bt, 0, 0xffffffff, 0x00020000);
;     rsrc_t rA1 = rA0, rB1 = rB0;
;     if constexpr (Sched::TWO) { rA1 = __builtin_amdgcn_make_buffer_rsrc((void*)S.A1, 0, 0xffffffff, 0x00020000); rB1 = __builtin_amdgcn_make_buffer_rsrc((void*)S.Bt1, 0, 0xffffffff, 0x00020000); }
;     const unsigned ldsw = (unsigned)wid * 1024u;
;     const int aoff = lds_byte(wr * 64 + fr, fq * 8), boff = lds_byte(wc * 32 + fr, fq * 8);
;     ...
;     Unit cur, nxt; int ui = 0;
;     if (!S.next(0, cur)) return;
;     f32x4 acc[2][2][4][2];
;     ...
;     PG8_ZERO_ACC();
;     v8i_t At[4], B0[2], B1[2];
;     unsigned cA = S.a_off(cur, g), cB = S.b_off(cur, g); rsrc_t rAc = (Sched::TWO && cur.part) ? rA1 : rA0, rBc = (Sched::TWO && cur.part) ? rB1 : rB0;
;     S.a_ready(cur);
;     if constexpr (SP2) {
;         PG8_STAGE(PG8_SB(0, 0), rBc, cB, voffB); PG8_STAGE(PG8_SB(0, 1), rBc, cB + hstep, voffB); PG8_STAGE(PG8_SA(0, 0), rAc, cA, voffA); PG8_STAGE(PG8_SA(0, 1), rAc, cA + hstep, voffA);
;         if (wr == 1) PG8_BAR;
; __global__ void __launch_bounds__(512, 2) mega(Ptrs Pdummy) {
;     ...
;                 REP(11) { unsigned char* ws = KWS; pg8::Gemm g{(const bf16*)(ws + WS_HB8), (const bf16*)(ws + WS_W13D) + (size_t)(l >> 1) * 2 * DFF * DM, DM / 2, 0}; pg8::StaticOrder S; S.init(M, 2 * DFF, opaque_s(G), opaque_s(c));
.LBB0_1770:
	s_and_b64 vcc, exec, s[2:3]
	s_cbranch_vccz .LBB0_1923
	v_readlane_b32 s4, v255, 4
	s_mov_b64 s[2:3], s[88:89]
	s_mov_b32 s1, s4
	s_mov_b32 s20, s92
	s_mov_b32 s4, s38
	s_movk_i32 s14, 0x200
	v_mbcnt_lo_u32_b32 v0, s4, 0
	v_mbcnt_hi_u32_b32 v0, s4, v0
	v_add_u32_e32 v4, s93, v0
	s_cmpk_lt_i32 s20, 0xe00
	v_readfirstlane_b32 s13, v4
	v_readlane_b32 s5, v255, 5
	s_cbranch_scc0 .LBB0_1789
	v_bfe_i32 v2, v4, 27, 1
	v_lshlrev_b32_e32 v0, 4, v4
	v_lshrrev_b32_e32 v2, 22, v2
	v_add_u32_e32 v2, v0, v2
	v_and_b32_e32 v2, 0xfffffc00, v2
	v_sub_u32_e32 v2, v0, v2
	v_lshrrev_b32_e32 v3, 4, v2
	v_ashrrev_i32_e32 v1, 31, v4
	v_bitop3_b32 v3, v3, v2, 32 bitop3:0x6c
	v_ashrrev_i32_e32 v2, 31, v2
	v_lshrrev_b32_e32 v1, 26, v1
	v_lshrrev_b32_e32 v2, 26, v2
	v_add_u32_e32 v1, v4, v1
	v_add_u32_e32 v2, v3, v2
	v_ashrrev_i32_e32 v1, 6, v1
	v_ashrrev_i32_e32 v2, 6, v2
	v_lshlrev_b32_e32 v5, 3, v1
	v_mul_i32_i24_e32 v6, 64, v2
	v_and_b32_e32 v5, -16, v5
	v_lshlrev_b32_e32 v1, 5, v1
	v_sub_u32_e32 v3, v3, v6
	v_add_u32_e32 v5, v2, v5
	v_and_b32_e32 v1, 32, v1
	v_ashrrev_i16_sdwa v3, v231, sext(v3) dst_sel:DWORD dst_unused:UNUSED_PAD src0_sel:DWORD src1_sel:BYTE_0
	v_add_u32_sdwa v1, v1, sext(v3) dst_sel:DWORD dst_unused:UNUSED_PAD src0_sel:DWORD src1_sel:WORD_0
	v_lshlrev_b32_e32 v3, 1, v5
	v_lshrrev_b32_e32 v6, 2, v5
	v_and_b32_e32 v2, 3, v2
	s_mov_b32 s5, 0x7fffffe0
	v_and_b32_e32 v3, 24, v3
	v_and_b32_e32 v6, 4, v6
	v_and_or_b32 v2, v5, s5, v2
	v_or3_b32 v2, v2, v6, v3
	v_mul_lo_u32 v3, v5, s14
	v_mul_lo_u32 v2, v2, s14
	v_add_u32_e32 v0, 0x2000, v0
	v_add_lshl_u32 v148, v1, v3, 1
	v_add_lshl_u32 v149, v2, v1, 1
	v_ashrrev_i32_e32 v1, 31, v0
	v_lshrrev_b32_e32 v1, 22, v1
	v_add_u32_e32 v1, v0, v1
	v_ashrrev_i32_e32 v1, 10, v1
	s_mov_b64 s[10:11], s[100:101]
	v_mul_i32_i24_e32 v2, 0x400, v1
	v_sub_u32_e32 v0, v0, v2
	v_lshrrev_b32_e32 v2, 4, v0
	v_bitop3_b32 v0, v2, v0, 32 bitop3:0x6c
	v_ashrrev_i32_e32 v3, 31, v0
	s_waitcnt lgkmcnt(0)
	s_add_u32 s36, s10, 0xb200000
	v_lshrrev_b32_e32 v3, 26, v3
	s_addc_u32 s2, s11, 0
	v_lshlrev_b32_e32 v2, 3, v1
	v_add_u32_e32 v3, v0, v3
	s_add_u32 s4, s10, 0x5d00000
	v_and_b32_e32 v2, -16, v2
	v_ashrrev_i32_e32 v5, 6, v3
	s_addc_u32 s3, s11, 0
	v_add_u32_e32 v2, v5, v2
	v_and_b32_e32 v5, 3, v5
	v_and_or_b32 v5, v2, s5, v5
	s_and_b32 s5, s3, 0xffff
	s_ashr_i32 s3, s20, 31
	s_lshr_b32 s3, s3, 29
	s_add_i32 s3, s20, s3
	s_ashr_i32 s15, s13, 6
	s_ashr_i32 s8, s3, 3
	s_and_b32 s3, s3, -8
	s_ashr_i32 s12, s13, 8
	s_lshl_b32 s21, s14, 8
	s_and_b32 s37, s2, 0xffff
	s_lshl_b32 s2, s15, 10
	s_sub_i32 s3, s20, s3
	s_cmp_lt_i32 s3, 0
	s_movk_i32 s9, 0x1c1
	s_cselect_b32 s9, s9, 0x1c0
	s_mul_i32 s3, s3, s9
	s_add_i32 s3, s3, s8
	s_mul_hi_i32 s8, s3, 0x92492493
	s_add_i32 s8, s8, s3
	s_lshr_b32 s9, s8, 31
	s_ashr_i32 s8, s8, 7
	s_add_i32 s8, s8, s9
	v_and_b32_e32 v3, 0xc0, v3
	s_lshl_b32 s9, s8, 3
	s_mulk_i32 s8, 0xe0
	v_lshlrev_b32_e32 v1, 5, v1
	v_sub_u32_e32 v0, v0, v3
	s_sub_i32 s3, s3, s8
	v_and_b32_e32 v1, 32, v1
	v_ashrrev_i16_sdwa v0, v231, sext(v0) dst_sel:DWORD dst_unused:UNUSED_PAD src0_sel:DWORD src1_sel:BYTE_0
	s_bfe_u32 s8, s3, 0x3001c
	v_add_u32_sdwa v0, v1, sext(v0) dst_sel:DWORD dst_unused:UNUSED_PAD src0_sel:DWORD src1_sel:WORD_0
	v_lshlrev_b32_e32 v1, 1, v2
	v_lshrrev_b32_e32 v3, 2, v2
	s_add_i32 s8, s3, s8
	v_and_b32_e32 v1, 24, v1
	v_and_b32_e32 v3, 4, v3
	s_sext_i32_i16 s16, s8
	s_add_i32 s22, s2, 0
	v_or3_b32 v1, v5, v3, v1
	s_ashr_i32 s57, s16, 3
	s_add_i32 s23, s22, 0x10000
	v_mul_lo_u32 v2, v2, s14
	v_mul_lo_u32 v1, v1, s14
	s_mov_b32 s6, s38
	s_mov_b32 s7, s39
	s_and_b32 s8, s8, 0xfff8
	s_lshl_b32 s54, s57, 18
	s_mov_b32 m0, s23
	s_add_i32 s24, s22, 0x12000
	v_add_lshl_u32 v150, v0, v2, 1
	v_add_lshl_u32 v151, v1, v0, 1
	s_sub_i32 s3, s3, s8
	v_mov_b32 v0, 0
	buffer_load_dwordx4 v149, s[4:7], s54 offen lds
	s_mov_b32 m0, s24
	s_add_i32 s25, s22, 0x14000
	s_sext_i32_i16 s3, s3
	buffer_load_dwordx4 v151, s[4:7], s54 offen lds
	s_add_i32 s16, s54, s21
	s_mov_b32 m0, s25
	s_add_i32 s26, s22, 0x16000
	s_add_i32 s58, s9, s3
	buffer_load_dwordx4 v149, s[4:7], s16 offen lds
	s_mov_b32 m0, s26
	s_lshl_b32 s55, s58, 18
	buffer_load_dwordx4 v151, s[4:7], s16 offen lds
	s_mov_b32 m0, s22
	s_add_i32 s27, s22, 0x2000
	buffer_load_dwordx4 v148, s[36:39], s55 offen lds
	s_mov_b32 m0, s27
	s_add_i32 s28, s22, 0x4000
	buffer_load_dwordx4 v150, s[36:39], s55 offen lds
	s_add_i32 s2, s55, s21
	s_mov_b32 m0, s28
	s_add_i32 s29, s22, 0x6000
	buffer_load_dwordx4 v148, s[36:39], s2 offen lds
	s_mov_b32 m0, s29
	s_cmp_eq_u32 s12, 1
	buffer_load_dwordx4 v150, s[36:39], s2 offen lds
	s_cselect_b64 s[2:3], -1, 0
	s_cmp_lg_u32 s12, 1
	s_cbranch_scc1 .LBB0_1774
	s_barrier

; __device__ __forceinline__ int opaque_s(int x) { asm volatile("" : "+s"(x)); return x; }
;     __device__ __forceinline__ bool next(int i, Unit& u) const { return so.next(i, u); }
;     __device__ __forceinline__ bool next(int i, Unit& u) const { const bool ok = so.next(i >> 1, u); u.part = i & 1; return ok; }
; #define KWS (kargs()->ws)
;     __host__ __device__ bool next(int i, Unit& u) const {
;         const int L = i * G + c; if (L >= nwg) return false;
;         int wgid = L; { const int q = nwg / NXCD, r = nwg % NXCD, xcd = wgid % NXCD, off = wgid / NXCD; wgid = (xcd < r ? xcd * (q + 1) : r * (q + 1) + (xcd - r) * q) + off; }
;         const int nig = WGM * nN, gid = wgid / nig, fm = gid * WGM, gsz = (nM - fm) < WGM ? (nM - fm) : WGM;
;         u.pm = fm + ((wgid % nig) % gsz); u.pn = (wgid % nig) / gsz; u.part = 0; return true;
; __global__ void __launch_bounds__(512, 2) mega(Ptrs Pdummy) {
;     ...
;                 { unsigned char* ws = KWS; pg8::Gemm g{(const bf16*)(ws + WS_R + R_G), (const bf16*)(ws + WS_W2D) + (size_t)(l >> 1) * DM * DFF, DFF / 2, 0}; pg8::StaticOrder S; S.init(M, DM, opaque_s(G), opaque_s(c));
;                   pg8::EpiResid<0> E{HBUF(hc), HBUF(hc), nullptr, SBUF(sc ^ 1), nullptr, nullptr, nullptr, 1.f / (W2_SCALE * G8_SCALE), 0}; pg8::gemm_phase<pg8::EpiResid<0>, pg8::StaticOrder, true, true, true>(lds, g, S, E, wbase); sc ^= 1; }
.LBB0_1834:
	s_or_b64 exec, exec, s[10:11]
	s_mov_b64 s[2:3], s[88:89]
	s_waitcnt lgkmcnt(0)
	s_barrier
	s_mov_b64 s[10:11], s[100:101]
	v_readlane_b32 s2, v255, 4
	s_mov_b32 s1, s2
	s_mov_b32 s22, s92
	s_mov_b32 s2, s38
	v_readlane_b32 s3, v255, 5
	v_mbcnt_lo_u32_b32 v0, s2, 0
	v_mbcnt_hi_u32_b32 v0, s2, v0
	v_add_u32_e32 v4, s93, v0
	s_cmpk_lt_i32 s22, 0x200
	s_movk_i32 s14, 0x700
	v_readfirstlane_b32 s13, v4
	s_cselect_b64 s[2:3], -1, 0
	s_cmpk_gt_i32 s22, 0x1ff
	s_cbranch_scc1 .LBB0_1840
	s_ashr_i32 s4, s22, 31
	s_lshr_b32 s4, s4, 29
	s_add_i32 s6, s22, s4
	s_and_b32 s4, s6, -8
	s_sub_i32 s7, s22, s4
	s_cmp_gt_i32 s7, -1
	s_mov_b64 s[4:5], -1
	s_cbranch_scc0 .LBB0_1837
	s_lshl_b32 s8, s7, 6
	s_mov_b64 s[4:5], 0

; __device__ __forceinline__ int opaque_tid(int wbase) { int t = wbase + lane_id(); asm volatile("" : "+v"(t)); return t; }
; template <class Epi, class Sched, bool ALIGN_EPI = false, bool SP2 = false, bool FP8 = false>
; __device__ __forceinline__ void gemm_phase(LAS unsigned char* lds, const Gemm g, const Sched& S, const Epi& E, int wbase) {
;     const int tid = opaque_tid(wbase), wid = __builtin_amdgcn_readfirstlane(tid >> 6), lane = tid & 63, wr = wid >> 2, wc = wid & 3, fr = lane & 15, fq = lane >> 4;
;     const int K = opaque_s(g.K), nt = K / BK;
;     unsigned voffA[2], voffB[2];
; #pragma unroll
;     for (int i = 0; i < 2; ++i) { int R, C; stage_rc(tid * 16 + i * 8192, R, C); const int Rb = Epi::PERM ? ((R & ~31) + perm32(R & 31)) : R;
;         voffA[i] = (unsigned)(R * K + C) * 2u; voffB[i] = (unsigned)(Rb * K + C) * 2u; }
;     const unsigned kstep = (unsigned)(BK * 2);
;     const unsigned hstep = (unsigned)HALF * (unsigned)K * 2u;
;     typedef __amdgpu_buffer_rsrc_t rsrc_t;
;     const rsrc_t rA0 = __builtin_amdgcn_make_buffer_rsrc((void*)g.A, 0, 0xffffffff, 0x00020000), rB0 = __builtin_amdgcn_make_buffer_rsrc((void*)g.Bt, 0, 0xffffffff, 0x00020000);
;     rsrc_t rA1 = rA0, rB1 = rB0;
;     if constexpr (Sched::TWO) { rA1 = __builtin_amdgcn_make_buffer_rsrc((void*)S.A1, 0, 0xffffffff, 0x00020000); rB1 = __builtin_amdgcn_make_buffer_rsrc((void*)S.Bt1, 0, 0xffffffff, 0x00020000); }
;     const unsigned ldsw = (unsigned)wid * 1024u;
;     const int aoff = lds_byte(wr * 64 + fr, fq * 8), boff = lds_byte(wc * 32 + fr, fq * 8);
;     ...
;     Unit cur, nxt; int ui = 0;
;     if (!S.next(0, cur)) return;
;     f32x4 acc[2][2][4][2];
;     ...
;     PG8_ZERO_ACC();
;     v8i_t At[4], B0[2], B1[2];
;     unsigned cA = S.a_off(cur, g), cB = S.b_off(cur, g); rsrc_t rAc = (Sched::TWO && cur.part) ? rA1 : rA0, rBc = (Sched::TWO && cur.part) ? rB1 : rB0;
;     S.a_ready(cur);
;     if constexpr (SP2) {
;         PG8_STAGE(PG8_SB(0, 0), rBc, cB, voffB); PG8_STAGE(PG8_SB(0, 1), rBc, cB + hstep, voffB); PG8_STAGE(PG8_SA(0, 0), rAc, cA, voffA); PG8_STAGE(PG8_SA(0, 1), rAc, cA + hstep, voffA);
;         if (wr == 1) PG8_BAR;
; __global__ void __launch_bounds__(512, 2) mega(Ptrs Pdummy) {
;     ...
;         { unsigned char* ws = KWS; pg8::Gemm g{HBUF(hc), (const bf16*)(ws + WS_WPG) + (size_t)l * DM * DM, DM, 0}; pg8::StaticOrder S; S.init(M, DM, opaque_s(G), opaque_s(c));
.LBB0_1930:
	s_mov_b64 s[18:19], s[100:101]
	s_andn2_b64 vcc, exec, s[4:5]
	s_cbranch_vccnz .LBB0_1968
	v_bfe_i32 v2, v4, 27, 1
	v_lshlrev_b32_e32 v0, 4, v4
	v_lshrrev_b32_e32 v2, 22, v2
	v_add_u32_e32 v2, v0, v2
	v_and_b32_e32 v2, 0xfffffc00, v2
	v_sub_u32_e32 v2, v0, v2
	v_readlane_b32 s2, v255, 10
	v_lshrrev_b32_e32 v3, 4, v2
	s_cmp_eq_u32 s2, 0
	s_mov_b32 s2, 0x13200000
	v_ashrrev_i32_e32 v1, 31, v4
	v_bitop3_b32 v3, v3, v2, 32 bitop3:0x6c
	v_ashrrev_i32_e32 v2, 31, v2
	s_cselect_b32 s2, s2, 0x1b800000
	v_lshrrev_b32_e32 v1, 26, v1
	v_lshrrev_b32_e32 v2, 26, v2
	s_waitcnt lgkmcnt(0)
	s_add_u32 s36, s18, s2
	v_readlane_b32 s2, v255, 40
	v_add_u32_e32 v1, v4, v1
	v_add_u32_e32 v2, v3, v2
	s_addc_u32 s3, s19, 0
	s_lshl_b32 s2, s2, 1
	v_ashrrev_i32_e32 v1, 6, v1
	v_ashrrev_i32_e32 v2, 6, v2
	s_add_u32 s2, s18, s2
	v_lshlrev_b32_e32 v5, 3, v1
	v_mul_i32_i24_e32 v6, 64, v2
	s_addc_u32 s5, s19, 0
	v_and_b32_e32 v5, -16, v5
	v_lshlrev_b32_e32 v1, 5, v1
	v_sub_u32_e32 v3, v3, v6
	s_add_u32 s4, s2, 0x4500000
	v_add_u32_e32 v5, v2, v5
	v_and_b32_e32 v1, 32, v1
	v_ashrrev_i16_sdwa v3, v231, sext(v3) dst_sel:DWORD dst_unused:UNUSED_PAD src0_sel:DWORD src1_sel:BYTE_0
	s_addc_u32 s2, s5, 0
	v_add_u32_sdwa v1, v1, sext(v3) dst_sel:DWORD dst_unused:UNUSED_PAD src0_sel:DWORD src1_sel:WORD_0
	v_lshlrev_b32_e32 v3, 1, v5
	v_lshrrev_b32_e32 v6, 2, v5
	v_and_b32_e32 v2, 3, v2
	s_mov_b32 s5, 0x7fffffe0
	v_and_b32_e32 v3, 24, v3
	v_and_b32_e32 v6, 4, v6
	v_and_or_b32 v2, v5, s5, v2
	v_or3_b32 v2, v2, v6, v3
	v_mul_lo_u32 v3, v5, s22
	v_mul_lo_u32 v2, v2, s22
	v_add_u32_e32 v0, 0x2000, v0
	v_add_lshl_u32 v168, v1, v3, 1
	v_add_lshl_u32 v169, v2, v1, 1
	v_ashrrev_i32_e32 v1, 31, v0
	v_lshrrev_b32_e32 v1, 22, v1
	v_add_u32_e32 v1, v0, v1
	v_ashrrev_i32_e32 v1, 10, v1
	v_mul_i32_i24_e32 v2, 0x400, v1
	v_sub_u32_e32 v0, v0, v2
	v_lshrrev_b32_e32 v2, 4, v0
	v_bitop3_b32 v0, v2, v0, 32 bitop3:0x6c
	v_ashrrev_i32_e32 v3, 31, v0
	v_lshrrev_b32_e32 v3, 26, v3
	v_add_u32_e32 v3, v0, v3
	v_lshlrev_b32_e32 v2, 3, v1
	v_ashrrev_i32_e32 v5, 6, v3
	v_and_b32_e32 v3, 0xc0, v3
	v_and_b32_e32 v2, -16, v2
	v_lshlrev_b32_e32 v1, 5, v1
	v_sub_u32_e32 v0, v0, v3
	s_ashr_i32 s20, s21, 6
	v_add_u32_e32 v2, v5, v2
	v_and_b32_e32 v1, 32, v1
	v_ashrrev_i16_sdwa v0, v231, sext(v0) dst_sel:DWORD dst_unused:UNUSED_PAD src0_sel:DWORD src1_sel:BYTE_0
	v_and_b32_e32 v5, 3, v5
	v_add_u32_sdwa v0, v1, sext(v0) dst_sel:DWORD dst_unused:UNUSED_PAD src0_sel:DWORD src1_sel:WORD_0
	v_lshlrev_b32_e32 v1, 1, v2
	v_lshrrev_b32_e32 v3, 2, v2
	v_and_or_b32 v5, v2, s5, v5
	s_and_b32 s5, s2, 0xffff
	s_lshl_b32 s2, s20, 10
	v_and_b32_e32 v1, 24, v1
	v_and_b32_e32 v3, 4, v3
	s_add_i32 s34, s2, 0
	v_or3_b32 v1, v5, v3, v1
	s_add_i32 s35, s34, 0x10000
	v_mul_lo_u32 v2, v2, s22
	v_mul_lo_u32 v1, v1, s22
	s_mov_b32 s6, s38
	s_mov_b32 s7, s39
	s_lshl_b32 s54, s31, 19
	s_mov_b32 m0, s35
	s_add_i32 s41, s34, 0x12000
	v_add_lshl_u32 v170, v0, v2, 1
	v_add_lshl_u32 v171, v1, v0, 1
	s_lshl_b32 s33, s22, 8
	v_mov_b32 v0, 0
	buffer_load_dwordx4 v169, s[4:7], s54 offen lds
	s_mov_b32 m0, s41
	s_add_i32 s42, s34, 0x14000
	buffer_load_dwordx4 v171, s[4:7], s54 offen lds
	s_add_i32 s24, s54, s33
	s_mov_b32 m0, s42
	s_add_i32 s43, s34, 0x16000
	buffer_load_dwordx4 v169, s[4:7], s24 offen lds
	s_mov_b32 m0, s43
	s_and_b32 s37, s3, 0xffff
	buffer_load_dwordx4 v171, s[4:7], s24 offen lds
	s_lshl_b32 s55, s28, 19
	s_mov_b32 m0, s34
	s_add_i32 s44, s34, 0x2000
	buffer_load_dwordx4 v168, s[36:39], s55 offen lds
	s_mov_b32 m0, s44
	s_add_i32 s45, s34, 0x4000
	buffer_load_dwordx4 v170, s[36:39], s55 offen lds
	s_add_i32 s2, s55, s33
	s_mov_b32 m0, s45
	s_add_i32 s46, s34, 0x6000
	buffer_load_dwordx4 v168, s[36:39], s2 offen lds
	s_mov_b32 m0, s46
	s_ashr_i32 s23, s21, 8
	buffer_load_dwordx4 v170, s[36:39], s2 offen lds
	s_cmp_eq_u32 s23, 1
	s_cselect_b64 s[8:9], -1, 0
	s_cmp_lg_u32 s23, 1
	s_mov_b32 s2, s36
	s_cbranch_scc1 .LBB0_1933
	s_barrier

; __device__ __forceinline__ int opaque_s(int x) { asm volatile("" : "+s"(x)); return x; }
; template <class Epi, class Sched, bool ALIGN_EPI = false, bool SP2 = false, bool FP8 = false>
; __device__ __forceinline__ void gemm_phase(LAS unsigned char* lds, const Gemm g, const Sched& S, const Epi& E, int wbase) {
;     const int tid = opaque_tid(wbase), wid = __builtin_amdgcn_readfirstlane(tid >> 6), lane = tid & 63, wr = wid >> 2, wc = wid & 3, fr = lane & 15, fq = lane >> 4;
;     const int K = opaque_s(g.K), nt = K / BK;
;     unsigned voffA[2], voffB[2];
; #pragma unroll
;     for (int i = 0; i < 2; ++i) { int R, C; stage_rc(tid * 16 + i * 8192, R, C); const int Rb = Epi::PERM ? ((R & ~31) + perm32(R & 31)) : R;
;         voffA[i] = (unsigned)(R * K + C) * 2u; voffB[i] = (unsigned)(Rb * K + C) * 2u; }
;     const unsigned kstep = (unsigned)(BK * 2);
;     const unsigned hstep = (unsigned)HALF * (unsigned)K * 2u;
;     typedef __amdgpu_buffer_rsrc_t rsrc_t;
;     const rsrc_t rA0 = __builtin_amdgcn_make_buffer_rsrc((void*)g.A, 0, 0xffffffff, 0x00020000), rB0 = __builtin_amdgcn_make_buffer_rsrc((void*)g.Bt, 0, 0xffffffff, 0x00020000);
;     rsrc_t rA1 = rA0, rB1 = rB0;
;     if constexpr (Sched::TWO) { rA1 = __builtin_amdgcn_make_buffer_rsrc((void*)S.A1, 0, 0xffffffff, 0x00020000); rB1 = __builtin_amdgcn_make_buffer_rsrc((void*)S.Bt1, 0, 0xffffffff, 0x00020000); }
;     const unsigned ldsw = (unsigned)wid * 1024u;
;     const int aoff = lds_byte(wr * 64 + fr, fq * 8), boff = lds_byte(wc * 32 + fr, fq * 8);
;     ...
;     Unit cur, nxt; int ui = 0;
;     if (!S.next(0, cur)) return;
;     f32x4 acc[2][2][4][2];
;     ...
;     PG8_ZERO_ACC();
;     v8i_t At[4], B0[2], B1[2];
;     unsigned cA = S.a_off(cur, g), cB = S.b_off(cur, g); rsrc_t rAc = (Sched::TWO && cur.part) ? rA1 : rA0, rBc = (Sched::TWO && cur.part) ? rB1 : rB0;
;     S.a_ready(cur);
;     if constexpr (SP2) {
;         PG8_STAGE(PG8_SB(0, 0), rBc, cB, voffB); PG8_STAGE(PG8_SB(0, 1), rBc, cB + hstep, voffB); PG8_STAGE(PG8_SA(0, 0), rAc, cA, voffA); PG8_STAGE(PG8_SA(0, 1), rAc, cA + hstep, voffA);
;         if (wr == 1) PG8_BAR;
; __global__ void __launch_bounds__(512, 2) mega(Ptrs Pdummy) {
;     ...
;           unsigned char* ws = KWS; pg8::Gemm g{(const bf16*)(ws + WS_HB8), (const bf16*)(ws + WS_WPG) + (size_t)l * DM * DM, DM / 2, 0}; pg8::StaticOrder S; S.init(M, DM, opaque_s(G), opaque_s(c));
.LBB0_1976:
	s_mov_b64 s[2:3], s[100:101]
	s_nop 0
	s_load_dwordx2 s[6:7], s[4:5], 0xf0
	s_andn2_b64 vcc, exec, s[8:9]
	s_cbranch_vccnz .LBB0_2079
	v_bfe_i32 v2, v4, 27, 1
	v_lshlrev_b32_e32 v0, 4, v4
	v_lshrrev_b32_e32 v2, 22, v2
	v_add_u32_e32 v2, v0, v2
	v_and_b32_e32 v2, 0xfffffc00, v2
	v_sub_u32_e32 v2, v0, v2
	v_lshrrev_b32_e32 v3, 4, v2
	v_ashrrev_i32_e32 v1, 31, v4
	v_bitop3_b32 v3, v3, v2, 32 bitop3:0x6c
	v_ashrrev_i32_e32 v2, 31, v2
	v_lshrrev_b32_e32 v1, 26, v1
	v_lshrrev_b32_e32 v2, 26, v2
	v_add_u32_e32 v1, v4, v1
	v_add_u32_e32 v2, v3, v2
	v_ashrrev_i32_e32 v1, 6, v1
	v_ashrrev_i32_e32 v2, 6, v2
	v_lshlrev_b32_e32 v5, 3, v1
	v_mul_i32_i24_e32 v6, 64, v2
	v_and_b32_e32 v5, -16, v5
	v_lshlrev_b32_e32 v1, 5, v1
	v_sub_u32_e32 v3, v3, v6
	v_add_u32_e32 v5, v2, v5
	v_and_b32_e32 v1, 32, v1
	v_ashrrev_i16_sdwa v3, v231, sext(v3) dst_sel:DWORD dst_unused:UNUSED_PAD src0_sel:DWORD src1_sel:BYTE_0
	v_add_u32_sdwa v1, v1, sext(v3) dst_sel:DWORD dst_unused:UNUSED_PAD src0_sel:DWORD src1_sel:WORD_0
	v_lshlrev_b32_e32 v3, 1, v5
	v_lshrrev_b32_e32 v6, 2, v5
	v_and_b32_e32 v2, 3, v2
	s_mov_b32 s9, 0x7fffffe0
	v_and_b32_e32 v3, 24, v3
	v_and_b32_e32 v6, 4, v6
	v_and_or_b32 v2, v5, s9, v2
	v_or3_b32 v2, v2, v6, v3
	v_mul_lo_u32 v3, v5, s26
	v_mul_lo_u32 v2, v2, s26
	v_add_u32_e32 v0, 0x2000, v0
	v_add_lshl_u32 v174, v1, v3, 1
	v_add_lshl_u32 v175, v2, v1, 1
	v_ashrrev_i32_e32 v1, 31, v0
	v_lshrrev_b32_e32 v1, 22, v1
	v_add_u32_e32 v1, v0, v1
	v_ashrrev_i32_e32 v1, 10, v1
	v_mul_i32_i24_e32 v2, 0x400, v1
	v_sub_u32_e32 v0, v0, v2
	v_lshrrev_b32_e32 v2, 4, v0
	v_bitop3_b32 v0, v2, v0, 32 bitop3:0x6c
	v_ashrrev_i32_e32 v3, 31, v0
	v_lshrrev_b32_e32 v3, 26, v3
	s_waitcnt lgkmcnt(0)
	s_add_u32 s36, s2, 0xb200000
	v_add_u32_e32 v3, v0, v3
	s_addc_u32 s4, s3, 0
	v_lshlrev_b32_e32 v2, 3, v1
	v_ashrrev_i32_e32 v5, 6, v3
	v_and_b32_e32 v3, 0xc0, v3
	s_add_u32 s12, s2, 0x4b00000
	v_and_b32_e32 v2, -16, v2
	v_lshlrev_b32_e32 v1, 5, v1
	v_sub_u32_e32 v0, v0, v3
	s_addc_u32 s5, s3, 0
	s_ashr_i32 s8, s25, 6
	v_add_u32_e32 v2, v5, v2
	v_and_b32_e32 v1, 32, v1
	v_ashrrev_i16_sdwa v0, v231, sext(v0) dst_sel:DWORD dst_unused:UNUSED_PAD src0_sel:DWORD src1_sel:BYTE_0
	v_add_u32_sdwa v0, v1, sext(v0) dst_sel:DWORD dst_unused:UNUSED_PAD src0_sel:DWORD src1_sel:WORD_0
	v_lshlrev_b32_e32 v1, 1, v2
	v_lshrrev_b32_e32 v3, 2, v2
	v_and_b32_e32 v5, 3, v5
	s_and_b32 s37, s4, 0xffff
	s_lshl_b32 s4, s8, 10
	v_and_b32_e32 v1, 24, v1
	v_and_b32_e32 v3, 4, v3
	v_and_or_b32 v5, v2, s9, v5
	s_add_i32 s43, s4, 0
	v_or3_b32 v1, v5, v3, v1
	s_add_i32 s44, s43, 0x10000
	v_mul_lo_u32 v2, v2, s26
	v_mul_lo_u32 v1, v1, s26
	s_and_b32 s13, s5, 0xffff
	s_mov_b32 s14, s38
	s_mov_b32 s15, s39
	s_lshl_b32 s5, s41, 18
	s_mov_b32 m0, s44
	s_add_i32 s45, s43, 0x12000
	v_add_lshl_u32 v176, v0, v2, 1
	v_add_lshl_u32 v177, v1, v0, 1
	s_lshl_b32 s42, s26, 8
	v_mov_b32 v0, 0
	buffer_load_dwordx4 v175, s[12:15], s5 offen lds
	s_mov_b32 m0, s45
	s_add_i32 s46, s43, 0x14000
	buffer_load_dwordx4 v177, s[12:15], s5 offen lds
	s_add_i32 s24, s5, s42
	s_mov_b32 m0, s46
	s_add_i32 s47, s43, 0x16000
	buffer_load_dwordx4 v175, s[12:15], s24 offen lds
	s_mov_b32 m0, s47
	s_lshl_b32 s4, s60, 18
	buffer_load_dwordx4 v177, s[12:15], s24 offen lds
	s_mov_b32 m0, s43
	s_add_i32 s48, s43, 0x2000
	buffer_load_dwordx4 v174, s[36:39], s4 offen lds
	s_mov_b32 m0, s48
	s_add_i32 s52, s43, 0x4000
	buffer_load_dwordx4 v176, s[36:39], s4 offen lds
	s_add_i32 s9, s4, s42
	s_mov_b32 m0, s52
	s_add_i32 s53, s43, 0x6000
	buffer_load_dwordx4 v174, s[36:39], s9 offen lds
	s_mov_b32 m0, s53
	s_mov_b32 s66, s94
	buffer_load_dwordx4 v176, s[36:39], s9 offen lds
	s_ashr_i32 s9, s25, 8
	s_cmp_eq_u32 s9, 1
	s_cselect_b64 s[80:81], -1, 0
	s_cmp_lg_u32 s9, 1
	s_cbranch_scc1 .LBB0_1979
	s_barrier

; __device__ __forceinline__ unsigned xb_ld(unsigned* p)              { return __hip_atomic_load(p, __ATOMIC_RELAXED, __HIP_MEMORY_SCOPE_AGENT); }
; __device__ __forceinline__ void xcd_barrier_complete(unsigned* bar, unsigned x, unsigned& nloc, unsigned& nx) {
;     const unsigned G = gridDim.x * gridDim.y * gridDim.z;
;     unsigned sum, cnt, mine, sp = 0u;
;     for (;;) {
;         sum = 0u; cnt = 0u; mine = 0u;
; #pragma unroll
;         for (unsigned j = 0; j < 16; ++j) { const unsigned c = xb_ld(&bar[XB_XCNT(j)]); sum += c; cnt += (c > 0u) ? 1u : 0u; mine = (j == x) ? c : mine; }
; __device__ __forceinline__ void xcd_barrier(const XcdBarrier& b, bool leader) {
;     asm volatile("s_waitcnt vmcnt(0)" ::: "memory");
;     __syncthreads();
;     if (leader) {
;         unsigned zo_; asm volatile("v_mov_b32 %0, 0" : "=v"(zo_)); unsigned* bar = b.bar + zo_;
;         __builtin_amdgcn_s_waitcnt(0);
;         unsigned nloc = b.st[0], nx = b.st[1];
;         if (nloc == 0u) { xcd_barrier_complete(bar, b.x, nloc, nx); b.st[0] = nloc; b.st[1] = nx; }
.LBB0_2081:
	s_mov_b64 s[2:3], s[100:101]
	v_mov_b32 v232, 0
	s_waitcnt vmcnt(0) expcnt(0) lgkmcnt(0)
	s_and_b32 s1, s1, 15
	v_lshl_add_u64 v[0:1], v[232:233], 2, s[2:3]
	s_mov_b64 s[2:3], 0x4000
	v_lshl_add_u64 v[0:1], v[0:1], 0, s[2:3]
	v_readlane_b32 s2, v255, 7
	s_nop 1
	v_mov_b32_e32 v2, s2
	ds_read_b32 v6, v2
	v_readlane_b32 s2, v255, 8
	s_waitcnt lgkmcnt(0)
	v_cmp_ne_u32_e32 vcc, 0, v6
	v_mov_b32_e32 v2, s2
	ds_read_b32 v4, v2
	s_cbranch_vccnz .LBB0_2095
	v_readlane_b32 s4, v255, 0
	v_readlane_b32 s5, v255, 1
	s_load_dwordx2 s[2:3], s[4:5], 0x4
	s_mov_b64 s[4:5], 0x1100
	s_waitcnt lgkmcnt(0)
	v_lshl_add_u64 v[4:5], v[0:1], 0, s[4:5]
	s_mov_b64 s[4:5], 0x1200
	v_lshl_add_u64 v[6:7], v[0:1], 0, s[4:5]
	s_mov_b64 s[4:5], 0x1300
	v_lshl_add_u64 v[8:9], v[0:1], 0, s[4:5]
	v_readlane_b32 s4, v255, 4
	s_mul_i32 s22, s2, s4
	v_lshl_add_u64 v[2:3], v[0:1], 0, s[72:73]
	v_readlane_b32 s5, v255, 5
	s_mul_i32 s22, s22, s3
	s_mov_b32 s23, 1
	s_mov_b64 s[2:3], 0
	s_branch .LBB0_2085

; __device__ __forceinline__ unsigned xb_ld(unsigned* p)              { return __hip_atomic_load(p, __ATOMIC_RELAXED, __HIP_MEMORY_SCOPE_AGENT); }
; #define KWS (kargs()->ws)
; #define KOUT (kargs()->out)
; #define WAVE_IDS() const int tid = opaque_tid(wbase), lane = tid & 63, wid = __builtin_amdgcn_readfirstlane(tid >> 6), gw = c * 8 + wid, ngw = G * 8; (void)tid; (void)lane; (void)gw; (void)ngw
; __global__ void __launch_bounds__(512, 2) mega(Ptrs Pdummy) {
;     ...
;     { WAVE_IDS(); if (xb_ld((unsigned*)(KWS + WS_CTL) + CW_BAR + XB_TMO) != 0u) { const float q = __builtin_nanf(""); float* out = KOUT;
;         for (int m = gw; m < M; m += ngw) { f32x4* o = (f32x4*)(out + (size_t)m * DM) + lane;
; #pragma unroll
;             for (int j = 0; j < 4; ++j) o[64 * j] = (f32x4){q, q, q, q}; } } }
.LBB0_2123:
	s_mov_b32 s0, -1
	v_mov_b32_e32 v1, 0x4000
	v_mbcnt_lo_u32_b32 v0, s0, 0
	v_mbcnt_hi_u32_b32 v0, s0, v0
	v_add_u32_e32 v0, s93, v0
	s_mov_b64 s[0:1], s[88:89]
	s_mov_b64 s[0:1], s[100:101]
	s_waitcnt lgkmcnt(0)
	global_load_dword v1, v1, s[0:1] offset:512 sc1
	v_readfirstlane_b32 s0, v0
	s_waitcnt vmcnt(0)
	v_cmp_ne_u32_e32 vcc, 0, v1
	s_cbranch_vccz .LBB0_2127
	s_ashr_i32 s0, s0, 6
	v_readlane_b32 s1, v255, 27
	s_add_i32 s2, s0, s1
	s_cmpk_gt_i32 s2, 0x7fff
	s_cbranch_scc1 .LBB0_2127
	s_load_dwordx2 s[0:1], s[88:89], 0xf0
	s_ashr_i32 s3, s2, 31
	s_lshl_b64 s[4:5], s[2:3], 12
	v_and_b32_e32 v0, 63, v0
	v_lshlrev_b32_e32 v0, 4, v0
	s_waitcnt lgkmcnt(0)
	s_add_u32 s0, s0, s4
	s_mov_b32 s4, 0x7fc00000
	v_mov_b32_e32 v1, 0
	s_addc_u32 s1, s1, s5
	s_mov_b32 s5, s4
	v_lshl_add_u64 v[0:1], s[0:1], 0, v[0:1]
	s_mov_b64 s[0:1], 0x800
	s_ashr_i32 s95, s94, 31
	s_mov_b32 s6, s4
	s_mov_b32 s7, s4
	v_mov_b64_e32 v[2:3], s[4:5]
	v_lshl_add_u64 v[0:1], v[0:1], 0, s[0:1]
	s_lshl_b64 s[0:1], s[94:95], 12
	v_mov_b64_e32 v[4:5], s[6:7]
